# P9/P10: expert row steps stored as (us, vs) pairs, one dwordx2 gather per index register instead of two dword gathers
# baseline (speedup 1.0000x reference)
; __device__ __forceinline__ float bf2f(bf16_t v) { return __uint_as_float(((unsigned)v) << 16); }
; #define LAS __attribute__((address_space(3)))
; __device__ __forceinline__ void route_half(float (&top)[16], LAS const unsigned char* keys_lds, const bf16_t* __restrict__ qrow, int r32, int hi) {
;     bf16x8 qf[8]; float ss = 0.f;
; #pragma unroll
;     for (int ks = 0; ks < 8; ++ks) { qf[ks] = __builtin_nontemporal_load((const bf16x8*)(qrow + 16 * ks + 8 * hi));
; #pragma unroll
;         for (int j = 0; j < 8; ++j) { const float f = bf2f((bf16_t)qf[ks][j]); ss += f * f; } }
;     ss += __shfl_xor(ss, 32);
;     const float rn = rsqrtf(ss * (1.f / 128.f) + EPS);
;     f32x16 acc[4];
; #pragma unroll
;     for (int kt = 0; kt < 4; ++kt) {
; #pragma unroll
;         for (int r = 0; r < 16; ++r) acc[kt][r] = 0.f;
; #pragma unroll
;         for (int ks = 0; ks < 8; ++ks) { const bf16x8 kf = *(LAS const bf16x8*)(keys_lds + (32 * kt + r32) * RT_KROW + (16 * ks + 8 * hi) * 2);
;             acc[kt] = __builtin_amdgcn_mfma_f32_32x32x16_bf16(kf, qf[ks], acc[kt], 0, 0, 0); }
.LBB0_910:
	v_ashrrev_i32_e32 v139, 31, v138
	v_lshlrev_b64 v[2:3], 12, v[138:139]
	v_lshl_add_u64 v[140:141], v[136:137], 0, v[2:3]
	global_load_dwordx4 v[18:21], v[140:141], off nt
	global_load_dwordx4 v[98:101], v[140:141], off offset:32 nt
	global_load_dwordx4 v[102:105], v[140:141], off offset:64 nt
	global_load_dwordx4 v[106:109], v[140:141], off offset:96 nt
	global_load_dwordx4 v[110:113], v[140:141], off offset:128 nt
	global_load_dwordx4 v[114:117], v[140:141], off offset:160 nt
	global_load_dwordx4 v[118:121], v[140:141], off offset:192 nt
	global_load_dwordx4 v[122:125], v[140:141], off offset:224 nt
	ds_read_b128 v[2:5], v143
	ds_read_b128 v[22:25], v143 offset:32
	ds_read_b128 v[26:29], v143 offset:64
	ds_read_b128 v[30:33], v143 offset:96
	ds_read_b128 v[34:37], v143 offset:128
	s_waitcnt vmcnt(7) lgkmcnt(4)
	v_mfma_f32_32x32x16_bf16 v[2:17], v[2:5], v[18:21], 0
	v_and_b32_e32 v46, 0xffff0000, v18
	v_lshlrev_b32_e32 v44, 16, v18
	v_mul_f32_e32 v46, v46, v46
	v_lshlrev_b32_e32 v47, 16, v19
	v_fmac_f32_e32 v46, v44, v44
	v_and_b32_e32 v48, 0xffff0000, v19
	v_fmac_f32_e32 v46, v47, v47
	v_lshlrev_b32_e32 v49, 16, v20
	v_fmac_f32_e32 v46, v48, v48
	v_and_b32_e32 v50, 0xffff0000, v20
	v_fmac_f32_e32 v46, v49, v49
	v_lshlrev_b32_e32 v51, 16, v21
	v_fmac_f32_e32 v46, v50, v50
	v_and_b32_e32 v52, 0xffff0000, v21
	v_fmac_f32_e32 v46, v51, v51
	s_waitcnt vmcnt(6)
	v_lshlrev_b32_e32 v53, 16, v98
	v_fmac_f32_e32 v46, v52, v52
	v_and_b32_e32 v54, 0xffff0000, v98
	v_fmac_f32_e32 v46, v53, v53
	v_lshlrev_b32_e32 v55, 16, v99
	v_fmac_f32_e32 v46, v54, v54
	v_and_b32_e32 v56, 0xffff0000, v99
	v_fmac_f32_e32 v46, v55, v55
	v_lshlrev_b32_e32 v57, 16, v100
	v_fmac_f32_e32 v46, v56, v56
	v_and_b32_e32 v58, 0xffff0000, v100
	v_fmac_f32_e32 v46, v57, v57
	v_lshlrev_b32_e32 v59, 16, v101
	v_fmac_f32_e32 v46, v58, v58
	v_and_b32_e32 v60, 0xffff0000, v101
	v_fmac_f32_e32 v46, v59, v59
	s_waitcnt vmcnt(5)
	v_lshlrev_b32_e32 v61, 16, v102
	v_fmac_f32_e32 v46, v60, v60
	v_and_b32_e32 v62, 0xffff0000, v102
	v_fmac_f32_e32 v46, v61, v61
	v_lshlrev_b32_e32 v63, 16, v103
	v_fmac_f32_e32 v46, v62, v62
	v_and_b32_e32 v64, 0xffff0000, v103
	v_fmac_f32_e32 v46, v63, v63
	v_lshlrev_b32_e32 v65, 16, v104
	v_fmac_f32_e32 v46, v64, v64
	v_and_b32_e32 v149, 0xffff0000, v104
	v_fmac_f32_e32 v46, v65, v65
	v_lshlrev_b32_e32 v150, 16, v105
	v_fmac_f32_e32 v46, v149, v149
	v_and_b32_e32 v151, 0xffff0000, v105
	v_fmac_f32_e32 v46, v150, v150
	s_waitcnt vmcnt(4)
	v_lshlrev_b32_e32 v152, 16, v106
	v_fmac_f32_e32 v46, v151, v151
	v_and_b32_e32 v153, 0xffff0000, v106
	v_fmac_f32_e32 v46, v152, v152
	v_lshlrev_b32_e32 v154, 16, v107
	v_fmac_f32_e32 v46, v153, v153
	v_and_b32_e32 v155, 0xffff0000, v107
	v_fmac_f32_e32 v46, v154, v154
	v_lshlrev_b32_e32 v156, 16, v108
	v_fmac_f32_e32 v46, v155, v155
	v_and_b32_e32 v157, 0xffff0000, v108
	v_fmac_f32_e32 v46, v156, v156
	v_lshlrev_b32_e32 v158, 16, v109
	v_fmac_f32_e32 v46, v157, v157
	v_and_b32_e32 v159, 0xffff0000, v109
	v_fmac_f32_e32 v46, v158, v158
	s_waitcnt vmcnt(3)
	v_lshlrev_b32_e32 v160, 16, v110
	v_fmac_f32_e32 v46, v159, v159
	v_and_b32_e32 v161, 0xffff0000, v110
	v_fmac_f32_e32 v46, v160, v160
	v_lshlrev_b32_e32 v162, 16, v111
	v_fmac_f32_e32 v46, v161, v161
	v_and_b32_e32 v163, 0xffff0000, v111
	v_fmac_f32_e32 v46, v162, v162
	v_lshlrev_b32_e32 v164, 16, v112
	v_fmac_f32_e32 v46, v163, v163
	v_and_b32_e32 v165, 0xffff0000, v112
	v_fmac_f32_e32 v46, v164, v164
	v_lshlrev_b32_e32 v166, 16, v113
	v_fmac_f32_e32 v46, v165, v165
	v_and_b32_e32 v167, 0xffff0000, v113
	v_fmac_f32_e32 v46, v166, v166
	s_waitcnt vmcnt(2)
	v_lshlrev_b32_e32 v168, 16, v114
	s_waitcnt lgkmcnt(3)
	v_mfma_f32_32x32x16_bf16 v[2:17], v[22:25], v[98:101], v[2:17]
	v_fmac_f32_e32 v46, v167, v167
	v_and_b32_e32 v169, 0xffff0000, v114
	v_fmac_f32_e32 v46, v168, v168
	v_lshlrev_b32_e32 v170, 16, v115
	v_fmac_f32_e32 v46, v169, v169
	v_and_b32_e32 v171, 0xffff0000, v115
	v_fmac_f32_e32 v46, v170, v170
	v_lshlrev_b32_e32 v172, 16, v116
	v_fmac_f32_e32 v46, v171, v171
	v_and_b32_e32 v173, 0xffff0000, v116
	v_fmac_f32_e32 v46, v172, v172
	v_lshlrev_b32_e32 v174, 16, v117
	v_fmac_f32_e32 v46, v173, v173
	v_and_b32_e32 v175, 0xffff0000, v117
	v_fmac_f32_e32 v46, v174, v174
	s_waitcnt vmcnt(1)
	v_lshlrev_b32_e32 v176, 16, v118
	s_waitcnt lgkmcnt(2)
	v_mfma_f32_32x32x16_bf16 v[2:17], v[26:29], v[102:105], v[2:17]
	v_fmac_f32_e32 v46, v175, v175
	v_and_b32_e32 v177, 0xffff0000, v118
	v_fmac_f32_e32 v46, v176, v176
	v_lshlrev_b32_e32 v178, 16, v119
	v_fmac_f32_e32 v46, v177, v177
	v_and_b32_e32 v179, 0xffff0000, v119
	v_fmac_f32_e32 v46, v178, v178
	v_lshlrev_b32_e32 v180, 16, v120
	v_fmac_f32_e32 v46, v179, v179
	v_and_b32_e32 v181, 0xffff0000, v120
	v_and_b32_e32 v39, 0xffff0000, v121
	v_lshlrev_b32_e32 v38, 16, v121
	v_fmac_f32_e32 v46, v180, v180
	v_pk_mul_f32 v[38:39], v[38:39], v[38:39]
	v_fmac_f32_e32 v46, v181, v181
	s_waitcnt vmcnt(0)
	v_and_b32_e32 v41, 0xffff0000, v122
	v_lshlrev_b32_e32 v40, 16, v122
	v_add_f32_e32 v22, v38, v46
	v_pk_mul_f32 v[40:41], v[40:41], v[40:41]
	s_waitcnt lgkmcnt(1)
	v_mfma_f32_32x32x16_bf16 v[2:17], v[30:33], v[106:109], v[2:17]
	v_add_f32_e32 v22, v39, v22
	v_and_b32_e32 v43, 0xffff0000, v123
	v_lshlrev_b32_e32 v42, 16, v123
	v_add_f32_e32 v22, v40, v22
	v_mul_f32_e64 v42, v42, v42
	v_mul_f32_e64 v43, v43, v43
	v_add_f32_e32 v22, v41, v22
	v_and_b32_e32 v45, 0xffff0000, v124
	v_add_f32_e32 v22, v42, v22
	v_lshlrev_b32_e32 v44, 16, v124
	v_add_f32_e32 v22, v43, v22
	v_pk_mul_f32 v[26:27], v[44:45], v[44:45]
	s_waitcnt lgkmcnt(0)
; #define LAS __attribute__((address_space(3)))
; __device__ __forceinline__ void route_half(float (&top)[16], LAS const unsigned char* keys_lds, const bf16_t* __restrict__ qrow, int r32, int hi) {
;     ...
;     ss += __shfl_xor(ss, 32);
;     const float rn = rsqrtf(ss * (1.f / 128.f) + EPS);
;     f32x16 acc[4];
; #pragma unroll
;     for (int kt = 0; kt < 4; ++kt) {
; #pragma unroll
;         for (int r = 0; r < 16; ++r) acc[kt][r] = 0.f;
; #pragma unroll
;         for (int ks = 0; ks < 8; ++ks) { const bf16x8 kf = *(LAS const bf16x8*)(keys_lds + (32 * kt + r32) * RT_KROW + (16 * ks + 8 * hi) * 2);
;             acc[kt] = __builtin_amdgcn_mfma_f32_32x32x16_bf16(kf, qf[ks], acc[kt], 0, 0, 0); }
;         __builtin_amdgcn_sched_barrier(0);
;     }
;     const unsigned hi4 = (unsigned)hi << 2;
;     float g[4][16];
; #pragma unroll
;     for (int kt = 0; kt < 4; ++kt)
; #pragma unroll
;         for (int r = 0; r < 16; ++r) { const unsigned base = (unsigned)(32 * kt + (r & 3) + 8 * (r >> 2)); g[kt][r] = __uint_as_float((__float_as_uint(acc[kt][r] * rn) & 0xFFFFFF80u) | base); }
	v_mfma_f32_32x32x16_bf16 v[2:17], v[34:37], v[110:113], v[2:17]
	v_add_f32_e32 v26, v26, v22
	v_add_f32_e32 v28, v27, v26
	v_and_b32_e32 v27, 0xffff0000, v125
	v_lshlrev_b32_e32 v26, 16, v125
	ds_read_b128 v[22:25], v143 offset:160
	v_pk_mul_f32 v[26:27], v[26:27], v[26:27]
	s_nop 0
	v_add_f32_e32 v26, v26, v28
	v_add_f32_e32 v26, v27, v26
	ds_bpermute_b32 v27, v142, v26
	s_waitcnt lgkmcnt(0)
	v_add_f32_e32 v26, v26, v27
	v_fmamk_f32 v30, v26, 0x3c000000, v146
	ds_read_b128 v[26:29], v143 offset:224
	v_mfma_f32_32x32x16_bf16 v[2:17], v[22:25], v[114:117], v[2:17]
	ds_read_b128 v[22:25], v143 offset:192
	v_mul_f32_e32 v31, 0x4b800000, v30
	v_cmp_gt_f32_e32 vcc, s40, v30
	s_waitcnt lgkmcnt(0)
	v_mfma_f32_32x32x16_bf16 v[2:17], v[22:25], v[118:121], v[2:17]
	v_cndmask_b32_e32 v22, v30, v31, vcc
	v_rsq_f32_e32 v149, v22
	s_nop 0
	v_mul_f32_e32 v154, 0x45800000, v149
	v_mfma_f32_32x32x16_bf16 v[2:17], v[26:29], v[122:125], v[2:17]
	ds_read_b128 v[22:25], v143 offset:8704
	ds_read_b128 v[26:29], v143 offset:8736
	s_waitcnt lgkmcnt(1)
	v_mfma_f32_32x32x16_bf16 v[50:65], v[22:25], v[18:21], 0
	s_waitcnt lgkmcnt(0)
	v_mfma_f32_32x32x16_bf16 v[50:65], v[26:29], v[98:101], v[50:65]
	ds_read_b128 v[22:25], v143 offset:8768
	ds_read_b128 v[26:29], v143 offset:8800
	s_waitcnt lgkmcnt(1)
	v_mfma_f32_32x32x16_bf16 v[50:65], v[22:25], v[102:105], v[50:65]
	s_waitcnt lgkmcnt(0)
	v_mfma_f32_32x32x16_bf16 v[50:65], v[26:29], v[106:109], v[50:65]
	ds_read_b128 v[22:25], v143 offset:8832
	ds_read_b128 v[26:29], v143 offset:8864
	s_waitcnt lgkmcnt(1)
	v_mfma_f32_32x32x16_bf16 v[50:65], v[22:25], v[110:113], v[50:65]
	s_waitcnt lgkmcnt(0)
	v_mfma_f32_32x32x16_bf16 v[50:65], v[26:29], v[114:117], v[50:65]
	ds_read_b128 v[22:25], v143 offset:8896
	ds_read_b128 v[26:29], v143 offset:8928
	s_waitcnt lgkmcnt(1)
	v_mfma_f32_32x32x16_bf16 v[50:65], v[22:25], v[118:121], v[50:65]
	s_waitcnt lgkmcnt(0)
	v_mfma_f32_32x32x16_bf16 v[50:65], v[26:29], v[122:125], v[50:65]
	ds_read_b128 v[22:25], v143 offset:17408
	ds_read_b128 v[26:29], v143 offset:17440
	s_waitcnt lgkmcnt(1)
	v_mfma_f32_32x32x16_bf16 v[34:49], v[22:25], v[18:21], 0
	s_waitcnt lgkmcnt(0)
	v_mfma_f32_32x32x16_bf16 v[34:49], v[26:29], v[98:101], v[34:49]
	ds_read_b128 v[22:25], v143 offset:17472
	ds_read_b128 v[26:29], v143 offset:17504
	s_waitcnt lgkmcnt(1)
	v_mfma_f32_32x32x16_bf16 v[34:49], v[22:25], v[102:105], v[34:49]
	s_waitcnt lgkmcnt(0)
	v_mfma_f32_32x32x16_bf16 v[34:49], v[26:29], v[106:109], v[34:49]
	ds_read_b128 v[22:25], v143 offset:17536
	ds_read_b128 v[26:29], v143 offset:17568
	s_waitcnt lgkmcnt(1)
	v_mfma_f32_32x32x16_bf16 v[34:49], v[22:25], v[110:113], v[34:49]
	s_waitcnt lgkmcnt(0)
	v_mfma_f32_32x32x16_bf16 v[34:49], v[26:29], v[114:117], v[34:49]
	ds_read_b128 v[22:25], v143 offset:17600
	ds_read_b128 v[26:29], v143 offset:17632
	s_waitcnt lgkmcnt(1)
	v_mfma_f32_32x32x16_bf16 v[34:49], v[22:25], v[118:121], v[34:49]
	s_waitcnt lgkmcnt(0)
	v_mfma_f32_32x32x16_bf16 v[34:49], v[26:29], v[122:125], v[34:49]
	ds_read_b128 v[22:25], v143 offset:26112
	ds_read_b128 v[150:153], v143 offset:26144
	s_waitcnt lgkmcnt(1)
	v_mfma_f32_32x32x16_bf16 v[18:33], v[22:25], v[18:21], 0
	s_waitcnt lgkmcnt(0)
	v_mfma_f32_32x32x16_bf16 v[18:33], v[150:153], v[98:101], v[18:33]
	ds_read_b128 v[98:101], v143 offset:26176
	ds_read_b128 v[150:153], v143 offset:26208
	s_waitcnt lgkmcnt(1)
	v_mfma_f32_32x32x16_bf16 v[18:33], v[98:101], v[102:105], v[18:33]
	ds_read_b128 v[98:101], v143 offset:26240
	ds_read_b128 v[102:105], v143 offset:26272
	s_waitcnt lgkmcnt(2)
	v_mfma_f32_32x32x16_bf16 v[18:33], v[150:153], v[106:109], v[18:33]
	s_waitcnt lgkmcnt(1)
	v_mfma_f32_32x32x16_bf16 v[18:33], v[98:101], v[110:113], v[18:33]
	s_waitcnt lgkmcnt(0)
	v_mfma_f32_32x32x16_bf16 v[18:33], v[102:105], v[114:117], v[18:33]
	ds_read_b128 v[98:101], v143 offset:26304
	ds_read_b128 v[102:105], v143 offset:26336
	s_waitcnt lgkmcnt(1)
	v_mfma_f32_32x32x16_bf16 v[18:33], v[98:101], v[118:121], v[18:33]
	s_waitcnt lgkmcnt(0)
	v_mfma_f32_32x32x16_bf16 v[18:33], v[102:105], v[122:125], v[18:33]
	v_cndmask_b32_e32 v98, v149, v154, vcc
	v_mul_f32_e32 v2, v2, v98
	v_and_b32_e32 v99, 0xffffff80, v2
	v_mul_f32_e32 v2, v3, v98
	v_and_or_b32 v100, v2, s41, 1
	v_mul_f32_e32 v2, v4, v98
	v_and_or_b32 v101, v2, s41, 2
	v_mul_f32_e32 v2, v5, v98
	v_and_or_b32 v102, v2, s41, 3
	v_mul_f32_e32 v2, v6, v98
	v_and_or_b32 v103, v2, s41, 8
	v_mul_f32_e32 v2, v7, v98
	v_and_or_b32 v104, v2, s41, 9
	v_mul_f32_e32 v2, v8, v98
	v_and_or_b32 v105, v2, s41, 10
	v_mul_f32_e32 v2, v9, v98
	v_and_or_b32 v106, v2, s41, 11
	v_mul_f32_e32 v2, v10, v98
	v_and_or_b32 v107, v2, s41, 16
	v_mul_f32_e32 v2, v11, v98
	v_and_or_b32 v108, v2, s41, 17
	v_mul_f32_e32 v2, v12, v98
	v_and_or_b32 v109, v2, s41, 18
	v_mul_f32_e32 v2, v13, v98
	v_and_or_b32 v110, v2, s41, 19
	v_mul_f32_e32 v2, v14, v98
	v_and_or_b32 v111, v2, s41, 24
	v_mul_f32_e32 v2, v15, v98
	v_and_or_b32 v112, v2, s41, 25
	v_mul_f32_e32 v2, v16, v98
	v_and_or_b32 v113, v2, s41, 26
	v_mul_f32_e32 v2, v17, v98
	v_and_or_b32 v114, v2, s41, 27
	v_mul_f32_e32 v2, v50, v98
	v_and_or_b32 v50, v2, s41, 32
	v_mul_f32_e32 v2, v51, v98
	v_and_or_b32 v51, v2, s41, 33
	v_mul_f32_e32 v2, v52, v98
	v_and_or_b32 v52, v2, s41, 34
	v_mul_f32_e32 v2, v53, v98
	v_and_or_b32 v53, v2, s41, 35
	v_mul_f32_e32 v2, v54, v98
	v_and_or_b32 v54, v2, s41, 40
	v_mul_f32_e32 v2, v55, v98
	v_and_or_b32 v55, v2, s41, 41
	v_mul_f32_e32 v2, v56, v98
	v_and_or_b32 v56, v2, s41, 42
	v_mul_f32_e32 v2, v57, v98
	v_and_or_b32 v57, v2, s41, 43
	v_mul_f32_e32 v2, v58, v98
	v_and_or_b32 v58, v2, s41, 48
	v_mul_f32_e32 v2, v59, v98
	v_and_or_b32 v59, v2, s41, 49
; __device__ __forceinline__ void route_half(float (&top)[16], LAS const unsigned char* keys_lds, const bf16_t* __restrict__ qrow, int r32, int hi) {
;     ...
;         for (int r = 0; r < 16; ++r) { const unsigned base = (unsigned)(32 * kt + (r & 3) + 8 * (r >> 2)); g[kt][r] = __uint_as_float((__float_as_uint(acc[kt][r] * rn) & 0xFFFFFF80u) | base); }
; #pragma unroll
;     for (int kt = 0; kt < 4; ++kt) sort16_desc(g[kt]);
	v_mul_f32_e32 v2, v60, v98
	v_and_or_b32 v60, v2, s41, 50
	v_mul_f32_e32 v2, v61, v98
	v_and_or_b32 v61, v2, s41, 51
	v_mul_f32_e32 v2, v62, v98
	v_and_or_b32 v62, v2, s41, 56
	v_mul_f32_e32 v2, v63, v98
	v_and_or_b32 v63, v2, s41, 57
	v_mul_f32_e32 v2, v64, v98
	v_and_or_b32 v64, v2, s41, 58
	v_mul_f32_e32 v2, v65, v98
	v_and_or_b32 v65, v2, s41, 59
	v_mul_f32_e32 v2, v34, v98
	v_and_or_b32 v115, v2, s41, 64
	v_mul_f32_e32 v2, v35, v98
	v_and_b32_e32 v2, 0xffffff80, v2
	v_or_b32_e32 v116, 0x41, v2
	v_mul_f32_e32 v2, v36, v98
	v_and_b32_e32 v2, 0xffffff80, v2
	v_or_b32_e32 v117, 0x42, v2
	v_mul_f32_e32 v2, v37, v98
	v_and_b32_e32 v2, 0xffffff80, v2
	v_or_b32_e32 v118, 0x43, v2
	v_mul_f32_e32 v2, v38, v98
	v_and_b32_e32 v2, 0xffffff80, v2
	v_or_b32_e32 v119, 0x48, v2
	v_mul_f32_e32 v2, v39, v98
	v_and_b32_e32 v2, 0xffffff80, v2
	v_or_b32_e32 v120, 0x49, v2
	v_mul_f32_e32 v2, v40, v98
	v_and_b32_e32 v2, 0xffffff80, v2
	v_or_b32_e32 v121, 0x4a, v2
	v_mul_f32_e32 v2, v41, v98
	v_and_b32_e32 v2, 0xffffff80, v2
	v_or_b32_e32 v122, 0x4b, v2
	v_mul_f32_e32 v2, v42, v98
	v_and_b32_e32 v2, 0xffffff80, v2
	v_or_b32_e32 v42, 0x50, v2
	v_mul_f32_e32 v2, v43, v98
	v_and_b32_e32 v2, 0xffffff80, v2
	v_or_b32_e32 v43, 0x51, v2
	v_mul_f32_e32 v2, v44, v98
	v_and_b32_e32 v2, 0xffffff80, v2
	v_or_b32_e32 v44, 0x52, v2
	v_mul_f32_e32 v2, v45, v98
	v_and_b32_e32 v2, 0xffffff80, v2
	v_or_b32_e32 v45, 0x53, v2
	v_mul_f32_e32 v2, v46, v98
	v_and_b32_e32 v2, 0xffffff80, v2
	v_or_b32_e32 v46, 0x58, v2
	v_mul_f32_e32 v2, v47, v98
	v_and_b32_e32 v2, 0xffffff80, v2
	v_or_b32_e32 v47, 0x59, v2
	v_mul_f32_e32 v2, v48, v98
	v_and_b32_e32 v2, 0xffffff80, v2
	v_or_b32_e32 v48, 0x5a, v2
	v_mul_f32_e32 v2, v49, v98
	v_and_b32_e32 v2, 0xffffff80, v2
	v_mul_f32_e32 v3, v98, v19
	v_or_b32_e32 v49, 0x5b, v2
	v_mul_f32_e32 v2, v98, v18
	v_and_b32_e32 v3, 0xffffff80, v3
	v_mul_f32_e32 v5, v98, v21
	v_max_f32_e32 v18, v100, v100
	v_max_f32_e32 v19, v99, v99
	v_or_b32_e32 v4, 0x61, v3
	v_mul_f32_e32 v3, v98, v20
	v_and_b32_e32 v5, 0xffffff80, v5
	v_mul_f32_e32 v7, v98, v23
	v_max_f32_e32 v20, v19, v18
	v_min_f32_e32 v18, v19, v18
	v_max_f32_e32 v19, v101, v101
	v_max_f32_e32 v21, v102, v102
	v_or_b32_e32 v6, 0x63, v5
	v_mul_f32_e32 v5, v98, v22
	v_and_b32_e32 v7, 0xffffff80, v7
	v_mul_f32_e32 v9, v98, v25
	v_max_f32_e32 v22, v21, v19
	v_min_f32_e32 v19, v21, v19
	v_max_f32_e32 v21, v104, v104
	v_max_f32_e32 v23, v103, v103
	v_or_b32_e32 v8, 0x69, v7
	v_mul_f32_e32 v7, v98, v24
	v_and_b32_e32 v9, 0xffffff80, v9
	v_mul_f32_e32 v11, v98, v27
	v_max_f32_e32 v24, v23, v21
	v_min_f32_e32 v21, v23, v21
	v_max_f32_e32 v23, v105, v105
	v_max_f32_e32 v25, v106, v106
	v_and_b32_e32 v2, 0xffffff80, v2
	v_or_b32_e32 v10, 0x6b, v9
	v_mul_f32_e32 v9, v98, v26
	v_and_b32_e32 v11, 0xffffff80, v11
	v_mul_f32_e32 v13, v98, v29
	v_max_f32_e32 v26, v25, v23
	v_min_f32_e32 v23, v25, v23
	v_max_f32_e32 v25, v108, v108
	v_max_f32_e32 v27, v107, v107
	v_or_b32_e32 v2, 0x60, v2
	v_and_b32_e32 v3, 0xffffff80, v3
	v_or_b32_e32 v12, 0x71, v11
	v_mul_f32_e32 v11, v98, v28
	v_and_b32_e32 v13, 0xffffff80, v13
	v_mul_f32_e32 v15, v98, v31
	v_max_f32_e32 v28, v27, v25
	v_min_f32_e32 v25, v27, v25
	v_max_f32_e32 v27, v109, v109
	v_max_f32_e32 v29, v110, v110
	v_or_b32_e32 v3, 0x62, v3
	v_and_b32_e32 v5, 0xffffff80, v5
	v_or_b32_e32 v14, 0x73, v13
	v_mul_f32_e32 v13, v98, v30
	v_and_b32_e32 v15, 0xffffff80, v15
	v_max_f32_e32 v30, v29, v27
	v_min_f32_e32 v27, v29, v27
	v_max_f32_e32 v29, v112, v112
	v_max_f32_e32 v31, v111, v111
	v_max_f32_e32 v51, v51, v51
	v_max_f32_e32 v50, v50, v50
	v_max_f32_e32 v4, v4, v4
	v_max_f32_e32 v2, v2, v2
	v_or_b32_e32 v5, 0x68, v5
	v_and_b32_e32 v7, 0xffffff80, v7
	v_or_b32_e32 v16, 0x79, v15
	v_mul_f32_e32 v15, v98, v32
	v_mul_f32_e32 v17, v98, v33
	v_max_f32_e32 v32, v31, v29
	v_min_f32_e32 v29, v31, v29
	v_max_f32_e32 v31, v113, v113
	v_max_f32_e32 v98, v50, v51
	v_min_f32_e32 v50, v50, v51
	v_max_f32_e32 v51, v52, v52
	v_max_f32_e32 v52, v53, v53
	v_max_f32_e32 v106, v115, v115
	v_max_f32_e32 v107, v116, v116
	v_max_f32_e32 v113, v122, v122
	v_max_f32_e32 v122, v2, v4
	v_min_f32_e32 v2, v2, v4
	v_max_f32_e32 v3, v3, v3
	v_max_f32_e32 v4, v6, v6
	v_or_b32_e32 v7, 0x6a, v7
	v_and_b32_e32 v9, 0xffffff80, v9
	v_max_f32_e32 v53, v52, v51
	v_min_f32_e32 v51, v52, v51
	v_max_f32_e32 v52, v55, v55
	v_max_f32_e32 v54, v54, v54
	v_max_f32_e32 v108, v106, v107
	v_min_f32_e32 v106, v106, v107
	v_max_f32_e32 v107, v117, v117
	v_max_f32_e32 v109, v118, v118
	v_max_f32_e32 v6, v4, v3
	v_min_f32_e32 v3, v4, v3
	v_max_f32_e32 v4, v8, v8
	v_max_f32_e32 v5, v5, v5
	v_or_b32_e32 v9, 0x70, v9
	v_and_b32_e32 v11, 0xffffff80, v11
	v_max_f32_e32 v55, v54, v52
	v_min_f32_e32 v52, v54, v52
	v_max_f32_e32 v54, v56, v56
	v_max_f32_e32 v56, v57, v57
	v_max_f32_e32 v110, v109, v107
	v_min_f32_e32 v107, v109, v107
	v_max_f32_e32 v109, v120, v120
	v_max_f32_e32 v111, v119, v119
	v_max_f32_e32 v8, v5, v4
	v_min_f32_e32 v4, v5, v4
	v_max_f32_e32 v5, v7, v7
	v_max_f32_e32 v7, v10, v10
	v_or_b32_e32 v11, 0x72, v11
	v_and_b32_e32 v13, 0xffffff80, v13
	v_max_f32_e32 v57, v56, v54
	v_min_f32_e32 v54, v56, v54
	v_max_f32_e32 v56, v59, v59
	v_max_f32_e32 v58, v58, v58
	v_max_f32_e32 v112, v111, v109
	v_min_f32_e32 v109, v111, v109
	v_max_f32_e32 v111, v121, v121
	v_max_f32_e32 v43, v43, v43
	v_max_f32_e32 v42, v42, v42
	v_max_f32_e32 v10, v7, v5
	v_min_f32_e32 v5, v7, v5
	v_max_f32_e32 v7, v12, v12
	v_max_f32_e32 v9, v9, v9
	v_or_b32_e32 v13, 0x78, v13
	v_and_b32_e32 v15, 0xffffff80, v15
	v_and_b32_e32 v17, 0xffffff80, v17
	v_max_f32_e32 v33, v114, v114
	v_max_f32_e32 v59, v58, v56
	v_min_f32_e32 v56, v58, v56
; #define CE_DESC(a, b) do { const float _t = fmaxf(a, b); b = fminf(a, b); a = _t; } while (0)
; __device__ __forceinline__ void sort16_desc(float (&v)[16]) {
; #pragma unroll
;     for (int k = 2; k <= 16; k <<= 1)
; #pragma unroll
;         for (int j = k >> 1; j > 0; j >>= 1)
; #pragma unroll
;             for (int i = 0; i < 16; ++i) { const int l = i ^ j; if (l > i) { if ((i & k) == 0 || k == 16) CE_DESC(v[i], v[l]); else CE_DESC(v[l], v[i]); } }
; }
; __device__ __forceinline__ void route_half(float (&top)[16], LAS const unsigned char* keys_lds, const bf16_t* __restrict__ qrow, int r32, int hi) {
;     ...
;     for (int kt = 0; kt < 4; ++kt) sort16_desc(g[kt]);
	v_max_f32_e32 v58, v60, v60
	v_max_f32_e32 v60, v61, v61
	v_max_f32_e32 v114, v113, v111
	v_min_f32_e32 v111, v113, v111
	v_max_f32_e32 v113, v42, v43
	v_min_f32_e32 v42, v42, v43
	v_max_f32_e32 v43, v44, v44
	v_max_f32_e32 v44, v45, v45
	v_max_f32_e32 v12, v9, v7
	v_min_f32_e32 v7, v9, v7
	v_max_f32_e32 v9, v11, v11
	v_max_f32_e32 v11, v14, v14
	v_or_b32_e32 v15, 0x7a, v15
	v_or_b32_e32 v17, 0x7b, v17
	v_max_f32_e32 v61, v60, v58
	v_min_f32_e32 v58, v60, v58
	v_max_f32_e32 v60, v63, v63
	v_max_f32_e32 v62, v62, v62
	v_max_f32_e32 v45, v44, v43
	v_min_f32_e32 v43, v44, v43
	v_max_f32_e32 v44, v47, v47
	v_max_f32_e32 v46, v46, v46
	v_max_f32_e32 v14, v11, v9
	v_min_f32_e32 v9, v11, v9
	v_max_f32_e32 v11, v16, v16
	v_max_f32_e32 v13, v13, v13
	v_max_f32_e32 v63, v62, v60
	v_min_f32_e32 v60, v62, v60
	v_max_f32_e32 v62, v64, v64
	v_max_f32_e32 v64, v65, v65
	v_max_f32_e32 v47, v46, v44
	v_min_f32_e32 v44, v46, v44
	v_max_f32_e32 v46, v48, v48
	v_max_f32_e32 v48, v49, v49
	v_max_f32_e32 v16, v13, v11
	v_min_f32_e32 v11, v13, v11
	v_max_f32_e32 v13, v15, v15
	v_max_f32_e32 v15, v17, v17
	v_max_f32_e32 v34, v33, v31
	v_min_f32_e32 v31, v33, v31
	v_max_f32_e32 v65, v64, v62
	v_min_f32_e32 v62, v64, v62
	v_max_f32_e32 v49, v48, v46
	v_min_f32_e32 v46, v48, v46
	v_max_f32_e32 v17, v15, v13
	v_min_f32_e32 v13, v15, v13
	v_max_f32_e32 v33, v20, v19
	v_min_f32_e32 v19, v20, v19
	v_max_f32_e32 v20, v18, v22
	v_min_f32_e32 v18, v18, v22
	v_max_f32_e32 v22, v23, v24
	v_min_f32_e32 v23, v23, v24
	v_max_f32_e32 v24, v26, v21
	v_min_f32_e32 v21, v26, v21
	v_max_f32_e32 v26, v28, v27
	v_min_f32_e32 v27, v28, v27
	v_max_f32_e32 v28, v25, v30
	v_min_f32_e32 v25, v25, v30
	v_max_f32_e32 v30, v31, v32
	v_min_f32_e32 v31, v31, v32
	v_max_f32_e32 v32, v34, v29
	v_min_f32_e32 v29, v34, v29
	v_max_f32_e32 v64, v98, v51
	v_min_f32_e32 v51, v98, v51
	v_max_f32_e32 v98, v50, v53
	v_min_f32_e32 v50, v50, v53
	v_max_f32_e32 v53, v54, v55
	v_min_f32_e32 v54, v54, v55
	v_max_f32_e32 v55, v57, v52
	v_min_f32_e32 v52, v57, v52
	v_max_f32_e32 v57, v59, v58
	v_min_f32_e32 v58, v59, v58
	v_max_f32_e32 v59, v56, v61
	v_min_f32_e32 v56, v56, v61
	v_max_f32_e32 v61, v62, v63
	v_min_f32_e32 v62, v62, v63
	v_max_f32_e32 v63, v65, v60
	v_min_f32_e32 v60, v65, v60
	v_max_f32_e32 v48, v108, v107
	v_min_f32_e32 v107, v108, v107
	v_max_f32_e32 v108, v106, v110
	v_min_f32_e32 v106, v106, v110
	v_max_f32_e32 v110, v111, v112
	v_min_f32_e32 v111, v111, v112
	v_max_f32_e32 v112, v114, v109
	v_min_f32_e32 v109, v114, v109
	v_max_f32_e32 v114, v113, v43
	v_min_f32_e32 v43, v113, v43
	v_max_f32_e32 v113, v42, v45
	v_min_f32_e32 v42, v42, v45
	v_max_f32_e32 v45, v46, v47
	v_min_f32_e32 v46, v46, v47
	v_max_f32_e32 v47, v49, v44
	v_min_f32_e32 v44, v49, v44
	v_max_f32_e32 v15, v122, v3
	v_min_f32_e32 v3, v122, v3
	v_max_f32_e32 v122, v2, v6
	v_min_f32_e32 v2, v2, v6
	v_max_f32_e32 v6, v5, v8
	v_min_f32_e32 v5, v5, v8
	v_max_f32_e32 v8, v10, v4
	v_min_f32_e32 v4, v10, v4
	v_max_f32_e32 v10, v12, v9
	v_min_f32_e32 v9, v12, v9
	v_max_f32_e32 v12, v7, v14
	v_min_f32_e32 v7, v7, v14
	v_max_f32_e32 v14, v13, v16
	v_min_f32_e32 v13, v13, v16
	v_max_f32_e32 v16, v17, v11
	v_min_f32_e32 v11, v17, v11
	v_max_f32_e32 v34, v33, v20
	v_min_f32_e32 v20, v33, v20
	v_max_f32_e32 v33, v19, v18
	v_min_f32_e32 v18, v19, v18
	v_max_f32_e32 v19, v21, v23
	v_min_f32_e32 v21, v21, v23
	v_max_f32_e32 v23, v24, v22
	v_min_f32_e32 v22, v24, v22
	v_max_f32_e32 v24, v26, v28
	v_min_f32_e32 v26, v26, v28
	v_max_f32_e32 v28, v27, v25
	v_min_f32_e32 v25, v27, v25
	v_max_f32_e32 v27, v29, v31
	v_min_f32_e32 v29, v29, v31
	v_max_f32_e32 v31, v32, v30
	v_min_f32_e32 v30, v32, v30
	v_max_f32_e32 v65, v64, v98
	v_min_f32_e32 v64, v64, v98
	v_max_f32_e32 v98, v51, v50
	v_min_f32_e32 v50, v51, v50
	v_max_f32_e32 v51, v52, v54
	v_min_f32_e32 v52, v52, v54
	v_max_f32_e32 v54, v55, v53
	v_min_f32_e32 v53, v55, v53
	v_max_f32_e32 v55, v57, v59
	v_min_f32_e32 v57, v57, v59
	v_max_f32_e32 v59, v58, v56
	v_min_f32_e32 v56, v58, v56
	v_max_f32_e32 v58, v60, v62
	v_min_f32_e32 v60, v60, v62
	v_max_f32_e32 v62, v63, v61
	v_min_f32_e32 v61, v63, v61
	v_max_f32_e32 v49, v48, v108
	v_min_f32_e32 v48, v48, v108
	v_max_f32_e32 v108, v107, v106
	v_min_f32_e32 v106, v107, v106
	v_max_f32_e32 v107, v109, v111
	v_min_f32_e32 v109, v109, v111
	v_max_f32_e32 v111, v112, v110
	v_min_f32_e32 v110, v112, v110
	v_max_f32_e32 v112, v114, v113
	v_min_f32_e32 v113, v114, v113
	v_max_f32_e32 v114, v43, v42
	v_min_f32_e32 v42, v43, v42
	v_max_f32_e32 v43, v44, v46
	v_min_f32_e32 v44, v44, v46
	v_max_f32_e32 v46, v47, v45
	v_min_f32_e32 v45, v47, v45
	v_max_f32_e32 v17, v15, v122
	v_min_f32_e32 v15, v15, v122
	v_max_f32_e32 v122, v3, v2
	v_min_f32_e32 v2, v3, v2
	v_max_f32_e32 v3, v4, v5
	v_min_f32_e32 v4, v4, v5
	v_max_f32_e32 v5, v8, v6
	v_min_f32_e32 v6, v8, v6
	v_max_f32_e32 v8, v10, v12
	v_min_f32_e32 v10, v10, v12
	v_max_f32_e32 v12, v9, v7
	v_min_f32_e32 v7, v9, v7
	v_max_f32_e32 v9, v11, v13
	v_min_f32_e32 v11, v11, v13
	v_max_f32_e32 v13, v16, v14
	v_min_f32_e32 v14, v16, v14
	v_max_f32_e32 v32, v34, v21
	v_min_f32_e32 v21, v34, v21
	v_max_f32_e32 v34, v20, v19
	v_min_f32_e32 v19, v20, v19
	v_max_f32_e32 v20, v33, v22
	v_min_f32_e32 v22, v33, v22
	v_max_f32_e32 v33, v18, v23
	v_min_f32_e32 v18, v18, v23
	v_max_f32_e32 v23, v29, v24
	v_min_f32_e32 v24, v29, v24
	v_max_f32_e32 v29, v27, v26
	v_min_f32_e32 v26, v27, v26
	v_max_f32_e32 v27, v30, v28
	v_min_f32_e32 v28, v30, v28
	v_max_f32_e32 v30, v31, v25
	v_min_f32_e32 v25, v31, v25
	v_max_f32_e32 v63, v65, v52
	v_min_f32_e32 v52, v65, v52
	v_max_f32_e32 v65, v64, v51
	v_min_f32_e32 v51, v64, v51
; #define CE_DESC(a, b) do { const float _t = fmaxf(a, b); b = fminf(a, b); a = _t; } while (0)
; __device__ __forceinline__ void sort16_desc(float (&v)[16]) {
; #pragma unroll
;     for (int k = 2; k <= 16; k <<= 1)
; #pragma unroll
;         for (int j = k >> 1; j > 0; j >>= 1)
; #pragma unroll
;             for (int i = 0; i < 16; ++i) { const int l = i ^ j; if (l > i) { if ((i & k) == 0 || k == 16) CE_DESC(v[i], v[l]); else CE_DESC(v[l], v[i]); } }
; }
; __device__ __forceinline__ void route_half(float (&top)[16], LAS const unsigned char* keys_lds, const bf16_t* __restrict__ qrow, int r32, int hi) {
;     ...
;     for (int kt = 0; kt < 4; ++kt) sort16_desc(g[kt]);
	v_max_f32_e32 v64, v98, v53
	v_min_f32_e32 v53, v98, v53
	v_max_f32_e32 v98, v50, v54
	v_min_f32_e32 v50, v50, v54
	v_max_f32_e32 v54, v60, v55
	v_min_f32_e32 v55, v60, v55
	v_max_f32_e32 v60, v58, v57
	v_min_f32_e32 v57, v58, v57
	v_max_f32_e32 v58, v61, v59
	v_min_f32_e32 v59, v61, v59
	v_max_f32_e32 v61, v62, v56
	v_min_f32_e32 v56, v62, v56
	v_max_f32_e32 v47, v49, v109
	v_min_f32_e32 v49, v49, v109
	v_max_f32_e32 v109, v48, v107
	v_min_f32_e32 v48, v48, v107
	v_max_f32_e32 v107, v108, v110
	v_min_f32_e32 v108, v108, v110
	v_max_f32_e32 v110, v106, v111
	v_min_f32_e32 v106, v106, v111
	v_max_f32_e32 v111, v44, v112
	v_min_f32_e32 v44, v44, v112
	v_max_f32_e32 v112, v43, v113
	v_min_f32_e32 v43, v43, v113
	v_max_f32_e32 v113, v45, v114
	v_min_f32_e32 v45, v45, v114
	v_max_f32_e32 v114, v46, v42
	v_min_f32_e32 v42, v46, v42
	v_max_f32_e32 v16, v17, v4
	v_min_f32_e32 v4, v17, v4
	v_max_f32_e32 v17, v15, v3
	v_min_f32_e32 v3, v15, v3
	v_max_f32_e32 v15, v122, v6
	v_min_f32_e32 v6, v122, v6
	v_max_f32_e32 v122, v2, v5
	v_min_f32_e32 v2, v2, v5
	v_max_f32_e32 v5, v11, v8
	v_min_f32_e32 v8, v11, v8
	v_max_f32_e32 v11, v9, v10
	v_min_f32_e32 v9, v9, v10
	v_max_f32_e32 v10, v14, v12
	v_min_f32_e32 v12, v14, v12
	v_max_f32_e32 v14, v13, v7
	v_min_f32_e32 v7, v13, v7
	v_max_f32_e32 v31, v32, v20
	v_min_f32_e32 v20, v32, v20
	v_max_f32_e32 v32, v34, v33
	v_min_f32_e32 v33, v34, v33
	v_max_f32_e32 v34, v21, v22
	v_min_f32_e32 v21, v21, v22
	v_max_f32_e32 v22, v19, v18
	v_min_f32_e32 v18, v19, v18
	v_max_f32_e32 v19, v28, v24
	v_min_f32_e32 v24, v28, v24
	v_max_f32_e32 v28, v25, v26
	v_min_f32_e32 v25, v25, v26
	v_max_f32_e32 v26, v27, v23
	v_min_f32_e32 v23, v27, v23
	v_max_f32_e32 v27, v30, v29
	v_min_f32_e32 v29, v30, v29
	v_max_f32_e32 v62, v63, v64
	v_min_f32_e32 v63, v63, v64
	v_max_f32_e32 v64, v65, v98
	v_min_f32_e32 v65, v65, v98
	v_max_f32_e32 v98, v52, v53
	v_min_f32_e32 v52, v52, v53
	v_max_f32_e32 v53, v51, v50
	v_min_f32_e32 v50, v51, v50
	v_max_f32_e32 v51, v59, v55
	v_min_f32_e32 v55, v59, v55
	v_max_f32_e32 v59, v56, v57
	v_min_f32_e32 v56, v56, v57
	v_max_f32_e32 v57, v58, v54
	v_min_f32_e32 v54, v58, v54
	v_max_f32_e32 v58, v61, v60
	v_min_f32_e32 v60, v61, v60
	v_max_f32_e32 v46, v47, v107
	v_min_f32_e32 v47, v47, v107
	v_max_f32_e32 v107, v109, v110
	v_min_f32_e32 v109, v109, v110
	v_max_f32_e32 v110, v49, v108
	v_min_f32_e32 v49, v49, v108
	v_max_f32_e32 v108, v48, v106
	v_min_f32_e32 v48, v48, v106
	v_max_f32_e32 v106, v45, v44
	v_min_f32_e32 v44, v45, v44
	v_max_f32_e32 v45, v42, v43
	v_min_f32_e32 v42, v42, v43
	v_max_f32_e32 v43, v113, v111
	v_min_f32_e32 v111, v113, v111
	v_max_f32_e32 v113, v114, v112
	v_min_f32_e32 v112, v114, v112
	v_max_f32_e32 v13, v16, v15
	v_min_f32_e32 v15, v16, v15
	v_max_f32_e32 v16, v17, v122
	v_min_f32_e32 v17, v17, v122
	v_max_f32_e32 v122, v4, v6
	v_min_f32_e32 v4, v4, v6
	v_max_f32_e32 v6, v3, v2
	v_min_f32_e32 v2, v3, v2
	v_max_f32_e32 v3, v12, v8
	v_min_f32_e32 v8, v12, v8
	v_max_f32_e32 v12, v7, v9
	v_min_f32_e32 v7, v7, v9
	v_max_f32_e32 v9, v10, v5
	v_min_f32_e32 v5, v10, v5
	v_max_f32_e32 v10, v14, v11
	v_min_f32_e32 v11, v14, v11
	v_max_f32_e32 v30, v31, v32
	v_min_f32_e32 v31, v31, v32
	v_max_f32_e32 v32, v20, v33
	v_min_f32_e32 v20, v20, v33
	v_max_f32_e32 v33, v34, v22
	v_min_f32_e32 v22, v34, v22
	v_max_f32_e32 v34, v21, v18
	v_min_f32_e32 v18, v21, v18
	v_max_f32_e32 v21, v25, v24
	v_min_f32_e32 v24, v25, v24
	v_max_f32_e32 v25, v28, v19
	v_min_f32_e32 v19, v28, v19
	v_max_f32_e32 v28, v29, v23
	v_min_f32_e32 v23, v29, v23
	v_max_f32_e32 v29, v27, v26
	v_min_f32_e32 v26, v27, v26
	v_max_f32_e32 v61, v62, v64
	v_min_f32_e32 v62, v62, v64
	v_max_f32_e32 v64, v63, v65
	v_min_f32_e32 v63, v63, v65
	v_max_f32_e32 v65, v98, v53
	v_min_f32_e32 v53, v98, v53
	v_max_f32_e32 v98, v52, v50
	v_min_f32_e32 v50, v52, v50
	v_max_f32_e32 v52, v56, v55
	v_min_f32_e32 v55, v56, v55
	v_max_f32_e32 v56, v59, v51
	v_min_f32_e32 v51, v59, v51
	v_max_f32_e32 v59, v60, v54
	v_min_f32_e32 v54, v60, v54
	v_max_f32_e32 v60, v58, v57
	v_min_f32_e32 v57, v58, v57
	v_max_f32_e32 v114, v46, v107
	v_min_f32_e32 v46, v46, v107
	v_max_f32_e32 v107, v47, v109
	v_min_f32_e32 v47, v47, v109
	v_max_f32_e32 v109, v110, v108
	v_min_f32_e32 v108, v110, v108
	v_max_f32_e32 v110, v49, v48
	v_min_f32_e32 v48, v49, v48
	v_max_f32_e32 v49, v42, v44
	v_min_f32_e32 v42, v42, v44
	v_max_f32_e32 v44, v45, v106
	v_min_f32_e32 v45, v45, v106
	v_max_f32_e32 v106, v112, v111
	v_min_f32_e32 v111, v112, v111
	v_max_f32_e32 v112, v113, v43
	v_min_f32_e32 v43, v113, v43
	v_max_f32_e32 v14, v13, v16
	v_min_f32_e32 v13, v13, v16
	v_max_f32_e32 v16, v15, v17
	v_min_f32_e32 v15, v15, v17
	v_max_f32_e32 v17, v122, v6
	v_min_f32_e32 v6, v122, v6
	v_max_f32_e32 v122, v4, v2
	v_min_f32_e32 v2, v4, v2
	v_max_f32_e32 v4, v7, v8
	v_min_f32_e32 v7, v7, v8
	v_max_f32_e32 v8, v12, v3
	v_min_f32_e32 v3, v12, v3
	v_max_f32_e32 v12, v11, v5
	v_min_f32_e32 v5, v11, v5
	v_max_f32_e32 v11, v10, v9
	v_min_f32_e32 v9, v10, v9
	v_max_f32_e32 v27, v30, v24
	v_min_f32_e32 v24, v30, v24
	v_max_f32_e32 v30, v31, v21
	v_min_f32_e32 v21, v31, v21
	v_max_f32_e32 v31, v32, v19
	v_min_f32_e32 v19, v32, v19
	v_max_f32_e32 v32, v20, v25
	v_min_f32_e32 v20, v20, v25
	v_max_f32_e32 v25, v33, v23
	v_min_f32_e32 v23, v33, v23
	v_max_f32_e32 v33, v22, v28
	v_min_f32_e32 v22, v22, v28
	v_max_f32_e32 v28, v34, v26
	v_min_f32_e32 v26, v34, v26
	v_max_f32_e32 v34, v18, v29
	v_min_f32_e32 v18, v18, v29
	v_max_f32_e32 v58, v61, v55
	v_min_f32_e32 v55, v61, v55
	v_max_f32_e32 v61, v62, v52
	v_min_f32_e32 v52, v62, v52
	v_max_f32_e32 v62, v64, v51
	v_min_f32_e32 v51, v64, v51
; #define CE_DESC(a, b) do { const float _t = fmaxf(a, b); b = fminf(a, b); a = _t; } while (0)
; __device__ __forceinline__ void sort16_desc(float (&v)[16]) {
; #pragma unroll
;     for (int k = 2; k <= 16; k <<= 1)
; #pragma unroll
;         for (int j = k >> 1; j > 0; j >>= 1)
; #pragma unroll
;             for (int i = 0; i < 16; ++i) { const int l = i ^ j; if (l > i) { if ((i & k) == 0 || k == 16) CE_DESC(v[i], v[l]); else CE_DESC(v[l], v[i]); } }
; }
; __device__ __forceinline__ void merge16_desc(float (&a)[16], const float (&b)[16]) {
; #pragma unroll
;     for (int i = 0; i < 16; ++i) a[i] = fmaxf(a[i], b[15 - i]);
; #pragma unroll
;     for (int j = 8; j > 0; j >>= 1)
; #pragma unroll
;         for (int i = 0; i < 16; ++i) { const int l = i ^ j; if (l > i) CE_DESC(a[i], a[l]); }
; __device__ __forceinline__ void route_half(float (&top)[16], LAS const unsigned char* keys_lds, const bf16_t* __restrict__ qrow, int r32, int hi) {
;     ...
;     for (int kt = 0; kt < 4; ++kt) sort16_desc(g[kt]);
;     merge16_desc(g[0], g[1]); merge16_desc(g[2], g[3]); merge16_desc(g[0], g[2]);
	v_max_f32_e32 v64, v63, v56
	v_min_f32_e32 v56, v63, v56
	v_max_f32_e32 v63, v65, v54
	v_min_f32_e32 v54, v65, v54
	v_max_f32_e32 v65, v53, v59
	v_min_f32_e32 v53, v53, v59
	v_max_f32_e32 v59, v98, v57
	v_min_f32_e32 v57, v98, v57
	v_max_f32_e32 v98, v50, v60
	v_min_f32_e32 v50, v50, v60
	v_max_f32_e32 v113, v114, v42
	v_min_f32_e32 v42, v114, v42
	v_max_f32_e32 v114, v46, v49
	v_min_f32_e32 v46, v46, v49
	v_max_f32_e32 v49, v107, v45
	v_min_f32_e32 v45, v107, v45
	v_max_f32_e32 v107, v47, v44
	v_min_f32_e32 v44, v47, v44
	v_max_f32_e32 v47, v109, v111
	v_min_f32_e32 v109, v109, v111
	v_max_f32_e32 v111, v108, v106
	v_min_f32_e32 v106, v108, v106
	v_max_f32_e32 v108, v110, v43
	v_min_f32_e32 v43, v110, v43
	v_max_f32_e32 v110, v48, v112
	v_min_f32_e32 v48, v48, v112
	v_max_f32_e32 v10, v14, v7
	v_min_f32_e32 v7, v14, v7
	v_max_f32_e32 v14, v13, v4
	v_min_f32_e32 v4, v13, v4
	v_max_f32_e32 v13, v16, v3
	v_min_f32_e32 v3, v16, v3
	v_max_f32_e32 v16, v15, v8
	v_min_f32_e32 v8, v15, v8
	v_max_f32_e32 v15, v17, v5
	v_min_f32_e32 v5, v17, v5
	v_max_f32_e32 v17, v6, v12
	v_min_f32_e32 v6, v6, v12
	v_max_f32_e32 v12, v122, v9
	v_min_f32_e32 v9, v122, v9
	v_max_f32_e32 v122, v2, v11
	v_min_f32_e32 v2, v2, v11
	v_max_f32_e32 v29, v27, v25
	v_min_f32_e32 v25, v27, v25
	v_max_f32_e32 v27, v30, v33
	v_min_f32_e32 v33, v30, v33
	v_max_f32_e32 v30, v31, v28
	v_min_f32_e32 v28, v31, v28
	v_max_f32_e32 v31, v32, v34
	v_min_f32_e32 v32, v32, v34
	v_max_f32_e32 v34, v24, v23
	v_min_f32_e32 v35, v24, v23
	v_max_f32_e32 v36, v21, v22
	v_min_f32_e32 v37, v21, v22
	v_max_f32_e32 v21, v19, v26
	v_min_f32_e32 v38, v19, v26
	v_max_f32_e32 v39, v20, v18
	v_min_f32_e32 v40, v20, v18
	v_max_f32_e32 v60, v58, v63
	v_min_f32_e32 v58, v58, v63
	v_max_f32_e32 v63, v61, v65
	v_min_f32_e32 v61, v61, v65
	v_max_f32_e32 v65, v62, v59
	v_min_f32_e32 v59, v62, v59
	v_max_f32_e32 v62, v64, v98
	v_min_f32_e32 v64, v64, v98
	v_max_f32_e32 v98, v55, v54
	v_min_f32_e32 v54, v55, v54
	v_max_f32_e32 v55, v52, v53
	v_min_f32_e32 v52, v52, v53
	v_max_f32_e32 v53, v51, v57
	v_min_f32_e32 v51, v51, v57
	v_max_f32_e32 v57, v56, v50
	v_min_f32_e32 v50, v56, v50
	v_max_f32_e32 v112, v113, v47
	v_min_f32_e32 v47, v113, v47
	v_max_f32_e32 v113, v114, v111
	v_min_f32_e32 v111, v114, v111
	v_max_f32_e32 v114, v49, v108
	v_min_f32_e32 v49, v49, v108
	v_max_f32_e32 v108, v107, v110
	v_min_f32_e32 v107, v107, v110
	v_max_f32_e32 v110, v42, v109
	v_min_f32_e32 v42, v42, v109
	v_max_f32_e32 v109, v46, v106
	v_min_f32_e32 v46, v46, v106
	v_max_f32_e32 v106, v45, v43
	v_min_f32_e32 v43, v45, v43
	v_max_f32_e32 v45, v44, v48
	v_min_f32_e32 v44, v44, v48
	v_max_f32_e32 v11, v10, v15
	v_min_f32_e32 v10, v10, v15
	v_max_f32_e32 v15, v14, v17
	v_min_f32_e32 v14, v14, v17
	v_max_f32_e32 v17, v13, v12
	v_min_f32_e32 v12, v13, v12
	v_max_f32_e32 v13, v16, v122
	v_min_f32_e32 v16, v16, v122
	v_max_f32_e32 v122, v7, v5
	v_min_f32_e32 v5, v7, v5
	v_max_f32_e32 v7, v4, v6
	v_min_f32_e32 v4, v4, v6
	v_max_f32_e32 v6, v3, v9
	v_min_f32_e32 v3, v3, v9
	v_max_f32_e32 v9, v8, v2
	v_min_f32_e32 v2, v8, v2
	v_max_f32_e32 v22, v29, v30
	v_min_f32_e32 v18, v29, v30
	v_max_f32_e32 v30, v27, v31
	v_min_f32_e32 v26, v27, v31
	v_max_f32_e32 v23, v25, v28
	v_min_f32_e32 v19, v25, v28
	v_max_f32_e32 v31, v33, v32
	v_min_f32_e32 v27, v33, v32
	v_max_f32_e32 v24, v34, v21
	v_min_f32_e32 v20, v34, v21
	v_max_f32_e32 v32, v36, v39
	v_min_f32_e32 v28, v36, v39
	v_max_f32_e32 v25, v35, v38
	v_min_f32_e32 v21, v35, v38
	v_max_f32_e32 v33, v37, v40
	v_min_f32_e32 v29, v37, v40
	v_max_f32_e32 v56, v60, v65
	v_min_f32_e32 v60, v60, v65
	v_max_f32_e32 v65, v63, v62
	v_min_f32_e32 v62, v63, v62
	v_max_f32_e32 v63, v58, v59
	v_min_f32_e32 v58, v58, v59
	v_max_f32_e32 v59, v61, v64
	v_min_f32_e32 v61, v61, v64
	v_max_f32_e32 v64, v98, v53
	v_min_f32_e32 v53, v98, v53
	v_max_f32_e32 v98, v55, v57
	v_min_f32_e32 v55, v55, v57
	v_max_f32_e32 v57, v54, v51
	v_min_f32_e32 v51, v54, v51
	v_max_f32_e32 v54, v52, v50
	v_min_f32_e32 v50, v52, v50
	v_max_f32_e32 v48, v112, v114
	v_min_f32_e32 v112, v112, v114
	v_max_f32_e32 v114, v113, v108
	v_min_f32_e32 v108, v113, v108
	v_max_f32_e32 v113, v47, v49
	v_min_f32_e32 v47, v47, v49
	v_max_f32_e32 v49, v111, v107
	v_min_f32_e32 v107, v111, v107
	v_max_f32_e32 v111, v110, v106
	v_min_f32_e32 v106, v110, v106
	v_max_f32_e32 v110, v109, v45
	v_min_f32_e32 v45, v109, v45
	v_max_f32_e32 v109, v42, v43
	v_min_f32_e32 v42, v42, v43
	v_max_f32_e32 v43, v46, v44
	v_min_f32_e32 v44, v46, v44
	v_max_f32_e32 v8, v11, v17
	v_min_f32_e32 v11, v11, v17
	v_max_f32_e32 v17, v15, v13
	v_min_f32_e32 v13, v15, v13
	v_max_f32_e32 v15, v10, v12
	v_min_f32_e32 v10, v10, v12
	v_max_f32_e32 v12, v14, v16
	v_min_f32_e32 v14, v14, v16
	v_max_f32_e32 v16, v122, v6
	v_min_f32_e32 v6, v122, v6
	v_max_f32_e32 v122, v7, v9
	v_min_f32_e32 v7, v7, v9
	v_max_f32_e32 v9, v5, v3
	v_min_f32_e32 v3, v5, v3
	v_max_f32_e32 v5, v4, v2
	v_min_f32_e32 v2, v4, v2
	v_min_f32_e32 v41, v22, v30
	v_min_f32_e32 v40, v18, v26
	v_min_f32_e32 v39, v23, v31
	v_min_f32_e32 v38, v19, v27
	v_min_f32_e32 v37, v24, v32
	v_min_f32_e32 v36, v20, v28
	v_min_f32_e32 v35, v25, v33
	v_min_f32_e32 v34, v21, v29
	v_min_f32_e32 v52, v56, v65
	v_min_f32_e32 v99, v60, v62
	v_min_f32_e32 v100, v63, v59
	v_min_f32_e32 v101, v58, v61
	v_min_f32_e32 v102, v64, v98
	v_min_f32_e32 v103, v53, v55
	v_min_f32_e32 v104, v57, v54
	v_min_f32_e32 v105, v51, v50
	v_min_f32_e32 v46, v48, v114
	v_min_f32_e32 v115, v112, v108
	v_min_f32_e32 v116, v113, v49
	v_min_f32_e32 v117, v47, v107
	v_min_f32_e32 v118, v111, v110
	v_min_f32_e32 v119, v106, v45
	v_min_f32_e32 v120, v109, v43
; #define CE_DESC(a, b) do { const float _t = fmaxf(a, b); b = fminf(a, b); a = _t; } while (0)
; __device__ __forceinline__ void merge16_desc(float (&a)[16], const float (&b)[16]) {
; #pragma unroll
;     for (int i = 0; i < 16; ++i) a[i] = fmaxf(a[i], b[15 - i]);
; #pragma unroll
;     for (int j = 8; j > 0; j >>= 1)
; #pragma unroll
;         for (int i = 0; i < 16; ++i) { const int l = i ^ j; if (l > i) CE_DESC(a[i], a[l]); }
; __device__ __forceinline__ void route_half(float (&top)[16], LAS const unsigned char* keys_lds, const bf16_t* __restrict__ qrow, int r32, int hi) {
;     ...
;     merge16_desc(g[0], g[1]); merge16_desc(g[2], g[3]); merge16_desc(g[0], g[2]);
	v_min_f32_e32 v121, v42, v44
	v_min_f32_e32 v4, v8, v17
	v_min_f32_e32 v123, v11, v13
	v_min_f32_e32 v124, v15, v12
	v_min_f32_e32 v125, v10, v14
	v_min_f32_e32 v149, v16, v122
	v_min_f32_e32 v150, v6, v7
	v_min_f32_e32 v151, v9, v5
	v_min_f32_e32 v152, v3, v2
	v_max3_f32 v22, v22, v30, v105
	v_max3_f32 v30, v41, v51, v50
	v_max3_f32 v18, v18, v26, v104
	v_max3_f32 v26, v40, v57, v54
	v_max3_f32 v23, v23, v31, v103
	v_max3_f32 v31, v39, v53, v55
	v_max3_f32 v19, v19, v27, v102
	v_max3_f32 v27, v38, v64, v98
	v_max3_f32 v24, v24, v32, v101
	v_max3_f32 v32, v37, v58, v61
	v_max3_f32 v20, v20, v28, v100
	v_max3_f32 v28, v36, v63, v59
	v_max3_f32 v25, v25, v33, v99
	v_max3_f32 v33, v35, v60, v62
	v_max3_f32 v21, v21, v29, v52
	v_max3_f32 v29, v34, v56, v65
	v_max3_f32 v48, v48, v114, v152
	v_max3_f32 v2, v46, v3, v2
	v_max3_f32 v3, v112, v108, v151
	v_max3_f32 v5, v115, v9, v5
	v_max3_f32 v9, v113, v49, v150
	v_max3_f32 v6, v116, v6, v7
	v_max3_f32 v7, v47, v107, v149
	v_max3_f32 v16, v117, v16, v122
	v_max3_f32 v46, v111, v110, v125
	v_max3_f32 v10, v118, v10, v14
	v_max3_f32 v14, v106, v45, v124
	v_max3_f32 v12, v119, v15, v12
	v_max3_f32 v15, v109, v43, v123
	v_max3_f32 v11, v120, v11, v13
	v_max3_f32 v4, v42, v44, v4
	v_max3_f32 v8, v121, v8, v17
	v_max_f32_e32 v34, v22, v24
	v_min_f32_e32 v22, v22, v24
	v_max_f32_e32 v24, v30, v32
	v_min_f32_e32 v30, v30, v32
	v_max_f32_e32 v32, v18, v20
	v_min_f32_e32 v18, v18, v20
	v_max_f32_e32 v20, v26, v28
	v_min_f32_e32 v26, v26, v28
	v_max_f32_e32 v28, v23, v25
	v_min_f32_e32 v23, v23, v25
	v_max_f32_e32 v25, v31, v33
	v_min_f32_e32 v31, v31, v33
	v_max_f32_e32 v33, v19, v21
	v_min_f32_e32 v19, v19, v21
	v_max_f32_e32 v21, v27, v29
	v_min_f32_e32 v27, v27, v29
	v_max_f32_e32 v13, v48, v46
	v_min_f32_e32 v17, v48, v46
	v_max_f32_e32 v42, v2, v10
	v_min_f32_e32 v2, v2, v10
	v_max_f32_e32 v10, v3, v14
	v_min_f32_e32 v3, v3, v14
	v_max_f32_e32 v14, v5, v12
	v_min_f32_e32 v5, v5, v12
	v_max_f32_e32 v12, v9, v15
	v_min_f32_e32 v9, v9, v15
	v_max_f32_e32 v15, v6, v11
	v_min_f32_e32 v6, v6, v11
	v_max_f32_e32 v11, v7, v4
	v_min_f32_e32 v4, v7, v4
	v_max_f32_e32 v7, v16, v8
	v_min_f32_e32 v8, v16, v8
	v_max_f32_e32 v29, v34, v28
	v_min_f32_e32 v28, v34, v28
	v_max_f32_e32 v34, v24, v25
	v_min_f32_e32 v24, v24, v25
	v_max_f32_e32 v25, v32, v33
	v_min_f32_e32 v32, v32, v33
	v_max_f32_e32 v33, v20, v21
	v_min_f32_e32 v20, v20, v21
	v_max_f32_e32 v21, v22, v23
	v_min_f32_e32 v22, v22, v23
	v_max_f32_e32 v23, v30, v31
	v_min_f32_e32 v30, v30, v31
	v_max_f32_e32 v31, v18, v19
	v_min_f32_e32 v18, v18, v19
	v_max_f32_e32 v19, v26, v27
	v_min_f32_e32 v26, v26, v27
	v_max_f32_e32 v16, v13, v12
	v_min_f32_e32 v12, v13, v12
	v_max_f32_e32 v13, v42, v15
	v_min_f32_e32 v15, v42, v15
	v_max_f32_e32 v42, v10, v11
	v_min_f32_e32 v10, v10, v11
	v_max_f32_e32 v11, v14, v7
	v_min_f32_e32 v7, v14, v7
	v_max_f32_e32 v14, v17, v9
	v_min_f32_e32 v9, v17, v9
	v_max_f32_e32 v17, v2, v6
	v_min_f32_e32 v2, v2, v6
	v_max_f32_e32 v6, v3, v4
	v_min_f32_e32 v3, v3, v4
	v_max_f32_e32 v4, v5, v8
	v_min_f32_e32 v5, v5, v8
	v_max_f32_e32 v27, v29, v25
	v_min_f32_e32 v25, v29, v25
	v_max_f32_e32 v29, v34, v33
	v_min_f32_e32 v33, v34, v33
	v_max_f32_e32 v34, v28, v32
	v_min_f32_e32 v28, v28, v32
	v_max_f32_e32 v32, v24, v20
	v_min_f32_e32 v20, v24, v20
	v_max_f32_e32 v24, v21, v31
	v_min_f32_e32 v21, v21, v31
	v_max_f32_e32 v31, v23, v19
	v_min_f32_e32 v19, v23, v19
	v_max_f32_e32 v23, v22, v18
	v_min_f32_e32 v18, v22, v18
	v_max_f32_e32 v22, v30, v26
	v_min_f32_e32 v26, v30, v26
	v_max_f32_e32 v8, v16, v42
	v_min_f32_e32 v16, v16, v42
	v_max_f32_e32 v42, v13, v11
	v_min_f32_e32 v11, v13, v11
	v_max_f32_e32 v13, v12, v10
	v_min_f32_e32 v10, v12, v10
	v_max_f32_e32 v12, v15, v7
	v_min_f32_e32 v7, v15, v7
	v_max_f32_e32 v15, v14, v6
	v_min_f32_e32 v6, v14, v6
	v_max_f32_e32 v14, v17, v4
	v_min_f32_e32 v4, v17, v4
	v_max_f32_e32 v17, v9, v3
	v_min_f32_e32 v3, v9, v3
	v_max_f32_e32 v9, v2, v5
	v_min_f32_e32 v2, v2, v5
	v_min_f32_e32 v30, v27, v29
	v_min_f32_e32 v35, v25, v33
	v_min_f32_e32 v36, v34, v32
	v_min_f32_e32 v37, v28, v20
	v_min_f32_e32 v38, v24, v31
	v_min_f32_e32 v39, v21, v19
	v_min_f32_e32 v40, v23, v22
	v_min_f32_e32 v41, v18, v26
	v_min_f32_e32 v5, v8, v42
	v_min_f32_e32 v43, v16, v11
	v_min_f32_e32 v44, v13, v12
	v_min_f32_e32 v45, v10, v7
	v_min_f32_e32 v46, v15, v14
	v_min_f32_e32 v47, v6, v4
	v_min_f32_e32 v48, v17, v9
	v_min_f32_e32 v49, v3, v2
	v_max3_f32 v27, v27, v29, v49
	v_max3_f32 v2, v30, v3, v2
	v_max3_f32 v3, v25, v33, v48
	v_max3_f32 v9, v35, v17, v9
	v_max3_f32 v17, v34, v32, v47
	v_max3_f32 v4, v36, v6, v4
	v_max3_f32 v6, v28, v20, v46
	v_max3_f32 v14, v37, v15, v14
	v_max3_f32 v15, v24, v31, v45
	v_max3_f32 v7, v38, v10, v7
	v_max3_f32 v10, v21, v19, v44
	v_max3_f32 v12, v39, v13, v12
	v_max3_f32 v13, v23, v22, v43
	v_max3_f32 v11, v40, v16, v11
	v_max3_f32 v5, v18, v26, v5
	v_max3_f32 v8, v41, v8, v42
	v_max_f32_e32 v16, v27, v15
	v_min_f32_e32 v15, v27, v15
	v_max_f32_e32 v18, v2, v7
	v_min_f32_e32 v2, v2, v7
	v_max_f32_e32 v7, v3, v10
	v_min_f32_e32 v3, v3, v10
	v_max_f32_e32 v10, v9, v12
	v_min_f32_e32 v9, v9, v12
	v_max_f32_e32 v12, v17, v13
	v_min_f32_e32 v13, v17, v13
	v_max_f32_e32 v17, v4, v11
	v_min_f32_e32 v4, v4, v11
	v_max_f32_e32 v11, v6, v5
	v_min_f32_e32 v5, v6, v5
	v_max_f32_e32 v6, v14, v8
	v_min_f32_e32 v8, v14, v8
	v_max_f32_e32 v14, v16, v12
	v_min_f32_e32 v12, v16, v12
	v_max_f32_e32 v16, v18, v17
	v_min_f32_e32 v17, v18, v17
	v_max_f32_e32 v18, v7, v11
	v_min_f32_e32 v7, v7, v11
	v_max_f32_e32 v11, v10, v6
	v_min_f32_e32 v6, v10, v6
	v_max_f32_e32 v10, v15, v13
	v_min_f32_e32 v13, v15, v13
; __device__ __forceinline__ void route_half(float (&top)[16], LAS const unsigned char* keys_lds, const bf16_t* __restrict__ qrow, int r32, int hi) {
;     ...
;     merge16_desc(g[0], g[1]); merge16_desc(g[2], g[3]); merge16_desc(g[0], g[2]);
;     float o[16];
; #pragma unroll
;     for (int i = 0; i < 16; ++i) { g[0][i] = __uint_as_float(__float_as_uint(g[0][i]) | hi4); o[i] = __shfl_xor(g[0][i], 32); }
;     merge16_desc(g[0], o);
	v_max_f32_e32 v15, v2, v4
	v_min_f32_e32 v2, v2, v4
	v_max_f32_e32 v4, v3, v5
	v_min_f32_e32 v3, v3, v5
	v_max_f32_e32 v5, v9, v8
	v_min_f32_e32 v8, v9, v8
	v_max_f32_e32 v9, v14, v18
	v_min_f32_e32 v14, v14, v18
	v_max_f32_e32 v18, v16, v11
	v_min_f32_e32 v11, v16, v11
	v_max_f32_e32 v16, v12, v7
	v_min_f32_e32 v7, v12, v7
	v_max_f32_e32 v12, v17, v6
	v_min_f32_e32 v6, v17, v6
	v_max_f32_e32 v17, v10, v4
	v_min_f32_e32 v4, v10, v4
	v_max_f32_e32 v10, v15, v5
	v_min_f32_e32 v5, v15, v5
	v_max_f32_e32 v15, v13, v3
	v_min_f32_e32 v3, v13, v3
	v_max_f32_e32 v13, v2, v8
	v_min_f32_e32 v2, v2, v8
	v_max_f32_e32 v8, v9, v18
	v_min_f32_e32 v9, v9, v18
	v_max_f32_e32 v18, v14, v11
	v_min_f32_e32 v11, v14, v11
	v_max_f32_e32 v14, v16, v12
	v_min_f32_e32 v12, v16, v12
	v_max_f32_e32 v16, v7, v6
	v_min_f32_e32 v6, v7, v6
	v_max_f32_e32 v7, v17, v10
	v_min_f32_e32 v10, v17, v10
	v_max_f32_e32 v17, v4, v5
	v_min_f32_e32 v4, v4, v5
	v_max_f32_e32 v5, v15, v13
	v_min_f32_e32 v13, v15, v13
	v_max_f32_e32 v15, v3, v2
	v_min_f32_e32 v2, v3, v2
	v_or_b32_e32 v173, v144, v8
	v_or_b32_e32 v172, v144, v9
	v_or_b32_e32 v171, v144, v18
	v_or_b32_e32 v169, v144, v11
	v_or_b32_e32 v168, v144, v14
	v_or_b32_e32 v167, v144, v12
	v_or_b32_e32 v166, v144, v16
	v_or_b32_e32 v165, v144, v6
	v_or_b32_e32 v164, v144, v7
	v_or_b32_e32 v162, v144, v10
	v_or_b32_e32 v161, v144, v17
	v_or_b32_e32 v160, v144, v4
	v_or_b32_e32 v159, v144, v5
	v_or_b32_e32 v158, v144, v13
	v_or_b32_e32 v156, v144, v15
	v_or_b32_e32 v155, v144, v2
	ds_bpermute_b32 v149, v142, v173
	ds_bpermute_b32 v150, v142, v172
	ds_bpermute_b32 v151, v142, v171
	ds_bpermute_b32 v152, v142, v169
	ds_bpermute_b32 v153, v142, v168
	ds_bpermute_b32 v154, v142, v167
	ds_bpermute_b32 v157, v142, v166
	ds_bpermute_b32 v163, v142, v165
	ds_bpermute_b32 v170, v142, v164
	ds_bpermute_b32 v174, v142, v162
	ds_bpermute_b32 v175, v142, v161
	ds_bpermute_b32 v176, v142, v160
	ds_bpermute_b32 v177, v142, v159
	ds_bpermute_b32 v178, v142, v158
	ds_bpermute_b32 v179, v142, v156
	ds_bpermute_b32 v180, v142, v155
	s_and_b64 vcc, exec, s[10:11]
	s_cbranch_vccnz .LBB0_916
; template <bool SIGNED4> __device__ __forceinline__ void qrow_store(const f32x4 (&v)[4], unsigned char* q, float* scale, int row, int lane) {
;     float ss = 0.f;
; #pragma unroll
;     for (int j = 0; j < 4; ++j) ss += v[j].x * v[j].x + v[j].y * v[j].y + v[j].z * v[j].z + v[j].w * v[j].w;
;     ss = wave_sum(ss);
;     const float sc = ss > 0.f ? 0.3352f * sqrtf(ss * (1.f / 1024.f)) : 1.f, inv = __builtin_amdgcn_rcpf(sc);
;     unsigned n[16];
; #pragma unroll
;     for (int j = 0; j < 4; ++j) {
; #pragma unroll
;         for (int i = 0; i < 4; ++i) { const float f = floorf(v[j][i] * inv) + 8.f; n[4 * j + i] = (unsigned)fminf(fmaxf(f, 0.f), 15.f); } }
;     u32x2 o;
; #pragma unroll
;     for (int m = 0; m < 2; ++m) { unsigned w = 0;
; #pragma unroll
;         for (int b = 0; b < 4; ++b) w |= (n[8 * m + b] | (n[8 * m + 4 + b] << 4)) << (8 * b);
;         o[m] = SIGNED4 ? (w ^ 0x88888888u) : w; }
;     *(u32x2*)(q + (size_t)row * 1024 + lane * 16) = o;
;     if (lane == 0) scale[row] = sc;
; }
	v_mul_f32_e32 v2, v67, v67
	v_mul_f32_e32 v3, v71, v71
	v_fmac_f32_e32 v2, v66, v66
	v_fmac_f32_e32 v3, v70, v70
	v_fmac_f32_e32 v2, v68, v68
	v_fmac_f32_e32 v3, v72, v72
	v_fmac_f32_e32 v2, v69, v69
	v_fmac_f32_e32 v3, v73, v73
	v_add_f32_e32 v2, v2, v3
	v_mul_f32_e32 v3, v75, v75
	v_fmac_f32_e32 v3, v74, v74
	v_fmac_f32_e32 v3, v76, v76
	v_fmac_f32_e32 v3, v77, v77
	v_add_f32_e32 v2, v3, v2
	v_mul_f32_e32 v3, v83, v83
	v_fmac_f32_e32 v3, v82, v82
	v_fmac_f32_e32 v3, v84, v84
	v_fmac_f32_e32 v3, v85, v85
	v_add_f32_e32 v2, v3, v2
	s_ashr_i32 s27, s26, 31
	s_lshl_b64 s[0:1], s[26:27], 10
	v_add_f32_dpp v2, v2, v2 quad_perm:[1,0,3,2] row_mask:0xf bank_mask:0xf bound_ctrl:1
	s_nop 1
	v_add_f32_dpp v2, v2, v2 quad_perm:[2,3,0,1] row_mask:0xf bank_mask:0xf bound_ctrl:1
	s_nop 1
	v_add_f32_dpp v2, v2, v2 row_ror:4 row_mask:0xf bank_mask:0xf bound_ctrl:1
	s_nop 1
	v_add_f32_dpp v2, v2, v2 row_ror:8 row_mask:0xf bank_mask:0xf bound_ctrl:1
	v_mov_b32_e32 v3, v2
	s_nop 1
	v_permlane16_swap_b32_e32 v2, v3
	v_add_f32_e32 v2, v2, v3
	v_mov_b32_e32 v3, v2
	s_nop 1
	v_permlane32_swap_b32_e32 v2, v3
	v_add_f32_e32 v2, v2, v3
	v_mul_f32_e32 v3, 0x3a800000, v2
	v_mul_f32_e32 v4, 0x4f800000, v3
	v_cmp_gt_f32_e32 vcc, s44, v3
	s_nop 1
	v_cndmask_b32_e32 v3, v3, v4, vcc
	v_sqrt_f32_e32 v4, v3
	s_nop 0
	v_add_u32_e32 v5, -1, v4
	v_fma_f32 v6, -v5, v4, v3
	v_cmp_ge_f32_e64 s[12:13], 0, v6
	v_add_u32_e32 v6, 1, v4
	s_nop 0
	v_cndmask_b32_e64 v5, v4, v5, s[12:13]
	v_fma_f32 v4, -v6, v4, v3
	v_cmp_lt_f32_e64 s[12:13], 0, v4
	s_nop 1
	v_cndmask_b32_e64 v4, v5, v6, s[12:13]
	v_mul_f32_e32 v5, 0x37800000, v4
	v_cndmask_b32_e32 v4, v4, v5, vcc
	v_cmp_class_f32_e32 vcc, v3, v147
	s_nop 1
	v_cndmask_b32_e32 v3, v4, v3, vcc
	v_mul_f32_e32 v3, 0x3eab9f56, v3
	v_cmp_lt_f32_e32 vcc, 0, v2
	s_nop 1
	v_cndmask_b32_e32 v2, 1.0, v3, vcc
	v_rcp_f32_e32 v3, v2
	s_nop 0
	v_mul_f32_e32 v11, v73, v3
	v_mul_f32_e32 v4, v66, v3
	v_mul_f32_e32 v7, v69, v3
	v_mul_f32_e32 v10, v72, v3
	v_floor_f32_e32 v11, v11
	v_floor_f32_e32 v4, v4
	v_mul_f32_e32 v5, v67, v3
	v_mul_f32_e32 v6, v68, v3
	v_floor_f32_e32 v7, v7
	v_mul_f32_e32 v9, v71, v3
	v_floor_f32_e32 v10, v10
	v_add_f32_e32 v11, 0x41000000, v11
	v_add_f32_e32 v4, 0x41000000, v4
	v_floor_f32_e32 v5, v5
	v_floor_f32_e32 v6, v6
	v_add_f32_e32 v7, 0x41000000, v7
	v_mul_f32_e32 v8, v70, v3
	v_floor_f32_e32 v9, v9
	v_add_f32_e32 v10, 0x41000000, v10
	v_med3_f32 v11, v11, 0, v148
	v_mul_f32_e32 v12, v74, v3
	v_mul_f32_e32 v13, v75, v3
	v_mul_f32_e32 v14, v76, v3
	v_mul_f32_e32 v15, v77, v3
	v_mul_f32_e32 v16, v82, v3
	v_mul_f32_e32 v17, v83, v3
	v_mul_f32_e32 v18, v84, v3
	v_mul_f32_e32 v3, v85, v3
	v_med3_f32 v4, v4, 0, v148
	v_add_f32_e32 v5, 0x41000000, v5
	v_add_f32_e32 v6, 0x41000000, v6
	v_med3_f32 v7, v7, 0, v148
	v_floor_f32_e32 v8, v8
	v_add_f32_e32 v9, 0x41000000, v9
	v_med3_f32 v10, v10, 0, v148
	v_cvt_u32_f32_e32 v11, v11
	v_floor_f32_e32 v3, v3
	v_cvt_u32_f32_e32 v4, v4
	v_med3_f32 v5, v5, 0, v148
	v_med3_f32 v6, v6, 0, v148
	v_cvt_u32_f32_sdwa v7, v7 dst_sel:BYTE_3 dst_unused:UNUSED_PAD src0_sel:DWORD
	v_add_f32_e32 v8, 0x41000000, v8
	v_med3_f32 v9, v9, 0, v148
	v_cvt_u32_f32_e32 v10, v10
	v_floor_f32_e32 v12, v12
	v_floor_f32_e32 v15, v15
	v_floor_f32_e32 v18, v18
	v_add_f32_e32 v3, 0x41000000, v3
	v_cvt_u32_f32_e32 v5, v5
	v_cvt_u32_f32_sdwa v6, v6 dst_sel:WORD_1 dst_unused:UNUSED_PAD src0_sel:DWORD
	v_med3_f32 v8, v8, 0, v148
	v_cvt_u32_f32_e32 v9, v9
	v_add_f32_e32 v12, 0x41000000, v12
	v_floor_f32_e32 v13, v13
	v_floor_f32_e32 v14, v14
	v_add_f32_e32 v15, 0x41000000, v15
	v_floor_f32_e32 v17, v17
	v_add_f32_e32 v18, 0x41000000, v18
	v_med3_f32 v3, v3, 0, v148
	v_cvt_u32_f32_e32 v8, v8
	v_med3_f32 v12, v12, 0, v148
	v_add_f32_e32 v13, 0x41000000, v13
	v_add_f32_e32 v14, 0x41000000, v14
	v_med3_f32 v15, v15, 0, v148
	v_floor_f32_e32 v16, v16
	v_add_f32_e32 v17, 0x41000000, v17
	v_med3_f32 v18, v18, 0, v148
	v_cvt_u32_f32_e32 v3, v3
	v_cvt_u32_f32_e32 v12, v12
	v_med3_f32 v13, v13, 0, v148
	v_med3_f32 v14, v14, 0, v148
	v_cvt_u32_f32_sdwa v15, v15 dst_sel:BYTE_3 dst_unused:UNUSED_PAD src0_sel:DWORD
	v_add_f32_e32 v16, 0x41000000, v16
	v_med3_f32 v17, v17, 0, v148
	v_cvt_u32_f32_e32 v18, v18
	v_lshlrev_b32_e32 v11, 28, v11
	v_cvt_u32_f32_e32 v13, v13
	v_cvt_u32_f32_sdwa v14, v14 dst_sel:WORD_1 dst_unused:UNUSED_PAD src0_sel:DWORD
	v_med3_f32 v16, v16, 0, v148
	v_cvt_u32_f32_e32 v17, v17
	v_lshlrev_b32_e32 v10, 20, v10
	v_or3_b32 v4, v7, v4, v11
	v_cvt_u32_f32_e32 v16, v16
	v_lshlrev_b32_e32 v9, 12, v9
	v_lshlrev_b32_e32 v5, 8, v5
	v_or3_b32 v4, v4, v6, v10
	v_lshlrev_b32_e32 v8, 4, v8
	v_or3_b32 v4, v4, v5, v9
	v_lshlrev_b32_e32 v3, 28, v3
	v_bitop3_b32 v4, v4, s45, v8 bitop3:0x36
	v_lshlrev_b32_e32 v8, 20, v18
	v_or3_b32 v3, v15, v12, v3
	v_lshlrev_b32_e32 v6, 12, v17
	v_lshlrev_b32_e32 v7, 8, v13
	v_or3_b32 v3, v3, v14, v8
	v_lshlrev_b32_e32 v5, 4, v16
	v_or3_b32 v3, v3, v7, v6
	v_bitop3_b32 v5, v3, s45, v5 bitop3:0x36
	v_lshl_add_u64 v[6:7], v[130:131], 0, s[0:1]
	global_store_dwordx2 v[6:7], v[4:5], off
	s_and_saveexec_b64 s[0:1], s[2:3]
	s_cbranch_execz .LBB0_913
	s_lshl_b64 s[4:5], s[26:27], 3
	s_add_u32 s4, s34, s4
	s_addc_u32 s5, s35, s5
	global_store_dword v127, v2, s[4:5]

; template <bool SIGNED4> __device__ __forceinline__ void qrow_store(const f32x4 (&v)[4], unsigned char* q, float* scale, int row, int lane) {
;     float ss = 0.f;
; #pragma unroll
;     for (int j = 0; j < 4; ++j) ss += v[j].x * v[j].x + v[j].y * v[j].y + v[j].z * v[j].z + v[j].w * v[j].w;
;     ss = wave_sum(ss);
;     const float sc = ss > 0.f ? 0.3352f * sqrtf(ss * (1.f / 1024.f)) : 1.f, inv = __builtin_amdgcn_rcpf(sc);
;     unsigned n[16];
; #pragma unroll
;     for (int j = 0; j < 4; ++j) {
; #pragma unroll
;         for (int i = 0; i < 4; ++i) { const float f = floorf(v[j][i] * inv) + 8.f; n[4 * j + i] = (unsigned)fminf(fmaxf(f, 0.f), 15.f); } }
;     u32x2 o;
; #pragma unroll
;     for (int m = 0; m < 2; ++m) { unsigned w = 0;
; #pragma unroll
;         for (int b = 0; b < 4; ++b) w |= (n[8 * m + b] | (n[8 * m + 4 + b] << 4)) << (8 * b);
;         o[m] = SIGNED4 ? (w ^ 0x88888888u) : w; }
;     *(u32x2*)(q + (size_t)row * 1024 + lane * 16) = o;
;     if (lane == 0) scale[row] = sc;
; }
.LBB0_917:
	v_mul_f32_e32 v2, v79, v79
	v_mul_f32_e32 v3, v87, v87
	v_fmac_f32_e32 v2, v78, v78
	v_fmac_f32_e32 v3, v86, v86
	v_fmac_f32_e32 v2, v80, v80
	v_fmac_f32_e32 v3, v88, v88
	v_fmac_f32_e32 v2, v81, v81
	v_fmac_f32_e32 v3, v89, v89
	v_add_f32_e32 v2, v2, v3
	v_mul_f32_e32 v3, v91, v91
	v_fmac_f32_e32 v3, v90, v90
	v_fmac_f32_e32 v3, v92, v92
	v_fmac_f32_e32 v3, v93, v93
	v_add_f32_e32 v2, v3, v2
	v_mul_f32_e32 v3, v95, v95
	v_fmac_f32_e32 v3, v94, v94
	v_fmac_f32_e32 v3, v96, v96
	v_fmac_f32_e32 v3, v97, v97
	v_add_f32_e32 v2, v3, v2
	s_ashr_i32 s25, s24, 31
	s_lshl_b64 s[0:1], s[24:25], 10
	v_add_f32_dpp v2, v2, v2 quad_perm:[1,0,3,2] row_mask:0xf bank_mask:0xf bound_ctrl:1
	s_nop 1
	v_add_f32_dpp v2, v2, v2 quad_perm:[2,3,0,1] row_mask:0xf bank_mask:0xf bound_ctrl:1
	s_nop 1
	v_add_f32_dpp v2, v2, v2 row_ror:4 row_mask:0xf bank_mask:0xf bound_ctrl:1
	s_nop 1
	v_add_f32_dpp v2, v2, v2 row_ror:8 row_mask:0xf bank_mask:0xf bound_ctrl:1
	v_mov_b32_e32 v3, v2
	s_nop 1
	v_permlane16_swap_b32_e32 v2, v3
	v_add_f32_e32 v2, v2, v3
	v_mov_b32_e32 v3, v2
	s_nop 1
	v_permlane32_swap_b32_e32 v2, v3
	v_add_f32_e32 v2, v2, v3
	v_mul_f32_e32 v3, 0x3a800000, v2
	v_mul_f32_e32 v4, 0x4f800000, v3
	v_cmp_gt_f32_e32 vcc, s44, v3
	s_nop 1
	v_cndmask_b32_e32 v3, v3, v4, vcc
	v_sqrt_f32_e32 v4, v3
	s_nop 0
	v_add_u32_e32 v5, -1, v4
	v_fma_f32 v6, -v5, v4, v3
	v_cmp_ge_f32_e64 s[12:13], 0, v6
	v_add_u32_e32 v6, 1, v4
	s_nop 0
	v_cndmask_b32_e64 v5, v4, v5, s[12:13]
	v_fma_f32 v4, -v6, v4, v3
	v_cmp_lt_f32_e64 s[12:13], 0, v4
	s_nop 1
	v_cndmask_b32_e64 v4, v5, v6, s[12:13]
	v_mul_f32_e32 v5, 0x37800000, v4
	v_cndmask_b32_e32 v4, v4, v5, vcc
	v_cmp_class_f32_e32 vcc, v3, v147
	s_nop 1
	v_cndmask_b32_e32 v3, v4, v3, vcc
	v_mul_f32_e32 v3, 0x3eab9f56, v3
	v_cmp_lt_f32_e32 vcc, 0, v2
	s_nop 1
	v_cndmask_b32_e32 v2, 1.0, v3, vcc
	v_rcp_f32_e32 v3, v2
	s_nop 0
	v_mul_f32_e32 v11, v89, v3
	v_mul_f32_e32 v4, v78, v3
	v_mul_f32_e32 v7, v81, v3
	v_mul_f32_e32 v10, v88, v3
	v_floor_f32_e32 v11, v11
	v_floor_f32_e32 v4, v4
	v_mul_f32_e32 v5, v79, v3
	v_mul_f32_e32 v6, v80, v3
	v_floor_f32_e32 v7, v7
	v_mul_f32_e32 v9, v87, v3
	v_floor_f32_e32 v10, v10
	v_add_f32_e32 v11, 0x41000000, v11
	v_add_f32_e32 v4, 0x41000000, v4
	v_floor_f32_e32 v5, v5
	v_floor_f32_e32 v6, v6
	v_add_f32_e32 v7, 0x41000000, v7
	v_mul_f32_e32 v8, v86, v3
	v_floor_f32_e32 v9, v9
	v_add_f32_e32 v10, 0x41000000, v10
	v_med3_f32 v11, v11, 0, v148
	v_mul_f32_e32 v12, v90, v3
	v_mul_f32_e32 v13, v91, v3
	v_mul_f32_e32 v14, v92, v3
	v_mul_f32_e32 v15, v93, v3
	v_mul_f32_e32 v16, v94, v3
	v_mul_f32_e32 v17, v95, v3
	v_mul_f32_e32 v18, v96, v3
	v_mul_f32_e32 v3, v97, v3
	v_med3_f32 v4, v4, 0, v148
	v_add_f32_e32 v5, 0x41000000, v5
	v_add_f32_e32 v6, 0x41000000, v6
	v_med3_f32 v7, v7, 0, v148
	v_floor_f32_e32 v8, v8
	v_add_f32_e32 v9, 0x41000000, v9
	v_med3_f32 v10, v10, 0, v148
	v_cvt_u32_f32_e32 v11, v11
	v_floor_f32_e32 v3, v3
	v_cvt_u32_f32_e32 v4, v4
	v_med3_f32 v5, v5, 0, v148
	v_med3_f32 v6, v6, 0, v148
	v_cvt_u32_f32_sdwa v7, v7 dst_sel:BYTE_3 dst_unused:UNUSED_PAD src0_sel:DWORD
	v_add_f32_e32 v8, 0x41000000, v8
	v_med3_f32 v9, v9, 0, v148
	v_cvt_u32_f32_e32 v10, v10
	v_floor_f32_e32 v12, v12
	v_floor_f32_e32 v15, v15
	v_floor_f32_e32 v18, v18
	v_add_f32_e32 v3, 0x41000000, v3
	v_cvt_u32_f32_e32 v5, v5
	v_cvt_u32_f32_sdwa v6, v6 dst_sel:WORD_1 dst_unused:UNUSED_PAD src0_sel:DWORD
	v_med3_f32 v8, v8, 0, v148
	v_cvt_u32_f32_e32 v9, v9
	v_add_f32_e32 v12, 0x41000000, v12
	v_floor_f32_e32 v13, v13
	v_floor_f32_e32 v14, v14
	v_add_f32_e32 v15, 0x41000000, v15
	v_floor_f32_e32 v17, v17
	v_add_f32_e32 v18, 0x41000000, v18
	v_med3_f32 v3, v3, 0, v148
	v_cvt_u32_f32_e32 v8, v8
	v_med3_f32 v12, v12, 0, v148
	v_add_f32_e32 v13, 0x41000000, v13
	v_add_f32_e32 v14, 0x41000000, v14
	v_med3_f32 v15, v15, 0, v148
	v_floor_f32_e32 v16, v16
	v_add_f32_e32 v17, 0x41000000, v17
	v_med3_f32 v18, v18, 0, v148
	v_cvt_u32_f32_e32 v3, v3
	v_cvt_u32_f32_e32 v12, v12
	v_med3_f32 v13, v13, 0, v148
	v_med3_f32 v14, v14, 0, v148
	v_cvt_u32_f32_sdwa v15, v15 dst_sel:BYTE_3 dst_unused:UNUSED_PAD src0_sel:DWORD
	v_add_f32_e32 v16, 0x41000000, v16
	v_med3_f32 v17, v17, 0, v148
	v_cvt_u32_f32_e32 v18, v18
	v_lshlrev_b32_e32 v11, 28, v11
	v_cvt_u32_f32_e32 v13, v13
	v_cvt_u32_f32_sdwa v14, v14 dst_sel:WORD_1 dst_unused:UNUSED_PAD src0_sel:DWORD
	v_med3_f32 v16, v16, 0, v148
	v_cvt_u32_f32_e32 v17, v17
	v_lshlrev_b32_e32 v10, 20, v10
	v_or3_b32 v4, v7, v4, v11
	v_cvt_u32_f32_e32 v16, v16
	v_lshlrev_b32_e32 v9, 12, v9
	v_lshlrev_b32_e32 v5, 8, v5
	v_or3_b32 v4, v4, v6, v10
	v_lshlrev_b32_e32 v8, 4, v8
	v_or3_b32 v4, v4, v5, v9
	v_lshlrev_b32_e32 v3, 28, v3
	v_bitop3_b32 v4, v4, s45, v8 bitop3:0x36
	v_lshlrev_b32_e32 v8, 20, v18
	v_or3_b32 v3, v15, v12, v3
	v_lshlrev_b32_e32 v6, 12, v17
	v_lshlrev_b32_e32 v7, 8, v13
	v_or3_b32 v3, v3, v14, v8
	v_lshlrev_b32_e32 v5, 4, v16
	v_or3_b32 v3, v3, v7, v6
	v_bitop3_b32 v5, v3, s45, v5 bitop3:0x36
	v_lshl_add_u64 v[6:7], v[130:131], 0, s[0:1]
	global_store_dwordx2 v[6:7], v[4:5], off
	s_and_saveexec_b64 s[0:1], s[2:3]
	s_cbranch_execz .LBB0_919
	s_lshl_b64 s[4:5], s[24:25], 3
	s_add_u32 s4, s34, s4
	s_addc_u32 s5, s35, s5
	global_store_dword v127, v2, s[4:5]

; __device__ __forceinline__ float bf2f(bf16_t v) { return __uint_as_float(((unsigned)v) << 16); }
; #define LAS __attribute__((address_space(3)))
; __device__ __forceinline__ void route_half(float (&top)[16], LAS const unsigned char* keys_lds, const bf16_t* __restrict__ qrow, int r32, int hi) {
;     bf16x8 qf[8]; float ss = 0.f;
; #pragma unroll
;     for (int ks = 0; ks < 8; ++ks) { qf[ks] = __builtin_nontemporal_load((const bf16x8*)(qrow + 16 * ks + 8 * hi));
; #pragma unroll
;         for (int j = 0; j < 8; ++j) { const float f = bf2f((bf16_t)qf[ks][j]); ss += f * f; } }
;     ss += __shfl_xor(ss, 32);
;     const float rn = rsqrtf(ss * (1.f / 128.f) + EPS);
;     f32x16 acc[4];
; #pragma unroll
;     for (int kt = 0; kt < 4; ++kt) {
; #pragma unroll
;         for (int r = 0; r < 16; ++r) acc[kt][r] = 0.f;
; #pragma unroll
;         for (int ks = 0; ks < 8; ++ks) { const bf16x8 kf = *(LAS const bf16x8*)(keys_lds + (32 * kt + r32) * RT_KROW + (16 * ks + 8 * hi) * 2);
;             acc[kt] = __builtin_amdgcn_mfma_f32_32x32x16_bf16(kf, qf[ks], acc[kt], 0, 0, 0); }
;         __builtin_amdgcn_sched_barrier(0);
;     }
.LBB0_922:
	global_load_dwordx4 v[18:21], v[140:141], off offset:256 nt
	global_load_dwordx4 v[98:101], v[140:141], off offset:288 nt
	global_load_dwordx4 v[102:105], v[140:141], off offset:320 nt
	global_load_dwordx4 v[106:109], v[140:141], off offset:352 nt
	global_load_dwordx4 v[110:113], v[140:141], off offset:384 nt
	global_load_dwordx4 v[114:117], v[140:141], off offset:416 nt
	global_load_dwordx4 v[118:121], v[140:141], off offset:448 nt
	global_load_dwordx4 v[122:125], v[140:141], off offset:480 nt
	ds_read_b128 v[2:5], v143 offset:34816
	ds_read_b128 v[22:25], v143 offset:34848
	ds_read_b128 v[26:29], v143 offset:34880
	ds_read_b128 v[30:33], v143 offset:34912
	ds_read_b128 v[34:37], v143 offset:34944
	s_waitcnt vmcnt(7) lgkmcnt(4)
	v_mfma_f32_32x32x16_bf16 v[2:17], v[2:5], v[18:21], 0
	v_and_b32_e32 v46, 0xffff0000, v18
	v_lshlrev_b32_e32 v44, 16, v18
	v_mul_f32_e32 v46, v46, v46
	v_lshlrev_b32_e32 v47, 16, v19
	v_fmac_f32_e32 v46, v44, v44
	v_and_b32_e32 v48, 0xffff0000, v19
	v_fmac_f32_e32 v46, v47, v47
	v_lshlrev_b32_e32 v49, 16, v20
	v_fmac_f32_e32 v46, v48, v48
	v_and_b32_e32 v50, 0xffff0000, v20
	v_fmac_f32_e32 v46, v49, v49
	v_lshlrev_b32_e32 v51, 16, v21
	v_fmac_f32_e32 v46, v50, v50
	v_and_b32_e32 v52, 0xffff0000, v21
	v_fmac_f32_e32 v46, v51, v51
	s_waitcnt vmcnt(6)
	v_lshlrev_b32_e32 v53, 16, v98
	v_fmac_f32_e32 v46, v52, v52
	v_and_b32_e32 v54, 0xffff0000, v98
	v_fmac_f32_e32 v46, v53, v53
	v_lshlrev_b32_e32 v55, 16, v99
	v_fmac_f32_e32 v46, v54, v54
	v_and_b32_e32 v56, 0xffff0000, v99
	v_fmac_f32_e32 v46, v55, v55
	v_lshlrev_b32_e32 v57, 16, v100
	v_fmac_f32_e32 v46, v56, v56
	v_and_b32_e32 v58, 0xffff0000, v100
	v_fmac_f32_e32 v46, v57, v57
	v_lshlrev_b32_e32 v59, 16, v101
	v_fmac_f32_e32 v46, v58, v58
	v_and_b32_e32 v60, 0xffff0000, v101
	v_fmac_f32_e32 v46, v59, v59
	s_waitcnt vmcnt(5)
	v_lshlrev_b32_e32 v61, 16, v102
	v_fmac_f32_e32 v46, v60, v60
	v_and_b32_e32 v62, 0xffff0000, v102
	v_fmac_f32_e32 v46, v61, v61
	v_lshlrev_b32_e32 v63, 16, v103
	v_fmac_f32_e32 v46, v62, v62
	v_and_b32_e32 v64, 0xffff0000, v103
	v_fmac_f32_e32 v46, v63, v63
	v_lshlrev_b32_e32 v65, 16, v104
	v_fmac_f32_e32 v46, v64, v64
	v_and_b32_e32 v140, 0xffff0000, v104
	v_fmac_f32_e32 v46, v65, v65
	v_lshlrev_b32_e32 v141, 16, v105
	v_fmac_f32_e32 v46, v140, v140
	v_and_b32_e32 v181, 0xffff0000, v105
	v_fmac_f32_e32 v46, v141, v141
	s_waitcnt vmcnt(4)
	v_lshlrev_b32_e32 v182, 16, v106
	v_fmac_f32_e32 v46, v181, v181
	v_and_b32_e32 v183, 0xffff0000, v106
	v_fmac_f32_e32 v46, v182, v182
	v_lshlrev_b32_e32 v184, 16, v107
	v_fmac_f32_e32 v46, v183, v183
	v_and_b32_e32 v185, 0xffff0000, v107
	v_fmac_f32_e32 v46, v184, v184
	v_lshlrev_b32_e32 v186, 16, v108
	v_fmac_f32_e32 v46, v185, v185
	v_and_b32_e32 v187, 0xffff0000, v108
	v_fmac_f32_e32 v46, v186, v186
	v_lshlrev_b32_e32 v188, 16, v109
	v_fmac_f32_e32 v46, v187, v187
	v_and_b32_e32 v189, 0xffff0000, v109
	v_fmac_f32_e32 v46, v188, v188
	s_waitcnt vmcnt(3)
	v_lshlrev_b32_e32 v190, 16, v110
	v_fmac_f32_e32 v46, v189, v189
	v_and_b32_e32 v191, 0xffff0000, v110
	v_fmac_f32_e32 v46, v190, v190
	v_lshlrev_b32_e32 v192, 16, v111
	v_fmac_f32_e32 v46, v191, v191
	v_and_b32_e32 v193, 0xffff0000, v111
	v_fmac_f32_e32 v46, v192, v192
	v_lshlrev_b32_e32 v194, 16, v112
	v_fmac_f32_e32 v46, v193, v193
	v_and_b32_e32 v195, 0xffff0000, v112
	v_fmac_f32_e32 v46, v194, v194
	v_lshlrev_b32_e32 v196, 16, v113
	v_fmac_f32_e32 v46, v195, v195
	v_and_b32_e32 v197, 0xffff0000, v113
	v_fmac_f32_e32 v46, v196, v196
	s_waitcnt vmcnt(2)
	v_lshlrev_b32_e32 v198, 16, v114
	s_waitcnt lgkmcnt(3)
	v_mfma_f32_32x32x16_bf16 v[2:17], v[22:25], v[98:101], v[2:17]
	v_fmac_f32_e32 v46, v197, v197
	v_and_b32_e32 v199, 0xffff0000, v114
	v_fmac_f32_e32 v46, v198, v198
	v_lshlrev_b32_e32 v200, 16, v115
	v_fmac_f32_e32 v46, v199, v199
	v_and_b32_e32 v201, 0xffff0000, v115
	v_fmac_f32_e32 v46, v200, v200
	v_lshlrev_b32_e32 v202, 16, v116
	v_fmac_f32_e32 v46, v201, v201
	v_and_b32_e32 v203, 0xffff0000, v116
	v_fmac_f32_e32 v46, v202, v202
	v_lshlrev_b32_e32 v204, 16, v117
	v_fmac_f32_e32 v46, v203, v203
	v_and_b32_e32 v205, 0xffff0000, v117
	v_fmac_f32_e32 v46, v204, v204
	s_waitcnt vmcnt(1)
	v_lshlrev_b32_e32 v206, 16, v118
	s_waitcnt lgkmcnt(2)
	v_mfma_f32_32x32x16_bf16 v[2:17], v[26:29], v[102:105], v[2:17]
	v_fmac_f32_e32 v46, v205, v205
	v_and_b32_e32 v207, 0xffff0000, v118
	v_fmac_f32_e32 v46, v206, v206
	v_lshlrev_b32_e32 v208, 16, v119
	v_fmac_f32_e32 v46, v207, v207
	v_and_b32_e32 v209, 0xffff0000, v119
	v_fmac_f32_e32 v46, v208, v208
	v_lshlrev_b32_e32 v210, 16, v120
	v_fmac_f32_e32 v46, v209, v209
	v_and_b32_e32 v211, 0xffff0000, v120
	v_and_b32_e32 v39, 0xffff0000, v121
	v_lshlrev_b32_e32 v38, 16, v121
	v_fmac_f32_e32 v46, v210, v210
	v_pk_mul_f32 v[38:39], v[38:39], v[38:39]
	v_fmac_f32_e32 v46, v211, v211
	s_waitcnt vmcnt(0)
	v_and_b32_e32 v41, 0xffff0000, v122
	v_lshlrev_b32_e32 v40, 16, v122
	v_add_f32_e32 v22, v38, v46
	v_pk_mul_f32 v[40:41], v[40:41], v[40:41]
	s_waitcnt lgkmcnt(1)
	v_mfma_f32_32x32x16_bf16 v[2:17], v[30:33], v[106:109], v[2:17]
	v_add_f32_e32 v22, v39, v22
	v_and_b32_e32 v43, 0xffff0000, v123
	v_lshlrev_b32_e32 v42, 16, v123
	v_add_f32_e32 v22, v40, v22
	v_mul_f32_e64 v42, v42, v42
	v_mul_f32_e64 v43, v43, v43
	v_add_f32_e32 v22, v41, v22
	v_and_b32_e32 v45, 0xffff0000, v124
	v_add_f32_e32 v22, v42, v22
	v_lshlrev_b32_e32 v44, 16, v124
	v_add_f32_e32 v22, v43, v22
	v_pk_mul_f32 v[26:27], v[44:45], v[44:45]
	s_waitcnt lgkmcnt(0)
; #define LAS __attribute__((address_space(3)))
; __device__ __forceinline__ void route_half(float (&top)[16], LAS const unsigned char* keys_lds, const bf16_t* __restrict__ qrow, int r32, int hi) {
;     ...
;     ss += __shfl_xor(ss, 32);
;     const float rn = rsqrtf(ss * (1.f / 128.f) + EPS);
;     f32x16 acc[4];
; #pragma unroll
;     for (int kt = 0; kt < 4; ++kt) {
; #pragma unroll
;         for (int r = 0; r < 16; ++r) acc[kt][r] = 0.f;
; #pragma unroll
;         for (int ks = 0; ks < 8; ++ks) { const bf16x8 kf = *(LAS const bf16x8*)(keys_lds + (32 * kt + r32) * RT_KROW + (16 * ks + 8 * hi) * 2);
;             acc[kt] = __builtin_amdgcn_mfma_f32_32x32x16_bf16(kf, qf[ks], acc[kt], 0, 0, 0); }
;         __builtin_amdgcn_sched_barrier(0);
;     }
;     const unsigned hi4 = (unsigned)hi << 2;
;     float g[4][16];
; #pragma unroll
;     for (int kt = 0; kt < 4; ++kt)
; #pragma unroll
;         for (int r = 0; r < 16; ++r) { const unsigned base = (unsigned)(32 * kt + (r & 3) + 8 * (r >> 2)); g[kt][r] = __uint_as_float((__float_as_uint(acc[kt][r] * rn) & 0xFFFFFF80u) | base); }
	v_mfma_f32_32x32x16_bf16 v[2:17], v[34:37], v[110:113], v[2:17]
	v_add_f32_e32 v26, v26, v22
	v_add_f32_e32 v28, v27, v26
	v_and_b32_e32 v27, 0xffff0000, v125
	v_lshlrev_b32_e32 v26, 16, v125
	ds_read_b128 v[22:25], v143 offset:34976
	v_pk_mul_f32 v[26:27], v[26:27], v[26:27]
	s_nop 0
	v_add_f32_e32 v26, v26, v28
	v_add_f32_e32 v26, v27, v26
	ds_bpermute_b32 v27, v142, v26
	s_waitcnt lgkmcnt(0)
	v_add_f32_e32 v26, v26, v27
	v_fmamk_f32 v30, v26, 0x3c000000, v146
	ds_read_b128 v[26:29], v143 offset:35040
	v_mfma_f32_32x32x16_bf16 v[2:17], v[22:25], v[114:117], v[2:17]
	ds_read_b128 v[22:25], v143 offset:35008
	v_mul_f32_e32 v31, 0x4b800000, v30
	v_cmp_gt_f32_e32 vcc, s40, v30
	s_waitcnt lgkmcnt(0)
	v_mfma_f32_32x32x16_bf16 v[2:17], v[22:25], v[118:121], v[2:17]
	v_cndmask_b32_e32 v22, v30, v31, vcc
	v_rsq_f32_e32 v140, v22
	s_nop 0
	v_mul_f32_e32 v141, 0x45800000, v140
	v_mfma_f32_32x32x16_bf16 v[2:17], v[26:29], v[122:125], v[2:17]
	ds_read_b128 v[22:25], v143 offset:43520
	ds_read_b128 v[26:29], v143 offset:43552
	s_waitcnt lgkmcnt(1)
	v_mfma_f32_32x32x16_bf16 v[50:65], v[22:25], v[18:21], 0
	s_waitcnt lgkmcnt(0)
	v_mfma_f32_32x32x16_bf16 v[50:65], v[26:29], v[98:101], v[50:65]
	ds_read_b128 v[22:25], v143 offset:43584
	ds_read_b128 v[26:29], v143 offset:43616
	s_waitcnt lgkmcnt(1)
	v_mfma_f32_32x32x16_bf16 v[50:65], v[22:25], v[102:105], v[50:65]
	s_waitcnt lgkmcnt(0)
	v_mfma_f32_32x32x16_bf16 v[50:65], v[26:29], v[106:109], v[50:65]
	ds_read_b128 v[22:25], v143 offset:43648
	ds_read_b128 v[26:29], v143 offset:43680
	s_waitcnt lgkmcnt(1)
	v_mfma_f32_32x32x16_bf16 v[50:65], v[22:25], v[110:113], v[50:65]
	s_waitcnt lgkmcnt(0)
	v_mfma_f32_32x32x16_bf16 v[50:65], v[26:29], v[114:117], v[50:65]
	ds_read_b128 v[22:25], v143 offset:43712
	ds_read_b128 v[26:29], v143 offset:43744
	s_waitcnt lgkmcnt(1)
	v_mfma_f32_32x32x16_bf16 v[50:65], v[22:25], v[118:121], v[50:65]
	s_waitcnt lgkmcnt(0)
	v_mfma_f32_32x32x16_bf16 v[50:65], v[26:29], v[122:125], v[50:65]
	ds_read_b128 v[22:25], v143 offset:52224
	ds_read_b128 v[26:29], v143 offset:52256
	s_waitcnt lgkmcnt(1)
	v_mfma_f32_32x32x16_bf16 v[34:49], v[22:25], v[18:21], 0
	s_waitcnt lgkmcnt(0)
	v_mfma_f32_32x32x16_bf16 v[34:49], v[26:29], v[98:101], v[34:49]
	ds_read_b128 v[22:25], v143 offset:52288
	ds_read_b128 v[26:29], v143 offset:52320
	s_waitcnt lgkmcnt(1)
	v_mfma_f32_32x32x16_bf16 v[34:49], v[22:25], v[102:105], v[34:49]
	s_waitcnt lgkmcnt(0)
	v_mfma_f32_32x32x16_bf16 v[34:49], v[26:29], v[106:109], v[34:49]
	ds_read_b128 v[22:25], v143 offset:52352
	ds_read_b128 v[26:29], v143 offset:52384
	s_waitcnt lgkmcnt(1)
	v_mfma_f32_32x32x16_bf16 v[34:49], v[22:25], v[110:113], v[34:49]
	s_waitcnt lgkmcnt(0)
	v_mfma_f32_32x32x16_bf16 v[34:49], v[26:29], v[114:117], v[34:49]
	ds_read_b128 v[22:25], v143 offset:52416
	ds_read_b128 v[26:29], v143 offset:52448
	s_waitcnt lgkmcnt(1)
	v_mfma_f32_32x32x16_bf16 v[34:49], v[22:25], v[118:121], v[34:49]
	s_waitcnt lgkmcnt(0)
	v_mfma_f32_32x32x16_bf16 v[34:49], v[26:29], v[122:125], v[34:49]
	ds_read_b128 v[22:25], v143 offset:60928
	ds_read_b128 v[182:185], v143 offset:60960
	s_waitcnt lgkmcnt(1)
	v_mfma_f32_32x32x16_bf16 v[18:33], v[22:25], v[18:21], 0
	s_waitcnt lgkmcnt(0)
	v_mfma_f32_32x32x16_bf16 v[18:33], v[182:185], v[98:101], v[18:33]
	ds_read_b128 v[98:101], v143 offset:60992
	ds_read_b128 v[182:185], v143 offset:61024
	s_waitcnt lgkmcnt(1)
	v_mfma_f32_32x32x16_bf16 v[18:33], v[98:101], v[102:105], v[18:33]
	ds_read_b128 v[98:101], v143 offset:61056
	ds_read_b128 v[102:105], v143 offset:61088
	s_waitcnt lgkmcnt(2)
	v_mfma_f32_32x32x16_bf16 v[18:33], v[182:185], v[106:109], v[18:33]
	s_waitcnt lgkmcnt(1)
	v_mfma_f32_32x32x16_bf16 v[18:33], v[98:101], v[110:113], v[18:33]
	s_waitcnt lgkmcnt(0)
	v_mfma_f32_32x32x16_bf16 v[18:33], v[102:105], v[114:117], v[18:33]
	ds_read_b128 v[98:101], v143 offset:61120
	ds_read_b128 v[102:105], v143 offset:61152
	s_waitcnt lgkmcnt(1)
	v_mfma_f32_32x32x16_bf16 v[18:33], v[98:101], v[118:121], v[18:33]
	s_waitcnt lgkmcnt(0)
	v_mfma_f32_32x32x16_bf16 v[18:33], v[102:105], v[122:125], v[18:33]
	v_cndmask_b32_e32 v98, v140, v141, vcc
	v_mul_f32_e32 v2, v2, v98
	v_and_b32_e32 v99, 0xffffff80, v2
	v_mul_f32_e32 v2, v3, v98
	v_and_or_b32 v100, v2, s41, 1
	v_mul_f32_e32 v2, v4, v98
	v_and_or_b32 v101, v2, s41, 2
	v_mul_f32_e32 v2, v5, v98
	v_and_or_b32 v102, v2, s41, 3
	v_mul_f32_e32 v2, v6, v98
	v_and_or_b32 v103, v2, s41, 8
	v_mul_f32_e32 v2, v7, v98
	v_and_or_b32 v104, v2, s41, 9
	v_mul_f32_e32 v2, v8, v98
	v_and_or_b32 v105, v2, s41, 10
	v_mul_f32_e32 v2, v9, v98
	v_and_or_b32 v106, v2, s41, 11
	v_mul_f32_e32 v2, v10, v98
	v_and_or_b32 v107, v2, s41, 16
	v_mul_f32_e32 v2, v11, v98
	v_and_or_b32 v108, v2, s41, 17
	v_mul_f32_e32 v2, v12, v98
	v_and_or_b32 v109, v2, s41, 18
	v_mul_f32_e32 v2, v13, v98
	v_and_or_b32 v110, v2, s41, 19
	v_mul_f32_e32 v2, v14, v98
	v_and_or_b32 v111, v2, s41, 24
	v_mul_f32_e32 v2, v15, v98
	v_and_or_b32 v112, v2, s41, 25
	v_mul_f32_e32 v2, v16, v98
	v_and_or_b32 v113, v2, s41, 26
	v_mul_f32_e32 v2, v17, v98
	v_and_or_b32 v114, v2, s41, 27
	v_mul_f32_e32 v2, v50, v98
	v_and_or_b32 v50, v2, s41, 32
	v_mul_f32_e32 v2, v51, v98
	v_and_or_b32 v51, v2, s41, 33
	v_mul_f32_e32 v2, v52, v98
	v_and_or_b32 v52, v2, s41, 34
	v_mul_f32_e32 v2, v53, v98
	v_and_or_b32 v53, v2, s41, 35
	v_mul_f32_e32 v2, v54, v98
	v_and_or_b32 v54, v2, s41, 40
	v_mul_f32_e32 v2, v55, v98
	v_and_or_b32 v55, v2, s41, 41
	v_mul_f32_e32 v2, v56, v98
	v_and_or_b32 v56, v2, s41, 42
	v_mul_f32_e32 v2, v57, v98
	v_and_or_b32 v57, v2, s41, 43
	v_mul_f32_e32 v2, v58, v98
	v_and_or_b32 v58, v2, s41, 48
	v_mul_f32_e32 v2, v59, v98
; #define CE_DESC(a, b) do { const float _t = fmaxf(a, b); b = fminf(a, b); a = _t; } while (0)
; __device__ __forceinline__ void sort16_desc(float (&v)[16]) {
; #pragma unroll
;     for (int k = 2; k <= 16; k <<= 1)
; #pragma unroll
;         for (int j = k >> 1; j > 0; j >>= 1)
; #pragma unroll
;             for (int i = 0; i < 16; ++i) { const int l = i ^ j; if (l > i) { if ((i & k) == 0 || k == 16) CE_DESC(v[i], v[l]); else CE_DESC(v[l], v[i]); } }
; }
; __device__ __forceinline__ void route_half(float (&top)[16], LAS const unsigned char* keys_lds, const bf16_t* __restrict__ qrow, int r32, int hi) {
;     ...
;         for (int r = 0; r < 16; ++r) { const unsigned base = (unsigned)(32 * kt + (r & 3) + 8 * (r >> 2)); g[kt][r] = __uint_as_float((__float_as_uint(acc[kt][r] * rn) & 0xFFFFFF80u) | base); }
; #pragma unroll
;     for (int kt = 0; kt < 4; ++kt) sort16_desc(g[kt]);
	v_and_or_b32 v59, v2, s41, 49
	v_mul_f32_e32 v2, v60, v98
	v_and_or_b32 v60, v2, s41, 50
	v_mul_f32_e32 v2, v61, v98
	v_and_or_b32 v61, v2, s41, 51
	v_mul_f32_e32 v2, v62, v98
	v_and_or_b32 v62, v2, s41, 56
	v_mul_f32_e32 v2, v63, v98
	v_and_or_b32 v63, v2, s41, 57
	v_mul_f32_e32 v2, v64, v98
	v_and_or_b32 v64, v2, s41, 58
	v_mul_f32_e32 v2, v65, v98
	v_and_or_b32 v65, v2, s41, 59
	v_mul_f32_e32 v2, v34, v98
	v_and_or_b32 v115, v2, s41, 64
	v_mul_f32_e32 v2, v35, v98
	v_and_b32_e32 v2, 0xffffff80, v2
	v_or_b32_e32 v116, 0x41, v2
	v_mul_f32_e32 v2, v36, v98
	v_and_b32_e32 v2, 0xffffff80, v2
	v_or_b32_e32 v117, 0x42, v2
	v_mul_f32_e32 v2, v37, v98
	v_and_b32_e32 v2, 0xffffff80, v2
	v_or_b32_e32 v118, 0x43, v2
	v_mul_f32_e32 v2, v38, v98
	v_and_b32_e32 v2, 0xffffff80, v2
	v_or_b32_e32 v119, 0x48, v2
	v_mul_f32_e32 v2, v39, v98
	v_and_b32_e32 v2, 0xffffff80, v2
	v_or_b32_e32 v120, 0x49, v2
	v_mul_f32_e32 v2, v40, v98
	v_and_b32_e32 v2, 0xffffff80, v2
	v_or_b32_e32 v121, 0x4a, v2
	v_mul_f32_e32 v2, v41, v98
	v_and_b32_e32 v2, 0xffffff80, v2
	v_or_b32_e32 v122, 0x4b, v2
	v_mul_f32_e32 v2, v42, v98
	v_and_b32_e32 v2, 0xffffff80, v2
	v_or_b32_e32 v42, 0x50, v2
	v_mul_f32_e32 v2, v43, v98
	v_and_b32_e32 v2, 0xffffff80, v2
	v_or_b32_e32 v43, 0x51, v2
	v_mul_f32_e32 v2, v44, v98
	v_and_b32_e32 v2, 0xffffff80, v2
	v_or_b32_e32 v44, 0x52, v2
	v_mul_f32_e32 v2, v45, v98
	v_and_b32_e32 v2, 0xffffff80, v2
	v_or_b32_e32 v45, 0x53, v2
	v_mul_f32_e32 v2, v46, v98
	v_and_b32_e32 v2, 0xffffff80, v2
	v_or_b32_e32 v46, 0x58, v2
	v_mul_f32_e32 v2, v47, v98
	v_and_b32_e32 v2, 0xffffff80, v2
	v_or_b32_e32 v47, 0x59, v2
	v_mul_f32_e32 v2, v48, v98
	v_and_b32_e32 v2, 0xffffff80, v2
	v_or_b32_e32 v48, 0x5a, v2
	v_mul_f32_e32 v2, v49, v98
	v_and_b32_e32 v2, 0xffffff80, v2
	v_mul_f32_e32 v3, v98, v19
	v_or_b32_e32 v49, 0x5b, v2
	v_mul_f32_e32 v2, v98, v18
	v_and_b32_e32 v3, 0xffffff80, v3
	v_mul_f32_e32 v5, v98, v21
	v_max_f32_e32 v18, v100, v100
	v_max_f32_e32 v19, v99, v99
	v_or_b32_e32 v4, 0x61, v3
	v_mul_f32_e32 v3, v98, v20
	v_and_b32_e32 v5, 0xffffff80, v5
	v_mul_f32_e32 v7, v98, v23
	v_max_f32_e32 v20, v19, v18
	v_min_f32_e32 v18, v19, v18
	v_max_f32_e32 v19, v101, v101
	v_max_f32_e32 v21, v102, v102
	v_or_b32_e32 v6, 0x63, v5
	v_mul_f32_e32 v5, v98, v22
	v_and_b32_e32 v7, 0xffffff80, v7
	v_mul_f32_e32 v9, v98, v25
	v_max_f32_e32 v22, v21, v19
	v_min_f32_e32 v19, v21, v19
	v_max_f32_e32 v21, v104, v104
	v_max_f32_e32 v23, v103, v103
	v_or_b32_e32 v8, 0x69, v7
	v_mul_f32_e32 v7, v98, v24
	v_and_b32_e32 v9, 0xffffff80, v9
	v_mul_f32_e32 v11, v98, v27
	v_max_f32_e32 v24, v23, v21
	v_min_f32_e32 v21, v23, v21
	v_max_f32_e32 v23, v105, v105
	v_max_f32_e32 v25, v106, v106
	v_and_b32_e32 v2, 0xffffff80, v2
	v_or_b32_e32 v10, 0x6b, v9
	v_mul_f32_e32 v9, v98, v26
	v_and_b32_e32 v11, 0xffffff80, v11
	v_mul_f32_e32 v13, v98, v29
	v_max_f32_e32 v26, v25, v23
	v_min_f32_e32 v23, v25, v23
	v_max_f32_e32 v25, v108, v108
	v_max_f32_e32 v27, v107, v107
	v_or_b32_e32 v2, 0x60, v2
	v_and_b32_e32 v3, 0xffffff80, v3
	v_or_b32_e32 v12, 0x71, v11
	v_mul_f32_e32 v11, v98, v28
	v_and_b32_e32 v13, 0xffffff80, v13
	v_mul_f32_e32 v15, v98, v31
	v_max_f32_e32 v28, v27, v25
	v_min_f32_e32 v25, v27, v25
	v_max_f32_e32 v27, v109, v109
	v_max_f32_e32 v29, v110, v110
	v_or_b32_e32 v3, 0x62, v3
	v_and_b32_e32 v5, 0xffffff80, v5
	v_or_b32_e32 v14, 0x73, v13
	v_mul_f32_e32 v13, v98, v30
	v_and_b32_e32 v15, 0xffffff80, v15
	v_max_f32_e32 v30, v29, v27
	v_min_f32_e32 v27, v29, v27
	v_max_f32_e32 v29, v112, v112
	v_max_f32_e32 v31, v111, v111
	v_max_f32_e32 v51, v51, v51
	v_max_f32_e32 v50, v50, v50
	v_max_f32_e32 v4, v4, v4
	v_max_f32_e32 v2, v2, v2
	v_or_b32_e32 v5, 0x68, v5
	v_and_b32_e32 v7, 0xffffff80, v7
	v_or_b32_e32 v16, 0x79, v15
	v_mul_f32_e32 v15, v98, v32
	v_mul_f32_e32 v17, v98, v33
	v_max_f32_e32 v32, v31, v29
	v_min_f32_e32 v29, v31, v29
	v_max_f32_e32 v31, v113, v113
	v_max_f32_e32 v98, v50, v51
	v_min_f32_e32 v50, v50, v51
	v_max_f32_e32 v51, v52, v52
	v_max_f32_e32 v52, v53, v53
	v_max_f32_e32 v106, v115, v115
	v_max_f32_e32 v107, v116, v116
	v_max_f32_e32 v113, v122, v122
	v_max_f32_e32 v122, v2, v4
	v_min_f32_e32 v2, v2, v4
	v_max_f32_e32 v3, v3, v3
	v_max_f32_e32 v4, v6, v6
	v_or_b32_e32 v7, 0x6a, v7
	v_and_b32_e32 v9, 0xffffff80, v9
	v_max_f32_e32 v53, v52, v51
	v_min_f32_e32 v51, v52, v51
	v_max_f32_e32 v52, v55, v55
	v_max_f32_e32 v54, v54, v54
	v_max_f32_e32 v108, v106, v107
	v_min_f32_e32 v106, v106, v107
	v_max_f32_e32 v107, v117, v117
	v_max_f32_e32 v109, v118, v118
	v_max_f32_e32 v6, v4, v3
	v_min_f32_e32 v3, v4, v3
	v_max_f32_e32 v4, v8, v8
	v_max_f32_e32 v5, v5, v5
	v_or_b32_e32 v9, 0x70, v9
	v_and_b32_e32 v11, 0xffffff80, v11
	v_max_f32_e32 v55, v54, v52
	v_min_f32_e32 v52, v54, v52
	v_max_f32_e32 v54, v56, v56
	v_max_f32_e32 v56, v57, v57
	v_max_f32_e32 v110, v109, v107
	v_min_f32_e32 v107, v109, v107
	v_max_f32_e32 v109, v120, v120
	v_max_f32_e32 v111, v119, v119
	v_max_f32_e32 v8, v5, v4
	v_min_f32_e32 v4, v5, v4
	v_max_f32_e32 v5, v7, v7
	v_max_f32_e32 v7, v10, v10
	v_or_b32_e32 v11, 0x72, v11
	v_and_b32_e32 v13, 0xffffff80, v13
	v_max_f32_e32 v57, v56, v54
	v_min_f32_e32 v54, v56, v54
	v_max_f32_e32 v56, v59, v59
	v_max_f32_e32 v58, v58, v58
	v_max_f32_e32 v112, v111, v109
	v_min_f32_e32 v109, v111, v109
	v_max_f32_e32 v111, v121, v121
	v_max_f32_e32 v43, v43, v43
	v_max_f32_e32 v42, v42, v42
	v_max_f32_e32 v10, v7, v5
	v_min_f32_e32 v5, v7, v5
	v_max_f32_e32 v7, v12, v12
	v_max_f32_e32 v9, v9, v9
	v_or_b32_e32 v13, 0x78, v13
	v_and_b32_e32 v15, 0xffffff80, v15
	v_and_b32_e32 v17, 0xffffff80, v17
	v_max_f32_e32 v33, v114, v114
	v_max_f32_e32 v59, v58, v56
; #define CE_DESC(a, b) do { const float _t = fmaxf(a, b); b = fminf(a, b); a = _t; } while (0)
; __device__ __forceinline__ void sort16_desc(float (&v)[16]) {
; #pragma unroll
;     for (int k = 2; k <= 16; k <<= 1)
; #pragma unroll
;         for (int j = k >> 1; j > 0; j >>= 1)
; #pragma unroll
;             for (int i = 0; i < 16; ++i) { const int l = i ^ j; if (l > i) { if ((i & k) == 0 || k == 16) CE_DESC(v[i], v[l]); else CE_DESC(v[l], v[i]); } }
; }
	v_min_f32_e32 v56, v58, v56
	v_max_f32_e32 v58, v60, v60
	v_max_f32_e32 v60, v61, v61
	v_max_f32_e32 v114, v113, v111
	v_min_f32_e32 v111, v113, v111
	v_max_f32_e32 v113, v42, v43
	v_min_f32_e32 v42, v42, v43
	v_max_f32_e32 v43, v44, v44
	v_max_f32_e32 v44, v45, v45
	v_max_f32_e32 v12, v9, v7
	v_min_f32_e32 v7, v9, v7
	v_max_f32_e32 v9, v11, v11
	v_max_f32_e32 v11, v14, v14
	v_or_b32_e32 v15, 0x7a, v15
	v_or_b32_e32 v17, 0x7b, v17
	v_max_f32_e32 v61, v60, v58
	v_min_f32_e32 v58, v60, v58
	v_max_f32_e32 v60, v63, v63
	v_max_f32_e32 v62, v62, v62
	v_max_f32_e32 v45, v44, v43
	v_min_f32_e32 v43, v44, v43
	v_max_f32_e32 v44, v47, v47
	v_max_f32_e32 v46, v46, v46
	v_max_f32_e32 v14, v11, v9
	v_min_f32_e32 v9, v11, v9
	v_max_f32_e32 v11, v16, v16
	v_max_f32_e32 v13, v13, v13
	v_max_f32_e32 v63, v62, v60
	v_min_f32_e32 v60, v62, v60
	v_max_f32_e32 v62, v64, v64
	v_max_f32_e32 v64, v65, v65
	v_max_f32_e32 v47, v46, v44
	v_min_f32_e32 v44, v46, v44
	v_max_f32_e32 v46, v48, v48
	v_max_f32_e32 v48, v49, v49
	v_max_f32_e32 v16, v13, v11
	v_min_f32_e32 v11, v13, v11
	v_max_f32_e32 v13, v15, v15
	v_max_f32_e32 v15, v17, v17
	v_max_f32_e32 v34, v33, v31
	v_min_f32_e32 v31, v33, v31
	v_max_f32_e32 v65, v64, v62
	v_min_f32_e32 v62, v64, v62
	v_max_f32_e32 v49, v48, v46
	v_min_f32_e32 v46, v48, v46
	v_max_f32_e32 v17, v15, v13
	v_min_f32_e32 v13, v15, v13
	v_max_f32_e32 v33, v20, v19
	v_min_f32_e32 v19, v20, v19
	v_max_f32_e32 v20, v18, v22
	v_min_f32_e32 v18, v18, v22
	v_max_f32_e32 v22, v23, v24
	v_min_f32_e32 v23, v23, v24
	v_max_f32_e32 v24, v26, v21
	v_min_f32_e32 v21, v26, v21
	v_max_f32_e32 v26, v28, v27
	v_min_f32_e32 v27, v28, v27
	v_max_f32_e32 v28, v25, v30
	v_min_f32_e32 v25, v25, v30
	v_max_f32_e32 v30, v31, v32
	v_min_f32_e32 v31, v31, v32
	v_max_f32_e32 v32, v34, v29
	v_min_f32_e32 v29, v34, v29
	v_max_f32_e32 v64, v98, v51
	v_min_f32_e32 v51, v98, v51
	v_max_f32_e32 v98, v50, v53
	v_min_f32_e32 v50, v50, v53
	v_max_f32_e32 v53, v54, v55
	v_min_f32_e32 v54, v54, v55
	v_max_f32_e32 v55, v57, v52
	v_min_f32_e32 v52, v57, v52
	v_max_f32_e32 v57, v59, v58
	v_min_f32_e32 v58, v59, v58
	v_max_f32_e32 v59, v56, v61
	v_min_f32_e32 v56, v56, v61
	v_max_f32_e32 v61, v62, v63
	v_min_f32_e32 v62, v62, v63
	v_max_f32_e32 v63, v65, v60
	v_min_f32_e32 v60, v65, v60
	v_max_f32_e32 v48, v108, v107
	v_min_f32_e32 v107, v108, v107
	v_max_f32_e32 v108, v106, v110
	v_min_f32_e32 v106, v106, v110
	v_max_f32_e32 v110, v111, v112
	v_min_f32_e32 v111, v111, v112
	v_max_f32_e32 v112, v114, v109
	v_min_f32_e32 v109, v114, v109
	v_max_f32_e32 v114, v113, v43
	v_min_f32_e32 v43, v113, v43
	v_max_f32_e32 v113, v42, v45
	v_min_f32_e32 v42, v42, v45
	v_max_f32_e32 v45, v46, v47
	v_min_f32_e32 v46, v46, v47
	v_max_f32_e32 v47, v49, v44
	v_min_f32_e32 v44, v49, v44
	v_max_f32_e32 v15, v122, v3
	v_min_f32_e32 v3, v122, v3
	v_max_f32_e32 v122, v2, v6
	v_min_f32_e32 v2, v2, v6
	v_max_f32_e32 v6, v5, v8
	v_min_f32_e32 v5, v5, v8
	v_max_f32_e32 v8, v10, v4
	v_min_f32_e32 v4, v10, v4
	v_max_f32_e32 v10, v12, v9
	v_min_f32_e32 v9, v12, v9
	v_max_f32_e32 v12, v7, v14
	v_min_f32_e32 v7, v7, v14
	v_max_f32_e32 v14, v13, v16
	v_min_f32_e32 v13, v13, v16
	v_max_f32_e32 v16, v17, v11
	v_min_f32_e32 v11, v17, v11
	v_max_f32_e32 v34, v33, v20
	v_min_f32_e32 v20, v33, v20
	v_max_f32_e32 v33, v19, v18
	v_min_f32_e32 v18, v19, v18
	v_max_f32_e32 v19, v21, v23
	v_min_f32_e32 v21, v21, v23
	v_max_f32_e32 v23, v24, v22
	v_min_f32_e32 v22, v24, v22
	v_max_f32_e32 v24, v26, v28
	v_min_f32_e32 v26, v26, v28
	v_max_f32_e32 v28, v27, v25
	v_min_f32_e32 v25, v27, v25
	v_max_f32_e32 v27, v29, v31
	v_min_f32_e32 v29, v29, v31
	v_max_f32_e32 v31, v32, v30
	v_min_f32_e32 v30, v32, v30
	v_max_f32_e32 v65, v64, v98
	v_min_f32_e32 v64, v64, v98
	v_max_f32_e32 v98, v51, v50
	v_min_f32_e32 v50, v51, v50
	v_max_f32_e32 v51, v52, v54
	v_min_f32_e32 v52, v52, v54
	v_max_f32_e32 v54, v55, v53
	v_min_f32_e32 v53, v55, v53
	v_max_f32_e32 v55, v57, v59
	v_min_f32_e32 v57, v57, v59
	v_max_f32_e32 v59, v58, v56
	v_min_f32_e32 v56, v58, v56
	v_max_f32_e32 v58, v60, v62
	v_min_f32_e32 v60, v60, v62
	v_max_f32_e32 v62, v63, v61
	v_min_f32_e32 v61, v63, v61
	v_max_f32_e32 v49, v48, v108
	v_min_f32_e32 v48, v48, v108
	v_max_f32_e32 v108, v107, v106
	v_min_f32_e32 v106, v107, v106
	v_max_f32_e32 v107, v109, v111
	v_min_f32_e32 v109, v109, v111
	v_max_f32_e32 v111, v112, v110
	v_min_f32_e32 v110, v112, v110
	v_max_f32_e32 v112, v114, v113
	v_min_f32_e32 v113, v114, v113
	v_max_f32_e32 v114, v43, v42
	v_min_f32_e32 v42, v43, v42
	v_max_f32_e32 v43, v44, v46
	v_min_f32_e32 v44, v44, v46
	v_max_f32_e32 v46, v47, v45
	v_min_f32_e32 v45, v47, v45
	v_max_f32_e32 v17, v15, v122
	v_min_f32_e32 v15, v15, v122
	v_max_f32_e32 v122, v3, v2
	v_min_f32_e32 v2, v3, v2
	v_max_f32_e32 v3, v4, v5
	v_min_f32_e32 v4, v4, v5
	v_max_f32_e32 v5, v8, v6
	v_min_f32_e32 v6, v8, v6
	v_max_f32_e32 v8, v10, v12
	v_min_f32_e32 v10, v10, v12
	v_max_f32_e32 v12, v9, v7
	v_min_f32_e32 v7, v9, v7
	v_max_f32_e32 v9, v11, v13
	v_min_f32_e32 v11, v11, v13
	v_max_f32_e32 v13, v16, v14
	v_min_f32_e32 v14, v16, v14
	v_max_f32_e32 v32, v34, v21
	v_min_f32_e32 v21, v34, v21
	v_max_f32_e32 v34, v20, v19
	v_min_f32_e32 v19, v20, v19
	v_max_f32_e32 v20, v33, v22
	v_min_f32_e32 v22, v33, v22
	v_max_f32_e32 v33, v18, v23
	v_min_f32_e32 v18, v18, v23
	v_max_f32_e32 v23, v29, v24
	v_min_f32_e32 v24, v29, v24
	v_max_f32_e32 v29, v27, v26
	v_min_f32_e32 v26, v27, v26
	v_max_f32_e32 v27, v30, v28
	v_min_f32_e32 v28, v30, v28
	v_max_f32_e32 v30, v31, v25
	v_min_f32_e32 v25, v31, v25
	v_max_f32_e32 v63, v65, v52
	v_min_f32_e32 v52, v65, v52
	v_max_f32_e32 v65, v64, v51
; #define CE_DESC(a, b) do { const float _t = fmaxf(a, b); b = fminf(a, b); a = _t; } while (0)
; __device__ __forceinline__ void sort16_desc(float (&v)[16]) {
; #pragma unroll
;     for (int k = 2; k <= 16; k <<= 1)
; #pragma unroll
;         for (int j = k >> 1; j > 0; j >>= 1)
; #pragma unroll
;             for (int i = 0; i < 16; ++i) { const int l = i ^ j; if (l > i) { if ((i & k) == 0 || k == 16) CE_DESC(v[i], v[l]); else CE_DESC(v[l], v[i]); } }
; }
	v_min_f32_e32 v51, v64, v51
	v_max_f32_e32 v64, v98, v53
	v_min_f32_e32 v53, v98, v53
	v_max_f32_e32 v98, v50, v54
	v_min_f32_e32 v50, v50, v54
	v_max_f32_e32 v54, v60, v55
	v_min_f32_e32 v55, v60, v55
	v_max_f32_e32 v60, v58, v57
	v_min_f32_e32 v57, v58, v57
	v_max_f32_e32 v58, v61, v59
	v_min_f32_e32 v59, v61, v59
	v_max_f32_e32 v61, v62, v56
	v_min_f32_e32 v56, v62, v56
	v_max_f32_e32 v47, v49, v109
	v_min_f32_e32 v49, v49, v109
	v_max_f32_e32 v109, v48, v107
	v_min_f32_e32 v48, v48, v107
	v_max_f32_e32 v107, v108, v110
	v_min_f32_e32 v108, v108, v110
	v_max_f32_e32 v110, v106, v111
	v_min_f32_e32 v106, v106, v111
	v_max_f32_e32 v111, v44, v112
	v_min_f32_e32 v44, v44, v112
	v_max_f32_e32 v112, v43, v113
	v_min_f32_e32 v43, v43, v113
	v_max_f32_e32 v113, v45, v114
	v_min_f32_e32 v45, v45, v114
	v_max_f32_e32 v114, v46, v42
	v_min_f32_e32 v42, v46, v42
	v_max_f32_e32 v16, v17, v4
	v_min_f32_e32 v4, v17, v4
	v_max_f32_e32 v17, v15, v3
	v_min_f32_e32 v3, v15, v3
	v_max_f32_e32 v15, v122, v6
	v_min_f32_e32 v6, v122, v6
	v_max_f32_e32 v122, v2, v5
	v_min_f32_e32 v2, v2, v5
	v_max_f32_e32 v5, v11, v8
	v_min_f32_e32 v8, v11, v8
	v_max_f32_e32 v11, v9, v10
	v_min_f32_e32 v9, v9, v10
	v_max_f32_e32 v10, v14, v12
	v_min_f32_e32 v12, v14, v12
	v_max_f32_e32 v14, v13, v7
	v_min_f32_e32 v7, v13, v7
	v_max_f32_e32 v31, v32, v20
	v_min_f32_e32 v20, v32, v20
	v_max_f32_e32 v32, v34, v33
	v_min_f32_e32 v33, v34, v33
	v_max_f32_e32 v34, v21, v22
	v_min_f32_e32 v21, v21, v22
	v_max_f32_e32 v22, v19, v18
	v_min_f32_e32 v18, v19, v18
	v_max_f32_e32 v19, v28, v24
	v_min_f32_e32 v24, v28, v24
	v_max_f32_e32 v28, v25, v26
	v_min_f32_e32 v25, v25, v26
	v_max_f32_e32 v26, v27, v23
	v_min_f32_e32 v23, v27, v23
	v_max_f32_e32 v27, v30, v29
	v_min_f32_e32 v29, v30, v29
	v_max_f32_e32 v62, v63, v64
	v_min_f32_e32 v63, v63, v64
	v_max_f32_e32 v64, v65, v98
	v_min_f32_e32 v65, v65, v98
	v_max_f32_e32 v98, v52, v53
	v_min_f32_e32 v52, v52, v53
	v_max_f32_e32 v53, v51, v50
	v_min_f32_e32 v50, v51, v50
	v_max_f32_e32 v51, v59, v55
	v_min_f32_e32 v55, v59, v55
	v_max_f32_e32 v59, v56, v57
	v_min_f32_e32 v56, v56, v57
	v_max_f32_e32 v57, v58, v54
	v_min_f32_e32 v54, v58, v54
	v_max_f32_e32 v58, v61, v60
	v_min_f32_e32 v60, v61, v60
	v_max_f32_e32 v46, v47, v107
	v_min_f32_e32 v47, v47, v107
	v_max_f32_e32 v107, v109, v110
	v_min_f32_e32 v109, v109, v110
	v_max_f32_e32 v110, v49, v108
	v_min_f32_e32 v49, v49, v108
	v_max_f32_e32 v108, v48, v106
	v_min_f32_e32 v48, v48, v106
	v_max_f32_e32 v106, v45, v44
	v_min_f32_e32 v44, v45, v44
	v_max_f32_e32 v45, v42, v43
	v_min_f32_e32 v42, v42, v43
	v_max_f32_e32 v43, v113, v111
	v_min_f32_e32 v111, v113, v111
	v_max_f32_e32 v113, v114, v112
	v_min_f32_e32 v112, v114, v112
	v_max_f32_e32 v13, v16, v15
	v_min_f32_e32 v15, v16, v15
	v_max_f32_e32 v16, v17, v122
	v_min_f32_e32 v17, v17, v122
	v_max_f32_e32 v122, v4, v6
	v_min_f32_e32 v4, v4, v6
	v_max_f32_e32 v6, v3, v2
	v_min_f32_e32 v2, v3, v2
	v_max_f32_e32 v3, v12, v8
	v_min_f32_e32 v8, v12, v8
	v_max_f32_e32 v12, v7, v9
	v_min_f32_e32 v7, v7, v9
	v_max_f32_e32 v9, v10, v5
	v_min_f32_e32 v5, v10, v5
	v_max_f32_e32 v10, v14, v11
	v_min_f32_e32 v11, v14, v11
	v_max_f32_e32 v30, v31, v32
	v_min_f32_e32 v31, v31, v32
	v_max_f32_e32 v32, v20, v33
	v_min_f32_e32 v20, v20, v33
	v_max_f32_e32 v33, v34, v22
	v_min_f32_e32 v22, v34, v22
	v_max_f32_e32 v34, v21, v18
	v_min_f32_e32 v18, v21, v18
	v_max_f32_e32 v21, v25, v24
	v_min_f32_e32 v24, v25, v24
	v_max_f32_e32 v25, v28, v19
	v_min_f32_e32 v19, v28, v19
	v_max_f32_e32 v28, v29, v23
	v_min_f32_e32 v23, v29, v23
	v_max_f32_e32 v29, v27, v26
	v_min_f32_e32 v26, v27, v26
	v_max_f32_e32 v61, v62, v64
	v_min_f32_e32 v62, v62, v64
	v_max_f32_e32 v64, v63, v65
	v_min_f32_e32 v63, v63, v65
	v_max_f32_e32 v65, v98, v53
	v_min_f32_e32 v53, v98, v53
	v_max_f32_e32 v98, v52, v50
	v_min_f32_e32 v50, v52, v50
	v_max_f32_e32 v52, v56, v55
	v_min_f32_e32 v55, v56, v55
	v_max_f32_e32 v56, v59, v51
	v_min_f32_e32 v51, v59, v51
	v_max_f32_e32 v59, v60, v54
	v_min_f32_e32 v54, v60, v54
	v_max_f32_e32 v60, v58, v57
	v_min_f32_e32 v57, v58, v57
	v_max_f32_e32 v114, v46, v107
	v_min_f32_e32 v46, v46, v107
	v_max_f32_e32 v107, v47, v109
	v_min_f32_e32 v47, v47, v109
	v_max_f32_e32 v109, v110, v108
	v_min_f32_e32 v108, v110, v108
	v_max_f32_e32 v110, v49, v48
	v_min_f32_e32 v48, v49, v48
	v_max_f32_e32 v49, v42, v44
	v_min_f32_e32 v42, v42, v44
	v_max_f32_e32 v44, v45, v106
	v_min_f32_e32 v45, v45, v106
	v_max_f32_e32 v106, v112, v111
	v_min_f32_e32 v111, v112, v111
	v_max_f32_e32 v112, v113, v43
	v_min_f32_e32 v43, v113, v43
	v_max_f32_e32 v14, v13, v16
	v_min_f32_e32 v13, v13, v16
	v_max_f32_e32 v16, v15, v17
	v_min_f32_e32 v15, v15, v17
	v_max_f32_e32 v17, v122, v6
	v_min_f32_e32 v6, v122, v6
	v_max_f32_e32 v122, v4, v2
	v_min_f32_e32 v2, v4, v2
	v_max_f32_e32 v4, v7, v8
	v_min_f32_e32 v7, v7, v8
	v_max_f32_e32 v8, v12, v3
	v_min_f32_e32 v3, v12, v3
	v_max_f32_e32 v12, v11, v5
	v_min_f32_e32 v5, v11, v5
	v_max_f32_e32 v11, v10, v9
	v_min_f32_e32 v9, v10, v9
	v_max_f32_e32 v27, v30, v24
	v_min_f32_e32 v24, v30, v24
	v_max_f32_e32 v30, v31, v21
	v_min_f32_e32 v21, v31, v21
	v_max_f32_e32 v31, v32, v19
	v_min_f32_e32 v19, v32, v19
	v_max_f32_e32 v32, v20, v25
	v_min_f32_e32 v20, v20, v25
	v_max_f32_e32 v25, v33, v23
	v_min_f32_e32 v23, v33, v23
	v_max_f32_e32 v33, v22, v28
	v_min_f32_e32 v22, v22, v28
	v_max_f32_e32 v28, v34, v26
	v_min_f32_e32 v26, v34, v26
	v_max_f32_e32 v34, v18, v29
	v_min_f32_e32 v18, v18, v29
	v_max_f32_e32 v58, v61, v55
	v_min_f32_e32 v55, v61, v55
	v_max_f32_e32 v61, v62, v52
	v_min_f32_e32 v52, v62, v52
	v_max_f32_e32 v62, v64, v51
; #define CE_DESC(a, b) do { const float _t = fmaxf(a, b); b = fminf(a, b); a = _t; } while (0)
; __device__ __forceinline__ void sort16_desc(float (&v)[16]) {
; #pragma unroll
;     for (int k = 2; k <= 16; k <<= 1)
; #pragma unroll
;         for (int j = k >> 1; j > 0; j >>= 1)
; #pragma unroll
;             for (int i = 0; i < 16; ++i) { const int l = i ^ j; if (l > i) { if ((i & k) == 0 || k == 16) CE_DESC(v[i], v[l]); else CE_DESC(v[l], v[i]); } }
; }
; __device__ __forceinline__ void merge16_desc(float (&a)[16], const float (&b)[16]) {
; #pragma unroll
;     for (int i = 0; i < 16; ++i) a[i] = fmaxf(a[i], b[15 - i]);
; #pragma unroll
;     for (int j = 8; j > 0; j >>= 1)
; #pragma unroll
;         for (int i = 0; i < 16; ++i) { const int l = i ^ j; if (l > i) CE_DESC(a[i], a[l]); }
; }
	v_min_f32_e32 v51, v64, v51
	v_max_f32_e32 v64, v63, v56
	v_min_f32_e32 v56, v63, v56
	v_max_f32_e32 v63, v65, v54
	v_min_f32_e32 v54, v65, v54
	v_max_f32_e32 v65, v53, v59
	v_min_f32_e32 v53, v53, v59
	v_max_f32_e32 v59, v98, v57
	v_min_f32_e32 v57, v98, v57
	v_max_f32_e32 v98, v50, v60
	v_min_f32_e32 v50, v50, v60
	v_max_f32_e32 v113, v114, v42
	v_min_f32_e32 v42, v114, v42
	v_max_f32_e32 v114, v46, v49
	v_min_f32_e32 v46, v46, v49
	v_max_f32_e32 v49, v107, v45
	v_min_f32_e32 v45, v107, v45
	v_max_f32_e32 v107, v47, v44
	v_min_f32_e32 v44, v47, v44
	v_max_f32_e32 v47, v109, v111
	v_min_f32_e32 v109, v109, v111
	v_max_f32_e32 v111, v108, v106
	v_min_f32_e32 v106, v108, v106
	v_max_f32_e32 v108, v110, v43
	v_min_f32_e32 v43, v110, v43
	v_max_f32_e32 v110, v48, v112
	v_min_f32_e32 v48, v48, v112
	v_max_f32_e32 v10, v14, v7
	v_min_f32_e32 v7, v14, v7
	v_max_f32_e32 v14, v13, v4
	v_min_f32_e32 v4, v13, v4
	v_max_f32_e32 v13, v16, v3
	v_min_f32_e32 v3, v16, v3
	v_max_f32_e32 v16, v15, v8
	v_min_f32_e32 v8, v15, v8
	v_max_f32_e32 v15, v17, v5
	v_min_f32_e32 v5, v17, v5
	v_max_f32_e32 v17, v6, v12
	v_min_f32_e32 v6, v6, v12
	v_max_f32_e32 v12, v122, v9
	v_min_f32_e32 v9, v122, v9
	v_max_f32_e32 v122, v2, v11
	v_min_f32_e32 v2, v2, v11
	v_max_f32_e32 v29, v27, v25
	v_min_f32_e32 v25, v27, v25
	v_max_f32_e32 v27, v30, v33
	v_min_f32_e32 v33, v30, v33
	v_max_f32_e32 v30, v31, v28
	v_min_f32_e32 v28, v31, v28
	v_max_f32_e32 v31, v32, v34
	v_min_f32_e32 v32, v32, v34
	v_max_f32_e32 v34, v24, v23
	v_min_f32_e32 v35, v24, v23
	v_max_f32_e32 v36, v21, v22
	v_min_f32_e32 v37, v21, v22
	v_max_f32_e32 v21, v19, v26
	v_min_f32_e32 v38, v19, v26
	v_max_f32_e32 v39, v20, v18
	v_min_f32_e32 v40, v20, v18
	v_max_f32_e32 v60, v58, v63
	v_min_f32_e32 v58, v58, v63
	v_max_f32_e32 v63, v61, v65
	v_min_f32_e32 v61, v61, v65
	v_max_f32_e32 v65, v62, v59
	v_min_f32_e32 v59, v62, v59
	v_max_f32_e32 v62, v64, v98
	v_min_f32_e32 v64, v64, v98
	v_max_f32_e32 v98, v55, v54
	v_min_f32_e32 v54, v55, v54
	v_max_f32_e32 v55, v52, v53
	v_min_f32_e32 v52, v52, v53
	v_max_f32_e32 v53, v51, v57
	v_min_f32_e32 v51, v51, v57
	v_max_f32_e32 v57, v56, v50
	v_min_f32_e32 v50, v56, v50
	v_max_f32_e32 v112, v113, v47
	v_min_f32_e32 v47, v113, v47
	v_max_f32_e32 v113, v114, v111
	v_min_f32_e32 v111, v114, v111
	v_max_f32_e32 v114, v49, v108
	v_min_f32_e32 v49, v49, v108
	v_max_f32_e32 v108, v107, v110
	v_min_f32_e32 v107, v107, v110
	v_max_f32_e32 v110, v42, v109
	v_min_f32_e32 v42, v42, v109
	v_max_f32_e32 v109, v46, v106
	v_min_f32_e32 v46, v46, v106
	v_max_f32_e32 v106, v45, v43
	v_min_f32_e32 v43, v45, v43
	v_max_f32_e32 v45, v44, v48
	v_min_f32_e32 v44, v44, v48
	v_max_f32_e32 v11, v10, v15
	v_min_f32_e32 v10, v10, v15
	v_max_f32_e32 v15, v14, v17
	v_min_f32_e32 v14, v14, v17
	v_max_f32_e32 v17, v13, v12
	v_min_f32_e32 v12, v13, v12
	v_max_f32_e32 v13, v16, v122
	v_min_f32_e32 v16, v16, v122
	v_max_f32_e32 v122, v7, v5
	v_min_f32_e32 v5, v7, v5
	v_max_f32_e32 v7, v4, v6
	v_min_f32_e32 v4, v4, v6
	v_max_f32_e32 v6, v3, v9
	v_min_f32_e32 v3, v3, v9
	v_max_f32_e32 v9, v8, v2
	v_min_f32_e32 v2, v8, v2
	v_max_f32_e32 v22, v29, v30
	v_min_f32_e32 v18, v29, v30
	v_max_f32_e32 v30, v27, v31
	v_min_f32_e32 v26, v27, v31
	v_max_f32_e32 v23, v25, v28
	v_min_f32_e32 v19, v25, v28
	v_max_f32_e32 v31, v33, v32
	v_min_f32_e32 v27, v33, v32
	v_max_f32_e32 v24, v34, v21
	v_min_f32_e32 v20, v34, v21
	v_max_f32_e32 v32, v36, v39
	v_min_f32_e32 v28, v36, v39
	v_max_f32_e32 v25, v35, v38
	v_min_f32_e32 v21, v35, v38
	v_max_f32_e32 v33, v37, v40
	v_min_f32_e32 v29, v37, v40
	v_max_f32_e32 v56, v60, v65
	v_min_f32_e32 v60, v60, v65
	v_max_f32_e32 v65, v63, v62
	v_min_f32_e32 v62, v63, v62
	v_max_f32_e32 v63, v58, v59
	v_min_f32_e32 v58, v58, v59
	v_max_f32_e32 v59, v61, v64
	v_min_f32_e32 v61, v61, v64
	v_max_f32_e32 v64, v98, v53
	v_min_f32_e32 v53, v98, v53
	v_max_f32_e32 v98, v55, v57
	v_min_f32_e32 v55, v55, v57
	v_max_f32_e32 v57, v54, v51
	v_min_f32_e32 v51, v54, v51
	v_max_f32_e32 v54, v52, v50
	v_min_f32_e32 v50, v52, v50
	v_max_f32_e32 v48, v112, v114
	v_min_f32_e32 v112, v112, v114
	v_max_f32_e32 v114, v113, v108
	v_min_f32_e32 v108, v113, v108
	v_max_f32_e32 v113, v47, v49
	v_min_f32_e32 v47, v47, v49
	v_max_f32_e32 v49, v111, v107
	v_min_f32_e32 v107, v111, v107
	v_max_f32_e32 v111, v110, v106
	v_min_f32_e32 v106, v110, v106
	v_max_f32_e32 v110, v109, v45
	v_min_f32_e32 v45, v109, v45
	v_max_f32_e32 v109, v42, v43
	v_min_f32_e32 v42, v42, v43
	v_max_f32_e32 v43, v46, v44
	v_min_f32_e32 v44, v46, v44
	v_max_f32_e32 v8, v11, v17
	v_min_f32_e32 v11, v11, v17
	v_max_f32_e32 v17, v15, v13
	v_min_f32_e32 v13, v15, v13
	v_max_f32_e32 v15, v10, v12
	v_min_f32_e32 v10, v10, v12
	v_max_f32_e32 v12, v14, v16
	v_min_f32_e32 v14, v14, v16
	v_max_f32_e32 v16, v122, v6
	v_min_f32_e32 v6, v122, v6
	v_max_f32_e32 v122, v7, v9
	v_min_f32_e32 v7, v7, v9
	v_max_f32_e32 v9, v5, v3
	v_min_f32_e32 v3, v5, v3
	v_max_f32_e32 v5, v4, v2
	v_min_f32_e32 v2, v4, v2
	v_min_f32_e32 v41, v22, v30
	v_min_f32_e32 v40, v18, v26
	v_min_f32_e32 v39, v23, v31
	v_min_f32_e32 v38, v19, v27
	v_min_f32_e32 v37, v24, v32
	v_min_f32_e32 v36, v20, v28
	v_min_f32_e32 v35, v25, v33
	v_min_f32_e32 v34, v21, v29
	v_min_f32_e32 v52, v56, v65
	v_min_f32_e32 v99, v60, v62
	v_min_f32_e32 v100, v63, v59
	v_min_f32_e32 v101, v58, v61
	v_min_f32_e32 v102, v64, v98
	v_min_f32_e32 v103, v53, v55
	v_min_f32_e32 v104, v57, v54
	v_min_f32_e32 v105, v51, v50
	v_min_f32_e32 v46, v48, v114
	v_min_f32_e32 v115, v112, v108
	v_min_f32_e32 v116, v113, v49
	v_min_f32_e32 v117, v47, v107
	v_min_f32_e32 v118, v111, v110
	v_min_f32_e32 v119, v106, v45
; #define CE_DESC(a, b) do { const float _t = fmaxf(a, b); b = fminf(a, b); a = _t; } while (0)
; __device__ __forceinline__ void merge16_desc(float (&a)[16], const float (&b)[16]) {
; #pragma unroll
;     for (int i = 0; i < 16; ++i) a[i] = fmaxf(a[i], b[15 - i]);
; #pragma unroll
;     for (int j = 8; j > 0; j >>= 1)
; #pragma unroll
;         for (int i = 0; i < 16; ++i) { const int l = i ^ j; if (l > i) CE_DESC(a[i], a[l]); }
; }
; __device__ __forceinline__ void route_half(float (&top)[16], LAS const unsigned char* keys_lds, const bf16_t* __restrict__ qrow, int r32, int hi) {
;     ...
;     merge16_desc(g[0], g[1]); merge16_desc(g[2], g[3]); merge16_desc(g[0], g[2]);
	v_min_f32_e32 v120, v109, v43
	v_min_f32_e32 v121, v42, v44
	v_min_f32_e32 v4, v8, v17
	v_min_f32_e32 v123, v11, v13
	v_min_f32_e32 v124, v15, v12
	v_min_f32_e32 v125, v10, v14
	v_min_f32_e32 v140, v16, v122
	v_min_f32_e32 v141, v6, v7
	v_min_f32_e32 v181, v9, v5
	v_min_f32_e32 v182, v3, v2
	v_max3_f32 v22, v22, v30, v105
	v_max3_f32 v30, v41, v51, v50
	v_max3_f32 v18, v18, v26, v104
	v_max3_f32 v26, v40, v57, v54
	v_max3_f32 v23, v23, v31, v103
	v_max3_f32 v31, v39, v53, v55
	v_max3_f32 v19, v19, v27, v102
	v_max3_f32 v27, v38, v64, v98
	v_max3_f32 v24, v24, v32, v101
	v_max3_f32 v32, v37, v58, v61
	v_max3_f32 v20, v20, v28, v100
	v_max3_f32 v28, v36, v63, v59
	v_max3_f32 v25, v25, v33, v99
	v_max3_f32 v33, v35, v60, v62
	v_max3_f32 v21, v21, v29, v52
	v_max3_f32 v29, v34, v56, v65
	v_max3_f32 v48, v48, v114, v182
	v_max3_f32 v2, v46, v3, v2
	v_max3_f32 v3, v112, v108, v181
	v_max3_f32 v5, v115, v9, v5
	v_max3_f32 v9, v113, v49, v141
	v_max3_f32 v6, v116, v6, v7
	v_max3_f32 v7, v47, v107, v140
	v_max3_f32 v16, v117, v16, v122
	v_max3_f32 v46, v111, v110, v125
	v_max3_f32 v10, v118, v10, v14
	v_max3_f32 v14, v106, v45, v124
	v_max3_f32 v12, v119, v15, v12
	v_max3_f32 v15, v109, v43, v123
	v_max3_f32 v11, v120, v11, v13
	v_max3_f32 v4, v42, v44, v4
	v_max3_f32 v8, v121, v8, v17
	v_max_f32_e32 v34, v22, v24
	v_min_f32_e32 v22, v22, v24
	v_max_f32_e32 v24, v30, v32
	v_min_f32_e32 v30, v30, v32
	v_max_f32_e32 v32, v18, v20
	v_min_f32_e32 v18, v18, v20
	v_max_f32_e32 v20, v26, v28
	v_min_f32_e32 v26, v26, v28
	v_max_f32_e32 v28, v23, v25
	v_min_f32_e32 v23, v23, v25
	v_max_f32_e32 v25, v31, v33
	v_min_f32_e32 v31, v31, v33
	v_max_f32_e32 v33, v19, v21
	v_min_f32_e32 v19, v19, v21
	v_max_f32_e32 v21, v27, v29
	v_min_f32_e32 v27, v27, v29
	v_max_f32_e32 v13, v48, v46
	v_min_f32_e32 v17, v48, v46
	v_max_f32_e32 v42, v2, v10
	v_min_f32_e32 v2, v2, v10
	v_max_f32_e32 v10, v3, v14
	v_min_f32_e32 v3, v3, v14
	v_max_f32_e32 v14, v5, v12
	v_min_f32_e32 v5, v5, v12
	v_max_f32_e32 v12, v9, v15
	v_min_f32_e32 v9, v9, v15
	v_max_f32_e32 v15, v6, v11
	v_min_f32_e32 v6, v6, v11
	v_max_f32_e32 v11, v7, v4
	v_min_f32_e32 v4, v7, v4
	v_max_f32_e32 v7, v16, v8
	v_min_f32_e32 v8, v16, v8
	v_max_f32_e32 v29, v34, v28
	v_min_f32_e32 v28, v34, v28
	v_max_f32_e32 v34, v24, v25
	v_min_f32_e32 v24, v24, v25
	v_max_f32_e32 v25, v32, v33
	v_min_f32_e32 v32, v32, v33
	v_max_f32_e32 v33, v20, v21
	v_min_f32_e32 v20, v20, v21
	v_max_f32_e32 v21, v22, v23
	v_min_f32_e32 v22, v22, v23
	v_max_f32_e32 v23, v30, v31
	v_min_f32_e32 v30, v30, v31
	v_max_f32_e32 v31, v18, v19
	v_min_f32_e32 v18, v18, v19
	v_max_f32_e32 v19, v26, v27
	v_min_f32_e32 v26, v26, v27
	v_max_f32_e32 v16, v13, v12
	v_min_f32_e32 v12, v13, v12
	v_max_f32_e32 v13, v42, v15
	v_min_f32_e32 v15, v42, v15
	v_max_f32_e32 v42, v10, v11
	v_min_f32_e32 v10, v10, v11
	v_max_f32_e32 v11, v14, v7
	v_min_f32_e32 v7, v14, v7
	v_max_f32_e32 v14, v17, v9
	v_min_f32_e32 v9, v17, v9
	v_max_f32_e32 v17, v2, v6
	v_min_f32_e32 v2, v2, v6
	v_max_f32_e32 v6, v3, v4
	v_min_f32_e32 v3, v3, v4
	v_max_f32_e32 v4, v5, v8
	v_min_f32_e32 v5, v5, v8
	v_max_f32_e32 v27, v29, v25
	v_min_f32_e32 v25, v29, v25
	v_max_f32_e32 v29, v34, v33
	v_min_f32_e32 v33, v34, v33
	v_max_f32_e32 v34, v28, v32
	v_min_f32_e32 v28, v28, v32
	v_max_f32_e32 v32, v24, v20
	v_min_f32_e32 v20, v24, v20
	v_max_f32_e32 v24, v21, v31
	v_min_f32_e32 v21, v21, v31
	v_max_f32_e32 v31, v23, v19
	v_min_f32_e32 v19, v23, v19
	v_max_f32_e32 v23, v22, v18
	v_min_f32_e32 v18, v22, v18
	v_max_f32_e32 v22, v30, v26
	v_min_f32_e32 v26, v30, v26
	v_max_f32_e32 v8, v16, v42
	v_min_f32_e32 v16, v16, v42
	v_max_f32_e32 v42, v13, v11
	v_min_f32_e32 v11, v13, v11
	v_max_f32_e32 v13, v12, v10
	v_min_f32_e32 v10, v12, v10
	v_max_f32_e32 v12, v15, v7
	v_min_f32_e32 v7, v15, v7
	v_max_f32_e32 v15, v14, v6
	v_min_f32_e32 v6, v14, v6
	v_max_f32_e32 v14, v17, v4
	v_min_f32_e32 v4, v17, v4
	v_max_f32_e32 v17, v9, v3
	v_min_f32_e32 v3, v9, v3
	v_max_f32_e32 v9, v2, v5
	v_min_f32_e32 v2, v2, v5
	v_min_f32_e32 v30, v27, v29
	v_min_f32_e32 v35, v25, v33
	v_min_f32_e32 v36, v34, v32
	v_min_f32_e32 v37, v28, v20
	v_min_f32_e32 v38, v24, v31
	v_min_f32_e32 v39, v21, v19
	v_min_f32_e32 v40, v23, v22
	v_min_f32_e32 v41, v18, v26
	v_min_f32_e32 v5, v8, v42
	v_min_f32_e32 v43, v16, v11
	v_min_f32_e32 v44, v13, v12
	v_min_f32_e32 v45, v10, v7
	v_min_f32_e32 v46, v15, v14
	v_min_f32_e32 v47, v6, v4
	v_min_f32_e32 v48, v17, v9
	v_min_f32_e32 v49, v3, v2
	v_max3_f32 v27, v27, v29, v49
	v_max3_f32 v2, v30, v3, v2
	v_max3_f32 v3, v25, v33, v48
	v_max3_f32 v9, v35, v17, v9
	v_max3_f32 v17, v34, v32, v47
	v_max3_f32 v4, v36, v6, v4
	v_max3_f32 v6, v28, v20, v46
	v_max3_f32 v14, v37, v15, v14
	v_max3_f32 v15, v24, v31, v45
	v_max3_f32 v7, v38, v10, v7
	v_max3_f32 v10, v21, v19, v44
	v_max3_f32 v12, v39, v13, v12
	v_max3_f32 v13, v23, v22, v43
	v_max3_f32 v11, v40, v16, v11
	v_max3_f32 v5, v18, v26, v5
	v_max3_f32 v8, v41, v8, v42
	v_max_f32_e32 v16, v27, v15
	v_min_f32_e32 v15, v27, v15
	v_max_f32_e32 v18, v2, v7
	v_min_f32_e32 v2, v2, v7
	v_max_f32_e32 v7, v3, v10
	v_min_f32_e32 v3, v3, v10
	v_max_f32_e32 v10, v9, v12
	v_min_f32_e32 v9, v9, v12
	v_max_f32_e32 v12, v17, v13
	v_min_f32_e32 v13, v17, v13
	v_max_f32_e32 v17, v4, v11
	v_min_f32_e32 v4, v4, v11
	v_max_f32_e32 v11, v6, v5
	v_min_f32_e32 v5, v6, v5
	v_max_f32_e32 v6, v14, v8
	v_min_f32_e32 v8, v14, v8
	v_max_f32_e32 v14, v16, v12
	v_min_f32_e32 v12, v16, v12
	v_max_f32_e32 v16, v18, v17
	v_min_f32_e32 v17, v18, v17
	v_max_f32_e32 v18, v7, v11
	v_min_f32_e32 v7, v7, v11
	v_max_f32_e32 v11, v10, v6
	v_min_f32_e32 v6, v10, v6
	v_max_f32_e32 v10, v15, v13
; __device__ __forceinline__ void route_half(float (&top)[16], LAS const unsigned char* keys_lds, const bf16_t* __restrict__ qrow, int r32, int hi) {
;     ...
;     merge16_desc(g[0], g[1]); merge16_desc(g[2], g[3]); merge16_desc(g[0], g[2]);
;     float o[16];
; #pragma unroll
;     for (int i = 0; i < 16; ++i) { g[0][i] = __uint_as_float(__float_as_uint(g[0][i]) | hi4); o[i] = __shfl_xor(g[0][i], 32); }
;     merge16_desc(g[0], o);
	v_min_f32_e32 v13, v15, v13
	v_max_f32_e32 v15, v2, v4
	v_min_f32_e32 v2, v2, v4
	v_max_f32_e32 v4, v3, v5
	v_min_f32_e32 v3, v3, v5
	v_max_f32_e32 v5, v9, v8
	v_min_f32_e32 v8, v9, v8
	v_max_f32_e32 v9, v14, v18
	v_min_f32_e32 v14, v14, v18
	v_max_f32_e32 v18, v16, v11
	v_min_f32_e32 v11, v16, v11
	v_max_f32_e32 v16, v12, v7
	v_min_f32_e32 v7, v12, v7
	v_max_f32_e32 v12, v17, v6
	v_min_f32_e32 v6, v17, v6
	v_max_f32_e32 v17, v10, v4
	v_min_f32_e32 v4, v10, v4
	v_max_f32_e32 v10, v15, v5
	v_min_f32_e32 v5, v15, v5
	v_max_f32_e32 v15, v13, v3
	v_min_f32_e32 v3, v13, v3
	v_max_f32_e32 v13, v2, v8
	v_min_f32_e32 v2, v2, v8
	v_max_f32_e32 v8, v9, v18
	v_min_f32_e32 v9, v9, v18
	v_max_f32_e32 v18, v14, v11
	v_min_f32_e32 v11, v14, v11
	v_max_f32_e32 v14, v16, v12
	v_min_f32_e32 v12, v16, v12
	v_max_f32_e32 v16, v7, v6
	v_min_f32_e32 v23, v7, v6
	v_max_f32_e32 v27, v17, v10
	v_min_f32_e32 v28, v17, v10
	v_max_f32_e32 v29, v4, v5
	v_min_f32_e32 v30, v4, v5
	v_max_f32_e32 v31, v15, v13
	v_min_f32_e32 v32, v15, v13
	v_max_f32_e32 v33, v3, v2
	v_min_f32_e32 v34, v3, v2
	v_or_b32_e32 v26, v144, v8
	v_or_b32_e32 v25, v144, v9
	v_or_b32_e32 v24, v144, v18
	v_or_b32_e32 v22, v144, v11
	v_or_b32_e32 v21, v144, v14
	v_or_b32_e32 v20, v144, v12
	v_or_b32_e32 v19, v144, v16
	v_or_b32_e32 v18, v144, v23
	v_or_b32_e32 v17, v144, v27
	v_or_b32_e32 v15, v144, v28
	v_or_b32_e32 v14, v144, v29
	v_or_b32_e32 v13, v144, v30
	v_or_b32_e32 v12, v144, v31
	v_or_b32_e32 v11, v144, v32
	v_or_b32_e32 v9, v144, v33
	v_or_b32_e32 v8, v144, v34
	ds_bpermute_b32 v2, v142, v26
	ds_bpermute_b32 v3, v142, v25
	ds_bpermute_b32 v4, v142, v24
	ds_bpermute_b32 v5, v142, v22
	ds_bpermute_b32 v6, v142, v21
	ds_bpermute_b32 v7, v142, v20
	ds_bpermute_b32 v10, v142, v19
	ds_bpermute_b32 v16, v142, v18
	ds_bpermute_b32 v23, v142, v17
	ds_bpermute_b32 v27, v142, v15
	ds_bpermute_b32 v28, v142, v14
	ds_bpermute_b32 v29, v142, v13
	ds_bpermute_b32 v30, v142, v12
	ds_bpermute_b32 v31, v142, v11
	ds_bpermute_b32 v32, v142, v9
	ds_bpermute_b32 v33, v142, v8
	s_and_b64 vcc, exec, s[10:11]
	s_cbranch_vccnz .LBB0_926
; template <bool SIGNED4> __device__ __forceinline__ void qrow_store(const f32x4 (&v)[4], unsigned char* q, float* scale, int row, int lane) {
;     float ss = 0.f;
; #pragma unroll
;     for (int j = 0; j < 4; ++j) ss += v[j].x * v[j].x + v[j].y * v[j].y + v[j].z * v[j].z + v[j].w * v[j].w;
;     ss = wave_sum(ss);
;     const float sc = ss > 0.f ? 0.3352f * sqrtf(ss * (1.f / 1024.f)) : 1.f, inv = __builtin_amdgcn_rcpf(sc);
;     unsigned n[16];
; #pragma unroll
;     for (int j = 0; j < 4; ++j) {
; #pragma unroll
;         for (int i = 0; i < 4; ++i) { const float f = floorf(v[j][i] * inv) + 8.f; n[4 * j + i] = (unsigned)fminf(fmaxf(f, 0.f), 15.f); } }
;     u32x2 o;
; #pragma unroll
;     for (int m = 0; m < 2; ++m) { unsigned w = 0;
; #pragma unroll
;         for (int b = 0; b < 4; ++b) w |= (n[8 * m + b] | (n[8 * m + 4 + b] << 4)) << (8 * b);
;         o[m] = SIGNED4 ? (w ^ 0x88888888u) : w; }
;     *(u32x2*)(q + (size_t)row * 1024 + lane * 16) = o;
;     if (lane == 0) scale[row] = sc;
; }
; __global__ void __launch_bounds__(NTHREADS, 2) mega(Args a) {
;     ...
;             if (oka) qrow_store<false>(qa, ws + WS_UQ + 8, (float*)(ws + WS_VS), ra, lane); if (okb) qrow_store<false>(qb, ws + WS_UQ + 8, (float*)(ws + WS_VS), rb_, lane);
	v_mul_f32_e32 v34, v67, v67
	v_mul_f32_e32 v35, v71, v71
	v_fmac_f32_e32 v34, v66, v66
	v_fmac_f32_e32 v35, v70, v70
	v_fmac_f32_e32 v34, v68, v68
	v_fmac_f32_e32 v35, v72, v72
	v_fmac_f32_e32 v34, v69, v69
	v_fmac_f32_e32 v35, v73, v73
	v_add_f32_e32 v34, v34, v35
	v_mul_f32_e32 v35, v75, v75
	v_fmac_f32_e32 v35, v74, v74
	v_fmac_f32_e32 v35, v76, v76
	v_fmac_f32_e32 v35, v77, v77
	v_add_f32_e32 v34, v35, v34
	v_mul_f32_e32 v35, v83, v83
	v_fmac_f32_e32 v35, v82, v82
	v_fmac_f32_e32 v35, v84, v84
	v_fmac_f32_e32 v35, v85, v85
	v_add_f32_e32 v34, v35, v34
	s_ashr_i32 s27, s26, 31
	s_lshl_b64 s[0:1], s[26:27], 10
	v_add_f32_dpp v34, v34, v34 quad_perm:[1,0,3,2] row_mask:0xf bank_mask:0xf bound_ctrl:1
	s_nop 1
	v_add_f32_dpp v34, v34, v34 quad_perm:[2,3,0,1] row_mask:0xf bank_mask:0xf bound_ctrl:1
	s_nop 1
	v_add_f32_dpp v34, v34, v34 row_ror:4 row_mask:0xf bank_mask:0xf bound_ctrl:1
	s_nop 1
	v_add_f32_dpp v34, v34, v34 row_ror:8 row_mask:0xf bank_mask:0xf bound_ctrl:1
	v_mov_b32_e32 v35, v34
	s_nop 1
	v_permlane16_swap_b32_e32 v34, v35
	v_add_f32_e32 v34, v34, v35
	v_mov_b32_e32 v35, v34
	s_nop 1
	v_permlane32_swap_b32_e32 v34, v35
	v_add_f32_e32 v34, v34, v35
	v_mul_f32_e32 v35, 0x3a800000, v34
	v_mul_f32_e32 v36, 0x4f800000, v35
	v_cmp_gt_f32_e32 vcc, s44, v35
	s_nop 1
	v_cndmask_b32_e32 v35, v35, v36, vcc
	v_sqrt_f32_e32 v36, v35
	s_nop 0
	v_add_u32_e32 v37, -1, v36
	v_fma_f32 v38, -v37, v36, v35
	v_cmp_ge_f32_e64 s[10:11], 0, v38
	v_add_u32_e32 v38, 1, v36
	s_nop 0
	v_cndmask_b32_e64 v37, v36, v37, s[10:11]
	v_fma_f32 v36, -v38, v36, v35
	v_cmp_lt_f32_e64 s[10:11], 0, v36
	s_nop 1
	v_cndmask_b32_e64 v36, v37, v38, s[10:11]
	v_mul_f32_e32 v37, 0x37800000, v36
	v_cndmask_b32_e32 v36, v36, v37, vcc
	v_cmp_class_f32_e32 vcc, v35, v147
	s_nop 1
	v_cndmask_b32_e32 v35, v36, v35, vcc
	v_mul_f32_e32 v35, 0x3eab9f56, v35
	v_cmp_lt_f32_e32 vcc, 0, v34
	s_nop 1
	v_cndmask_b32_e32 v34, 1.0, v35, vcc
	v_rcp_f32_e32 v35, v34
	s_nop 0
	v_mul_f32_e32 v36, v66, v35
	v_mul_f32_e32 v39, v69, v35
	v_mul_f32_e32 v43, v73, v35
	v_floor_f32_e32 v36, v36
	v_mul_f32_e32 v37, v67, v35
	v_mul_f32_e32 v38, v68, v35
	v_floor_f32_e32 v39, v39
	v_mul_f32_e32 v42, v72, v35
	v_floor_f32_e32 v43, v43
	v_add_f32_e32 v36, 0x41000000, v36
	v_floor_f32_e32 v37, v37
	v_floor_f32_e32 v38, v38
	v_add_f32_e32 v39, 0x41000000, v39
	v_mul_f32_e32 v40, v70, v35
	v_mul_f32_e32 v41, v71, v35
	v_floor_f32_e32 v42, v42
	v_add_f32_e32 v43, 0x41000000, v43
	v_med3_f32 v36, v36, 0, v148
	v_add_f32_e32 v37, 0x41000000, v37
	v_add_f32_e32 v38, 0x41000000, v38
	v_med3_f32 v39, v39, 0, v148
	v_floor_f32_e32 v40, v40
	v_floor_f32_e32 v41, v41
	v_add_f32_e32 v42, 0x41000000, v42
	v_med3_f32 v43, v43, 0, v148
	v_mul_f32_e32 v44, v74, v35
	v_mul_f32_e32 v45, v75, v35
	v_mul_f32_e32 v46, v76, v35
	v_mul_f32_e32 v47, v77, v35
	v_mul_f32_e32 v48, v82, v35
	v_mul_f32_e32 v49, v83, v35
	v_mul_f32_e32 v50, v84, v35
	v_mul_f32_e32 v35, v85, v35
	v_cvt_u32_f32_e32 v36, v36
	v_med3_f32 v37, v37, 0, v148
	v_med3_f32 v38, v38, 0, v148
	v_cvt_u32_f32_e32 v39, v39
	v_add_f32_e32 v40, 0x41000000, v40
	v_add_f32_e32 v41, 0x41000000, v41
	v_med3_f32 v42, v42, 0, v148
	v_cvt_u32_f32_e32 v43, v43
	v_floor_f32_e32 v44, v44
	v_floor_f32_e32 v47, v47
	v_floor_f32_e32 v35, v35
	v_cvt_u32_f32_e32 v37, v37
	v_cvt_u32_f32_sdwa v38, v38 dst_sel:WORD_1 dst_unused:UNUSED_PAD src0_sel:DWORD
	v_med3_f32 v40, v40, 0, v148
	v_med3_f32 v41, v41, 0, v148
	v_cvt_u32_f32_e32 v42, v42
	v_add_f32_e32 v44, 0x41000000, v44
	v_floor_f32_e32 v45, v45
	v_floor_f32_e32 v46, v46
	v_add_f32_e32 v47, 0x41000000, v47
	v_floor_f32_e32 v50, v50
	v_add_f32_e32 v35, 0x41000000, v35
	v_cvt_u32_f32_e32 v40, v40
	v_cvt_u32_f32_e32 v41, v41
	v_med3_f32 v44, v44, 0, v148
	v_add_f32_e32 v45, 0x41000000, v45
	v_add_f32_e32 v46, 0x41000000, v46
	v_med3_f32 v47, v47, 0, v148
	v_floor_f32_e32 v48, v48
	v_floor_f32_e32 v49, v49
	v_add_f32_e32 v50, 0x41000000, v50
	v_med3_f32 v35, v35, 0, v148
	v_cvt_u32_f32_e32 v44, v44
	v_med3_f32 v45, v45, 0, v148
	v_med3_f32 v46, v46, 0, v148
	v_cvt_u32_f32_e32 v47, v47
	v_add_f32_e32 v48, 0x41000000, v48
	v_add_f32_e32 v49, 0x41000000, v49
	v_med3_f32 v50, v50, 0, v148
	v_cvt_u32_f32_e32 v35, v35
	v_cvt_u32_f32_e32 v45, v45
	v_cvt_u32_f32_sdwa v46, v46 dst_sel:WORD_1 dst_unused:UNUSED_PAD src0_sel:DWORD
	v_med3_f32 v48, v48, 0, v148
	v_med3_f32 v49, v49, 0, v148
	v_cvt_u32_f32_e32 v50, v50
	v_lshlrev_b32_e32 v43, 28, v43
	v_lshl_or_b32 v36, v39, 24, v36
	v_cvt_u32_f32_e32 v48, v48
	v_cvt_u32_f32_e32 v49, v49
	v_lshlrev_b32_e32 v37, 8, v37
	v_lshlrev_b32_e32 v42, 20, v42
	v_or3_b32 v36, v36, v43, v38
	v_lshlrev_b32_e32 v40, 4, v40
	v_lshlrev_b32_e32 v41, 12, v41
	v_or3_b32 v36, v36, v42, v37
	v_or3_b32 v36, v36, v41, v40
	v_lshlrev_b32_e32 v35, 28, v35
	v_lshl_or_b32 v41, v47, 24, v44
	v_lshlrev_b32_e32 v39, 8, v45
	v_lshlrev_b32_e32 v40, 20, v50
	v_or3_b32 v35, v41, v35, v46
	v_lshlrev_b32_e32 v37, 4, v48
	v_lshlrev_b32_e32 v38, 12, v49
	v_or3_b32 v35, v35, v40, v39
	v_or3_b32 v37, v35, v38, v37
	v_lshl_add_u64 v[38:39], v[134:135], 0, s[0:1]
	global_store_dwordx2 v[38:39], v[36:37], off
	s_and_saveexec_b64 s[0:1], s[2:3]
	s_cbranch_execz .LBB0_925
	s_lshl_b64 s[4:5], s[26:27], 3
	s_add_u32 s4, s34, s4
	s_addc_u32 s5, s35, s5
	global_store_dword v127, v34, s[4:5] offset:4

; template <bool SIGNED4> __device__ __forceinline__ void qrow_store(const f32x4 (&v)[4], unsigned char* q, float* scale, int row, int lane) {
;     float ss = 0.f;
; #pragma unroll
;     for (int j = 0; j < 4; ++j) ss += v[j].x * v[j].x + v[j].y * v[j].y + v[j].z * v[j].z + v[j].w * v[j].w;
;     ss = wave_sum(ss);
;     const float sc = ss > 0.f ? 0.3352f * sqrtf(ss * (1.f / 1024.f)) : 1.f, inv = __builtin_amdgcn_rcpf(sc);
;     unsigned n[16];
; #pragma unroll
;     for (int j = 0; j < 4; ++j) {
; #pragma unroll
;         for (int i = 0; i < 4; ++i) { const float f = floorf(v[j][i] * inv) + 8.f; n[4 * j + i] = (unsigned)fminf(fmaxf(f, 0.f), 15.f); } }
;     u32x2 o;
; #pragma unroll
;     for (int m = 0; m < 2; ++m) { unsigned w = 0;
; #pragma unroll
;         for (int b = 0; b < 4; ++b) w |= (n[8 * m + b] | (n[8 * m + 4 + b] << 4)) << (8 * b);
;         o[m] = SIGNED4 ? (w ^ 0x88888888u) : w; }
;     *(u32x2*)(q + (size_t)row * 1024 + lane * 16) = o;
;     if (lane == 0) scale[row] = sc;
; }
; __global__ void __launch_bounds__(NTHREADS, 2) mega(Args a) {
;     ...
;             if (oka) qrow_store<false>(qa, ws + WS_UQ + 8, (float*)(ws + WS_VS), ra, lane); if (okb) qrow_store<false>(qb, ws + WS_UQ + 8, (float*)(ws + WS_VS), rb_, lane);
.LBB0_926:
	s_and_b64 vcc, exec, s[8:9]
	s_cbranch_vccnz .LBB0_930
	v_mul_f32_e32 v34, v79, v79
	v_mul_f32_e32 v35, v87, v87
	v_fmac_f32_e32 v34, v78, v78
	v_fmac_f32_e32 v35, v86, v86
	v_fmac_f32_e32 v34, v80, v80
	v_fmac_f32_e32 v35, v88, v88
	v_fmac_f32_e32 v34, v81, v81
	v_fmac_f32_e32 v35, v89, v89
	v_add_f32_e32 v34, v34, v35
	v_mul_f32_e32 v35, v91, v91
	v_fmac_f32_e32 v35, v90, v90
	v_fmac_f32_e32 v35, v92, v92
	v_fmac_f32_e32 v35, v93, v93
	v_add_f32_e32 v34, v35, v34
	v_mul_f32_e32 v35, v95, v95
	v_fmac_f32_e32 v35, v94, v94
	v_fmac_f32_e32 v35, v96, v96
	v_fmac_f32_e32 v35, v97, v97
	v_add_f32_e32 v34, v35, v34
	s_ashr_i32 s25, s24, 31
	s_lshl_b64 s[0:1], s[24:25], 10
	v_add_f32_dpp v34, v34, v34 quad_perm:[1,0,3,2] row_mask:0xf bank_mask:0xf bound_ctrl:1
	s_nop 1
	v_add_f32_dpp v34, v34, v34 quad_perm:[2,3,0,1] row_mask:0xf bank_mask:0xf bound_ctrl:1
	s_nop 1
	v_add_f32_dpp v34, v34, v34 row_ror:4 row_mask:0xf bank_mask:0xf bound_ctrl:1
	s_nop 1
	v_add_f32_dpp v34, v34, v34 row_ror:8 row_mask:0xf bank_mask:0xf bound_ctrl:1
	v_mov_b32_e32 v35, v34
	s_nop 1
	v_permlane16_swap_b32_e32 v34, v35
	v_add_f32_e32 v34, v34, v35
	v_mov_b32_e32 v35, v34
	s_nop 1
	v_permlane32_swap_b32_e32 v34, v35
	v_add_f32_e32 v34, v34, v35
	v_mul_f32_e32 v35, 0x3a800000, v34
	v_mul_f32_e32 v36, 0x4f800000, v35
	v_cmp_gt_f32_e32 vcc, s44, v35
	s_nop 1
	v_cndmask_b32_e32 v35, v35, v36, vcc
	v_sqrt_f32_e32 v36, v35
	s_nop 0
	v_add_u32_e32 v37, -1, v36
	v_fma_f32 v38, -v37, v36, v35
	v_cmp_ge_f32_e64 s[8:9], 0, v38
	v_add_u32_e32 v38, 1, v36
	s_nop 0
	v_cndmask_b32_e64 v37, v36, v37, s[8:9]
	v_fma_f32 v36, -v38, v36, v35
	v_cmp_lt_f32_e64 s[8:9], 0, v36
	s_nop 1
	v_cndmask_b32_e64 v36, v37, v38, s[8:9]
	v_mul_f32_e32 v37, 0x37800000, v36
	v_cndmask_b32_e32 v36, v36, v37, vcc
	v_cmp_class_f32_e32 vcc, v35, v147
	s_nop 1
	v_cndmask_b32_e32 v35, v36, v35, vcc
	v_mul_f32_e32 v35, 0x3eab9f56, v35
	v_cmp_lt_f32_e32 vcc, 0, v34
	s_nop 1
	v_cndmask_b32_e32 v34, 1.0, v35, vcc
	v_rcp_f32_e32 v35, v34
	s_nop 0
	v_mul_f32_e32 v36, v78, v35
	v_mul_f32_e32 v39, v81, v35
	v_mul_f32_e32 v43, v89, v35
	v_floor_f32_e32 v36, v36
	v_mul_f32_e32 v37, v79, v35
	v_mul_f32_e32 v38, v80, v35
	v_floor_f32_e32 v39, v39
	v_mul_f32_e32 v42, v88, v35
	v_floor_f32_e32 v43, v43
	v_add_f32_e32 v36, 0x41000000, v36
	v_floor_f32_e32 v37, v37
	v_floor_f32_e32 v38, v38
	v_add_f32_e32 v39, 0x41000000, v39
	v_mul_f32_e32 v40, v86, v35
	v_mul_f32_e32 v41, v87, v35
	v_floor_f32_e32 v42, v42
	v_add_f32_e32 v43, 0x41000000, v43
	v_med3_f32 v36, v36, 0, v148
	v_add_f32_e32 v37, 0x41000000, v37
	v_add_f32_e32 v38, 0x41000000, v38
	v_med3_f32 v39, v39, 0, v148
	v_floor_f32_e32 v40, v40
	v_floor_f32_e32 v41, v41
	v_add_f32_e32 v42, 0x41000000, v42
	v_med3_f32 v43, v43, 0, v148
	v_mul_f32_e32 v44, v90, v35
	v_mul_f32_e32 v45, v91, v35
	v_mul_f32_e32 v46, v92, v35
	v_mul_f32_e32 v47, v93, v35
	v_mul_f32_e32 v48, v94, v35
	v_mul_f32_e32 v49, v95, v35
	v_mul_f32_e32 v50, v96, v35
	v_mul_f32_e32 v35, v97, v35
	v_cvt_u32_f32_e32 v36, v36
	v_med3_f32 v37, v37, 0, v148
	v_med3_f32 v38, v38, 0, v148
	v_cvt_u32_f32_e32 v39, v39
	v_add_f32_e32 v40, 0x41000000, v40
	v_add_f32_e32 v41, 0x41000000, v41
	v_med3_f32 v42, v42, 0, v148
	v_cvt_u32_f32_e32 v43, v43
	v_floor_f32_e32 v44, v44
	v_floor_f32_e32 v47, v47
	v_floor_f32_e32 v35, v35
	v_cvt_u32_f32_e32 v37, v37
	v_cvt_u32_f32_sdwa v38, v38 dst_sel:WORD_1 dst_unused:UNUSED_PAD src0_sel:DWORD
	v_med3_f32 v40, v40, 0, v148
	v_med3_f32 v41, v41, 0, v148
	v_cvt_u32_f32_e32 v42, v42
	v_add_f32_e32 v44, 0x41000000, v44
	v_floor_f32_e32 v45, v45
	v_floor_f32_e32 v46, v46
	v_add_f32_e32 v47, 0x41000000, v47
	v_floor_f32_e32 v50, v50
	v_add_f32_e32 v35, 0x41000000, v35
	v_cvt_u32_f32_e32 v40, v40
	v_cvt_u32_f32_e32 v41, v41
	v_med3_f32 v44, v44, 0, v148
	v_add_f32_e32 v45, 0x41000000, v45
	v_add_f32_e32 v46, 0x41000000, v46
	v_med3_f32 v47, v47, 0, v148
	v_floor_f32_e32 v48, v48
	v_floor_f32_e32 v49, v49
	v_add_f32_e32 v50, 0x41000000, v50
	v_med3_f32 v35, v35, 0, v148
	v_cvt_u32_f32_e32 v44, v44
	v_med3_f32 v45, v45, 0, v148
	v_med3_f32 v46, v46, 0, v148
	v_cvt_u32_f32_e32 v47, v47
	v_add_f32_e32 v48, 0x41000000, v48
	v_add_f32_e32 v49, 0x41000000, v49
	v_med3_f32 v50, v50, 0, v148
	v_cvt_u32_f32_e32 v35, v35
	v_cvt_u32_f32_e32 v45, v45
	v_cvt_u32_f32_sdwa v46, v46 dst_sel:WORD_1 dst_unused:UNUSED_PAD src0_sel:DWORD
	v_med3_f32 v48, v48, 0, v148
	v_med3_f32 v49, v49, 0, v148
	v_cvt_u32_f32_e32 v50, v50
	v_lshlrev_b32_e32 v43, 28, v43
	v_lshl_or_b32 v36, v39, 24, v36
	v_cvt_u32_f32_e32 v48, v48
	v_cvt_u32_f32_e32 v49, v49
	v_lshlrev_b32_e32 v37, 8, v37
	v_lshlrev_b32_e32 v42, 20, v42
	v_or3_b32 v36, v36, v43, v38
	v_lshlrev_b32_e32 v40, 4, v40
	v_lshlrev_b32_e32 v41, 12, v41
	v_or3_b32 v36, v36, v42, v37
	v_or3_b32 v36, v36, v41, v40
	v_lshlrev_b32_e32 v35, 28, v35
	v_lshl_or_b32 v41, v47, 24, v44
	v_lshlrev_b32_e32 v39, 8, v45
	v_lshlrev_b32_e32 v40, 20, v50
	v_or3_b32 v35, v41, v35, v46
	v_lshlrev_b32_e32 v37, 4, v48
	v_lshlrev_b32_e32 v38, 12, v49
	v_or3_b32 v35, v35, v40, v39
	v_or3_b32 v37, v35, v38, v37
	v_lshl_add_u64 v[38:39], v[134:135], 0, s[0:1]
	global_store_dwordx2 v[38:39], v[36:37], off
	s_and_saveexec_b64 s[0:1], s[2:3]
	s_cbranch_execz .LBB0_929
	s_lshl_b64 s[4:5], s[24:25], 3
	s_add_u32 s4, s34, s4
	s_addc_u32 s5, s35, s5
	global_store_dword v127, v34, s[4:5] offset:4

; __device__ __forceinline__ void qrow_load(f32x4 (&v)[4], const float* __restrict__ src, int row, int lane) {
; #pragma unroll
;     for (int j = 0; j < 4; ++j) v[j] = __builtin_nontemporal_load((const f32x4*)(src + (size_t)row * 1024 + 256 * j + 4 * lane));
; }
; template <bool SIGNED4> __device__ __forceinline__ void qrow_store(const f32x4 (&v)[4], unsigned char* q, float* scale, int row, int lane) {
;     float ss = 0.f;
; #pragma unroll
;     for (int j = 0; j < 4; ++j) ss += v[j].x * v[j].x + v[j].y * v[j].y + v[j].z * v[j].z + v[j].w * v[j].w;
;     ss = wave_sum(ss);
;     const float sc = ss > 0.f ? 0.3352f * sqrtf(ss * (1.f / 1024.f)) : 1.f, inv = __builtin_amdgcn_rcpf(sc);
;     unsigned n[16];
; #pragma unroll
;     for (int j = 0; j < 4; ++j) {
; #pragma unroll
;         for (int i = 0; i < 4; ++i) { const float f = floorf(v[j][i] * inv) + 8.f; n[4 * j + i] = (unsigned)fminf(fmaxf(f, 0.f), 15.f); } }
;     u32x2 o;
; #pragma unroll
;     for (int m = 0; m < 2; ++m) { unsigned w = 0;
; #pragma unroll
;         for (int b = 0; b < 4; ++b) w |= (n[8 * m + b] | (n[8 * m + 4 + b] << 4)) << (8 * b);
;         o[m] = SIGNED4 ? (w ^ 0x88888888u) : w; }
;     *(u32x2*)(q + (size_t)row * 1024 + lane * 16) = o;
;     if (lane == 0) scale[row] = sc;
; }
; __global__ void __launch_bounds__(NTHREADS, 2) mega(Args a) {
;     ...
;         }
;         for (; qi < qrows; ++qi) { const int r = gw * qrows + qi; if (r < NEXP) { f32x4 qa[4]; qrow_load(qa, U, r, lane); qrow_store<true>(qa, ws + WS_UQ, (float*)(ws + WS_US), r, lane); qrow_load(qa, V, r, lane); qrow_store<false>(qa, ws + WS_UQ + 8, (float*)(ws + WS_VS), r, lane); } }
.LBB0_933:
	s_cmp_ge_i32 s22, s28
	s_cbranch_scc1 .LBB0_942
	s_add_i32 s0, s22, s29
	s_ashr_i32 s1, s0, 31
	s_lshl_b64 s[4:5], s[0:1], 3
	s_add_u32 s4, s20, s4
	s_addc_u32 s5, s21, s5
	s_add_u32 s4, s4, 0x1100004
	s_addc_u32 s5, s5, 0
	s_lshl_b64 s[6:7], s[0:1], 10
	s_add_u32 s8, s20, s6
	s_addc_u32 s9, s21, s7
	s_lshl_b64 s[0:1], s[0:1], 12
	s_add_u32 s10, s16, s0
	s_addc_u32 s11, s17, s1
	s_add_u32 s12, s18, s0
	v_mov_b32_e32 v127, 0
	v_cmp_eq_u32_e64 s[2:3], 0, v1
	s_addc_u32 s13, s19, s1
	s_mov_b32 s16, 0xf800000
	v_mov_b32_e32 v1, 0x260
	s_mov_b32 s17, 0x88888888
	v_mov_b32_e32 v4, 0x41700000
	s_branch .LBB0_937

; __device__ __forceinline__ void qrow_load(f32x4 (&v)[4], const float* __restrict__ src, int row, int lane) {
; #pragma unroll
;     for (int j = 0; j < 4; ++j) v[j] = __builtin_nontemporal_load((const f32x4*)(src + (size_t)row * 1024 + 256 * j + 4 * lane));
; }
; template <bool SIGNED4> __device__ __forceinline__ void qrow_store(const f32x4 (&v)[4], unsigned char* q, float* scale, int row, int lane) {
;     float ss = 0.f;
; #pragma unroll
;     for (int j = 0; j < 4; ++j) ss += v[j].x * v[j].x + v[j].y * v[j].y + v[j].z * v[j].z + v[j].w * v[j].w;
;     ss = wave_sum(ss);
;     const float sc = ss > 0.f ? 0.3352f * sqrtf(ss * (1.f / 1024.f)) : 1.f, inv = __builtin_amdgcn_rcpf(sc);
;     unsigned n[16];
; #pragma unroll
;     for (int j = 0; j < 4; ++j) {
; #pragma unroll
;         for (int i = 0; i < 4; ++i) { const float f = floorf(v[j][i] * inv) + 8.f; n[4 * j + i] = (unsigned)fminf(fmaxf(f, 0.f), 15.f); } }
;     u32x2 o;
; #pragma unroll
;     for (int m = 0; m < 2; ++m) { unsigned w = 0;
; #pragma unroll
;         for (int b = 0; b < 4; ++b) w |= (n[8 * m + b] | (n[8 * m + 4 + b] << 4)) << (8 * b);
;         o[m] = SIGNED4 ? (w ^ 0x88888888u) : w; }
;     *(u32x2*)(q + (size_t)row * 1024 + lane * 16) = o;
;     if (lane == 0) scale[row] = sc;
; }
; __global__ void __launch_bounds__(NTHREADS, 2) mega(Args a) {
;     ...
;         for (; qi < qrows; ++qi) { const int r = gw * qrows + qi; if (r < NEXP) { f32x4 qa[4]; qrow_load(qa, U, r, lane); qrow_store<true>(qa, ws + WS_UQ, (float*)(ws + WS_US), r, lane); qrow_load(qa, V, r, lane); qrow_store<false>(qa, ws + WS_UQ + 8, (float*)(ws + WS_VS), r, lane); } }
.LBB0_936:
	s_add_i32 s22, s22, 1
	s_add_u32 s4, s4, 8
	s_addc_u32 s5, s5, 0
	s_add_u32 s8, s8, 0x400
	s_addc_u32 s9, s9, 0
	s_add_u32 s10, s10, 0x1000
	s_addc_u32 s11, s11, 0
	s_add_u32 s12, s12, 0x1000
	s_addc_u32 s13, s13, 0
	s_cmp_lt_i32 s22, s28
	s_cbranch_scc0 .LBB0_942
.LBB0_937:
	s_add_i32 s0, s29, s22
	s_cmpk_gt_i32 s0, 0x3fff
	s_cbranch_scc1 .LBB0_936
	v_lshl_add_u64 v[2:3], s[10:11], 0, v[126:127]
	global_load_dwordx4 v[6:9], v[2:3], off nt
	global_load_dwordx4 v[10:13], v[2:3], off offset:1024 nt
	global_load_dwordx4 v[14:17], v[2:3], off offset:2048 nt
	global_load_dwordx4 v[18:21], v[2:3], off offset:3072 nt
	s_waitcnt vmcnt(3)
	v_mul_f32_e32 v2, v7, v7
	s_waitcnt vmcnt(2)
	v_mul_f32_e32 v3, v11, v11
	s_waitcnt vmcnt(1)
	v_mul_f32_e32 v5, v15, v15
	v_fmac_f32_e32 v2, v6, v6
	v_fmac_f32_e32 v3, v10, v10
	s_waitcnt vmcnt(0)
	v_mul_f32_e32 v22, v19, v19
	v_fmac_f32_e32 v5, v14, v14
	v_fmac_f32_e32 v2, v8, v8
	v_fmac_f32_e32 v3, v12, v12
	v_fmac_f32_e32 v22, v18, v18
	v_fmac_f32_e32 v5, v16, v16
	v_fmac_f32_e32 v2, v9, v9
	v_fmac_f32_e32 v3, v13, v13
	v_fmac_f32_e32 v22, v20, v20
	v_fmac_f32_e32 v5, v17, v17
	v_add_f32_e32 v2, v2, v3
	v_fmac_f32_e32 v22, v21, v21
	v_add_f32_e32 v2, v2, v5
	v_add_f32_e32 v2, v2, v22
	s_nop 1
	v_add_f32_dpp v2, v2, v2 quad_perm:[1,0,3,2] row_mask:0xf bank_mask:0xf bound_ctrl:1
	s_nop 1
	v_add_f32_dpp v2, v2, v2 quad_perm:[2,3,0,1] row_mask:0xf bank_mask:0xf bound_ctrl:1
	s_nop 1
	v_add_f32_dpp v2, v2, v2 row_ror:4 row_mask:0xf bank_mask:0xf bound_ctrl:1
	s_nop 1
	v_add_f32_dpp v2, v2, v2 row_ror:8 row_mask:0xf bank_mask:0xf bound_ctrl:1
	v_mov_b32_e32 v3, v2
	s_nop 1
	v_permlane16_swap_b32_e32 v2, v3
	v_add_f32_e32 v2, v2, v3
	v_mov_b32_e32 v3, v2
	s_nop 1
	v_permlane32_swap_b32_e32 v2, v3
	v_add_f32_e32 v2, v2, v3
	v_mul_f32_e32 v3, 0x3a800000, v2
	v_mul_f32_e32 v5, 0x4f800000, v3
	v_cmp_gt_f32_e32 vcc, s16, v3
	s_nop 1
	v_cndmask_b32_e32 v3, v3, v5, vcc
	v_sqrt_f32_e32 v5, v3
	s_nop 0
	v_add_u32_e32 v22, -1, v5
	v_add_u32_e32 v23, 1, v5
	v_fma_f32 v24, -v22, v5, v3
	v_fma_f32 v25, -v23, v5, v3
	v_cmp_ge_f32_e64 s[6:7], 0, v24
	s_nop 1
	v_cndmask_b32_e64 v5, v5, v22, s[6:7]
	v_cmp_lt_f32_e64 s[6:7], 0, v25
	s_nop 1
	v_cndmask_b32_e64 v5, v5, v23, s[6:7]
	v_mul_f32_e32 v22, 0x37800000, v5
	v_cndmask_b32_e32 v5, v5, v22, vcc
	v_cmp_class_f32_e32 vcc, v3, v1
	s_nop 1
	v_cndmask_b32_e32 v3, v5, v3, vcc
	v_mul_f32_e32 v3, 0x3eab9f56, v3
	v_cmp_lt_f32_e32 vcc, 0, v2
	s_nop 1
	v_cndmask_b32_e32 v5, 1.0, v3, vcc
	v_rcp_f32_e32 v2, v5
	s_nop 0
	v_mul_f32_e32 v3, v6, v2
	v_mul_f32_e32 v6, v7, v2
	v_mul_f32_e32 v7, v8, v2
	v_mul_f32_e32 v8, v9, v2
	v_mul_f32_e32 v9, v10, v2
	v_mul_f32_e32 v10, v11, v2
	v_mul_f32_e32 v11, v12, v2
	v_mul_f32_e32 v12, v13, v2
	v_floor_f32_e32 v12, v12
	v_floor_f32_e32 v3, v3
	v_floor_f32_e32 v8, v8
	v_floor_f32_e32 v11, v11
	v_add_f32_e32 v12, 0x41000000, v12
	v_mul_f32_e32 v13, v14, v2
	v_mul_f32_e32 v14, v15, v2
	v_mul_f32_e32 v15, v16, v2
	v_mul_f32_e32 v16, v17, v2
	v_mul_f32_e32 v17, v18, v2
	v_mul_f32_e32 v18, v19, v2
	v_floor_f32_e32 v6, v6
	v_floor_f32_e32 v7, v7
	v_floor_f32_e32 v10, v10
	v_add_f32_e32 v3, 0x41000000, v3
	v_add_f32_e32 v8, 0x41000000, v8
	v_add_f32_e32 v11, 0x41000000, v11
	v_med3_f32 v12, v12, 0, v4
	v_mul_f32_e32 v19, v20, v2
	v_mul_f32_e32 v2, v21, v2
	v_floor_f32_e32 v9, v9
	v_add_f32_e32 v6, 0x41000000, v6
	v_add_f32_e32 v7, 0x41000000, v7
	v_add_f32_e32 v10, 0x41000000, v10
	v_med3_f32 v3, v3, 0, v4
	v_med3_f32 v8, v8, 0, v4
	v_med3_f32 v11, v11, 0, v4
	v_cvt_u32_f32_e32 v12, v12
	v_floor_f32_e32 v2, v2
	v_floor_f32_e32 v13, v13
	v_floor_f32_e32 v16, v16
	v_add_f32_e32 v9, 0x41000000, v9
	v_med3_f32 v6, v6, 0, v4
	v_med3_f32 v7, v7, 0, v4
	v_med3_f32 v10, v10, 0, v4
	v_cvt_u32_f32_e32 v3, v3
	v_cvt_u32_f32_sdwa v8, v8 dst_sel:BYTE_3 dst_unused:UNUSED_PAD src0_sel:DWORD
	v_cvt_u32_f32_e32 v11, v11
	v_floor_f32_e32 v19, v19
	v_add_f32_e32 v2, 0x41000000, v2
	v_floor_f32_e32 v14, v14
	v_floor_f32_e32 v15, v15
	v_add_f32_e32 v13, 0x41000000, v13
	v_add_f32_e32 v16, 0x41000000, v16
	v_med3_f32 v9, v9, 0, v4
	v_cvt_u32_f32_e32 v6, v6
	v_cvt_u32_f32_sdwa v7, v7 dst_sel:WORD_1 dst_unused:UNUSED_PAD src0_sel:DWORD
	v_cvt_u32_f32_e32 v10, v10
	v_floor_f32_e32 v18, v18
	v_add_f32_e32 v19, 0x41000000, v19
	v_med3_f32 v2, v2, 0, v4
	v_floor_f32_e32 v17, v17
	v_add_f32_e32 v14, 0x41000000, v14
	v_add_f32_e32 v15, 0x41000000, v15
	v_med3_f32 v13, v13, 0, v4
	v_med3_f32 v16, v16, 0, v4
	v_cvt_u32_f32_e32 v9, v9
	v_add_f32_e32 v18, 0x41000000, v18
	v_med3_f32 v19, v19, 0, v4
	v_cvt_u32_f32_e32 v2, v2
	v_add_f32_e32 v17, 0x41000000, v17
	v_med3_f32 v14, v14, 0, v4
	v_med3_f32 v15, v15, 0, v4
	v_cvt_u32_f32_e32 v13, v13
	v_cvt_u32_f32_sdwa v16, v16 dst_sel:BYTE_3 dst_unused:UNUSED_PAD src0_sel:DWORD
	v_med3_f32 v18, v18, 0, v4
	v_cvt_u32_f32_e32 v19, v19
	v_lshlrev_b32_e32 v12, 28, v12
	v_med3_f32 v17, v17, 0, v4
	v_cvt_u32_f32_e32 v14, v14
	v_cvt_u32_f32_sdwa v15, v15 dst_sel:WORD_1 dst_unused:UNUSED_PAD src0_sel:DWORD
	v_cvt_u32_f32_e32 v18, v18
	v_lshlrev_b32_e32 v11, 20, v11
	v_or3_b32 v3, v8, v3, v12
	v_cvt_u32_f32_e32 v17, v17
	v_lshlrev_b32_e32 v10, 12, v10
	v_lshlrev_b32_e32 v6, 8, v6
	v_or3_b32 v3, v3, v7, v11
	v_lshlrev_b32_e32 v9, 4, v9
	v_or3_b32 v3, v3, v6, v10
	v_lshlrev_b32_e32 v2, 28, v2
	v_bitop3_b32 v6, v3, s17, v9 bitop3:0x36
	v_lshlrev_b32_e32 v9, 20, v19
	v_or3_b32 v2, v16, v13, v2
	v_lshlrev_b32_e32 v7, 12, v18
	v_lshlrev_b32_e32 v8, 8, v14
	v_or3_b32 v2, v2, v15, v9
	v_lshlrev_b32_e32 v3, 4, v17
	v_or3_b32 v2, v2, v8, v7
	v_bitop3_b32 v7, v2, s17, v3 bitop3:0x36
	v_lshl_add_u64 v[2:3], s[8:9], 0, v[126:127]
	v_add_co_u32_e32 v8, vcc, 0x1200000, v2
	s_nop 1
	v_addc_co_u32_e32 v9, vcc, 0, v3, vcc
	global_store_dwordx2 v[8:9], v[6:7], off
	s_and_saveexec_b64 s[0:1], s[2:3]
	s_cbranch_execz .LBB0_940
	s_add_u32 s6, s4, -4
	s_addc_u32 s7, s5, -1
	global_store_dword v127, v5, s[6:7]

; #define LAS __attribute__((address_space(3)))
; #define EXP_XROW(tt) do { const char* g_ = (const char*)(xin + (size_t)(tt) * 1024) + lane * 16; LAS unsigned char* l_ = xslot + ((tt) & 1) * 2048; \
;         __builtin_amdgcn_global_load_lds((const unsigned*)g_, (LAS unsigned*)l_, 16, 0, 2); __builtin_amdgcn_global_load_lds((const unsigned*)(g_ + 1024), (LAS unsigned*)(l_ + 1024), 16, 0, 2); } while (0)
; __device__ __forceinline__ void expert_tokens(const unsigned char* __restrict__ UV, const float* __restrict__ US, const float* __restrict__ VS, ...
;     if (t0 >= t1) return;
;     const unsigned lo16 = (unsigned)lane * 16u;
;     const int el = ((lane >> 5) & 1) * 8 + ((lane >> 4) & 1) * 4 + ((lane >> 1) & 1) * 2 + (lane & 1);
;     const unsigned cw0 = (unsigned)IDX[(size_t)t0 * 128 + lane], cw1 = (unsigned)IDX[(size_t)t0 * 128 + 64 + lane];
;     int ci0 = (int)cw0 & rmask, ci1 = (int)cw1 & rmask;
;     float cg0 = __uint_as_float(cw0 & 0xFFFF0000u), cg1 = __uint_as_float(cw1 & 0xFFFF0000u);
;     float csu0 = US[ci0], csu1 = US[ci1], csv0 = VS[ci0], csv1 = VS[ci1];
;     ...
;     EXP_XROW(t0);
; __global__ void __launch_bounds__(NTHREADS, 2) mega(Args a) {
;     ...
;                 const int tpw = (T + NGW - 1) / NGW, tb0 = vcu * NWAVES * tpw, b = (tb0 < T ? tb0 : 0) / SEQ;
;                 LAS float* pv = (LAS float*)lds; const float* md = MOD + b * 6144; const float* g_pre = ka->in[11]; const float* g_post = ka->in[12];
;                 for (int i = tid; i < 1024; i += NTHREADS) { pv[i] = g_pre[i] * (md[4096 + i] + 1.f); pv[1024 + i] = md[3072 + i]; pv[2048 + i] = md[5120 + i] * g_post[i]; }
;                 __syncthreads();
;                 const int t0 = gw * tpw, t1 = (t0 + tpw < T) ? t0 + tpw : T;
;                 if (rep_ == 0 && DUP_MODE == 2) { for (int t = t0; t < t1; ++t) gather_only_token((const unsigned char*)(ws + WS_UQ), IDX, outp, t, lane); } else
;                 expert_tokens((const unsigned char*)(ws + WS_UQ), (const float*)(ws + WS_US), (const float*)(ws + WS_VS), IDX, GATE, pv, (const bf16_t*)(ws + WS_HST), lds + 16384 + wave * 4096, outp, t0, t1, lane, rmask, pd);
.LBB0_1011:
	s_or_b64 exec, exec, s[12:13]
	s_waitcnt lgkmcnt(0)
	s_mul_i32 s8, s24, s96
	s_add_i32 s0, s8, s24
	s_min_i32 s17, s0, 0x8000
	s_sub_i32 s77, s96, s95
	s_add_i32 s77, s77, 8
	s_mul_i32 s77, s77, s24
	s_cmp_le_i32 s77, 0x8000
	s_cselect_b32 s77, 1, 0
	s_cmp_ge_i32 s8, s17
	s_waitcnt vmcnt(0)
	s_barrier
	s_cbranch_scc1 .LBB0_1025
	s_add_u32 s0, s6, 0xf800000
	s_addc_u32 s1, s7, 0
	s_add_u32 s10, s6, 0x1200000
	s_addc_u32 s11, s7, 0
	s_add_u32 s12, s6, 0x1100000
	s_addc_u32 s13, s7, 0
	s_add_u32 s14, s6, 0x1140000
	s_addc_u32 s15, s7, 0
	s_lshl_b32 s2, s95, 12
	s_add_i32 s26, s2, 0
	s_add_u32 s2, s6, 0x1b800000
	s_addc_u32 s3, s7, 0
	s_ashr_i32 s9, s8, 31
	s_lshl_b64 s[6:7], s[8:9], 9
	v_and_b32_e32 v74, 63, v0
	s_add_u32 s6, s0, s6
	s_addc_u32 s7, s1, s7
	v_lshlrev_b32_e32 v192, 2, v74
	global_load_dword v229, v192, s[6:7]
	global_load_dword v230, v192, s[6:7] offset:256
	s_lshl_b64 s[18:19], s[8:9], 11
	s_add_u32 s18, s2, s18
	s_addc_u32 s19, s3, s19
	s_lshl_b32 s9, s8, 11
	v_mov_b32_e32 v1, 0
	s_and_b32 s9, s9, 0x800
	v_lshlrev_b32_e32 v194, 4, v74
	v_mov_b32_e32 v195, v1
	s_add_i32 s9, s26, s9
	s_mov_b64 s[6:7], 0x400
	v_lshl_add_u64 v[2:3], s[18:19], 0, v[194:195]
	s_add_i32 m0, s9, 0x4000
	v_lshl_add_u64 v[2:3], v[2:3], 0, s[6:7]
	global_load_lds_dwordx4 v194, s[18:19] nt
	s_add_i32 m0, s9, 0x4400
	v_mov_b32_e32 v193, v1
	global_load_lds_dwordx4 v[2:3], off nt
	v_and_b32_e32 v77, 2, v0
	v_lshl_add_u64 v[196:197], s[0:1], 0, v[192:193]
	v_lshl_add_u64 v[198:199], s[2:3], 0, v[194:195]
	v_cmp_eq_u32_e64 s[0:1], 0, v77
	v_lshl_add_u64 v[200:201], s[4:5], 0, v[194:195]
	v_lshl_add_u32 v195, v74, 3, s26
	v_mov_b32_e32 v226, 0x358637bd
	v_mov_b32_e32 v227, 0xbf3a00e3
	s_waitcnt vmcnt(0)
	v_alignbit_b32 v229, v229, v229, 16
	v_alignbit_b32 v230, v230, v230, 16
	s_nop 1
	s_mov_b32 s58, 0x99999999
	s_mov_b32 s59, 0x99999999
	v_min_u32_dpp v202, v229, v229 quad_perm:[1,0,3,2] row_mask:0xf bank_mask:0xf
	v_max_u32_dpp v203, v229, v229 quad_perm:[1,0,3,2] row_mask:0xf bank_mask:0xf
	v_min_u32_dpp v204, v230, v230 quad_perm:[1,0,3,2] row_mask:0xf bank_mask:0xf
	v_max_u32_dpp v205, v230, v230 quad_perm:[1,0,3,2] row_mask:0xf bank_mask:0xf
	v_cndmask_b32_e64 v229, v203, v202, s[58:59]
	v_cndmask_b32_e64 v230, v205, v204, s[58:59]
	s_mov_b32 s58, 0xcc33cc33
	s_mov_b32 s59, 0xcc33cc33
	v_min_u32_dpp v202, v229, v229 quad_perm:[2,3,0,1] row_mask:0xf bank_mask:0xf
	v_max_u32_dpp v203, v229, v229 quad_perm:[2,3,0,1] row_mask:0xf bank_mask:0xf
	v_min_u32_dpp v204, v230, v230 quad_perm:[2,3,0,1] row_mask:0xf bank_mask:0xf
	v_max_u32_dpp v205, v230, v230 quad_perm:[2,3,0,1] row_mask:0xf bank_mask:0xf
	v_cndmask_b32_e64 v229, v203, v202, s[58:59]
	v_cndmask_b32_e64 v230, v205, v204, s[58:59]
	s_mov_b32 s58, 0xaa55aa55
	s_mov_b32 s59, 0xaa55aa55
	v_min_u32_dpp v202, v229, v229 quad_perm:[1,0,3,2] row_mask:0xf bank_mask:0xf
	v_max_u32_dpp v203, v229, v229 quad_perm:[1,0,3,2] row_mask:0xf bank_mask:0xf
	v_min_u32_dpp v204, v230, v230 quad_perm:[1,0,3,2] row_mask:0xf bank_mask:0xf
	v_max_u32_dpp v205, v230, v230 quad_perm:[1,0,3,2] row_mask:0xf bank_mask:0xf
	v_cndmask_b32_e64 v229, v203, v202, s[58:59]
	v_cndmask_b32_e64 v230, v205, v204, s[58:59]
	s_mov_b32 s58, 0xf00ff00f
	s_mov_b32 s59, 0xf00ff00f
	v_min_u32_dpp v202, v229, v229 row_ror:8 row_mask:0xf bank_mask:0xf
	v_max_u32_dpp v203, v229, v229 row_ror:8 row_mask:0xf bank_mask:0xf
	v_min_u32_dpp v204, v230, v230 row_ror:8 row_mask:0xf bank_mask:0xf
	v_max_u32_dpp v205, v230, v230 row_ror:8 row_mask:0xf bank_mask:0xf
	v_cndmask_b32_e64 v229, v203, v202, s[58:59]
	v_cndmask_b32_e64 v230, v205, v204, s[58:59]
	s_mov_b32 s58, 0xc3c3c3c3
	s_mov_b32 s59, 0xc3c3c3c3
	v_min_u32_dpp v202, v229, v229 quad_perm:[2,3,0,1] row_mask:0xf bank_mask:0xf
	v_max_u32_dpp v203, v229, v229 quad_perm:[2,3,0,1] row_mask:0xf bank_mask:0xf
	v_min_u32_dpp v204, v230, v230 quad_perm:[2,3,0,1] row_mask:0xf bank_mask:0xf
	v_max_u32_dpp v205, v230, v230 quad_perm:[2,3,0,1] row_mask:0xf bank_mask:0xf
	v_cndmask_b32_e64 v229, v203, v202, s[58:59]
	v_cndmask_b32_e64 v230, v205, v204, s[58:59]
	s_mov_b32 s58, 0xa5a5a5a5
	s_mov_b32 s59, 0xa5a5a5a5
	v_min_u32_dpp v202, v229, v229 quad_perm:[1,0,3,2] row_mask:0xf bank_mask:0xf
	v_max_u32_dpp v203, v229, v229 quad_perm:[1,0,3,2] row_mask:0xf bank_mask:0xf
	v_min_u32_dpp v204, v230, v230 quad_perm:[1,0,3,2] row_mask:0xf bank_mask:0xf
	v_max_u32_dpp v205, v230, v230 quad_perm:[1,0,3,2] row_mask:0xf bank_mask:0xf
	v_cndmask_b32_e64 v229, v203, v202, s[58:59]
	v_cndmask_b32_e64 v230, v205, v204, s[58:59]
	s_mov_b32 s58, 0xf0f00f0f
	s_mov_b32 s59, 0xf0f00f0f
	v_mov_b32_dpp v202, v229 row_half_mirror row_mask:0xf bank_mask:0xf
	v_mov_b32_dpp v204, v230 row_half_mirror row_mask:0xf bank_mask:0xf
	s_nop 0
	v_max_u32_dpp v203, v202, v229 quad_perm:[3,2,1,0] row_mask:0xf bank_mask:0xf
	v_max_u32_dpp v205, v204, v230 quad_perm:[3,2,1,0] row_mask:0xf bank_mask:0xf
	v_min_u32_dpp v202, v202, v229 quad_perm:[3,2,1,0] row_mask:0xf bank_mask:0xf
	v_min_u32_dpp v204, v204, v230 quad_perm:[3,2,1,0] row_mask:0xf bank_mask:0xf
	v_cndmask_b32_e64 v229, v203, v202, s[58:59]
	v_cndmask_b32_e64 v230, v205, v204, s[58:59]
	s_mov_b32 s58, 0xff0000ff
	s_mov_b32 s59, 0xff0000ff
	v_min_u32_dpp v202, v229, v229 row_ror:8 row_mask:0xf bank_mask:0xf
	v_max_u32_dpp v203, v229, v229 row_ror:8 row_mask:0xf bank_mask:0xf
	v_min_u32_dpp v204, v230, v230 row_ror:8 row_mask:0xf bank_mask:0xf
	v_max_u32_dpp v205, v230, v230 row_ror:8 row_mask:0xf bank_mask:0xf
	v_cndmask_b32_e64 v229, v203, v202, s[58:59]
	v_cndmask_b32_e64 v230, v205, v204, s[58:59]
	s_mov_b32 s58, 0xcccc3333
	s_mov_b32 s59, 0xcccc3333
; __device__ __forceinline__ void expert_tokens(const unsigned char* __restrict__ UV, const float* __restrict__ US, const float* __restrict__ VS, ...
;     ...
;     const unsigned cw0 = (unsigned)IDX[(size_t)t0 * 128 + lane], cw1 = (unsigned)IDX[(size_t)t0 * 128 + 64 + lane];
;     int ci0 = (int)cw0 & rmask, ci1 = (int)cw1 & rmask;
	v_min_u32_dpp v202, v229, v229 quad_perm:[2,3,0,1] row_mask:0xf bank_mask:0xf
	v_max_u32_dpp v203, v229, v229 quad_perm:[2,3,0,1] row_mask:0xf bank_mask:0xf
	v_min_u32_dpp v204, v230, v230 quad_perm:[2,3,0,1] row_mask:0xf bank_mask:0xf
	v_max_u32_dpp v205, v230, v230 quad_perm:[2,3,0,1] row_mask:0xf bank_mask:0xf
	v_cndmask_b32_e64 v229, v203, v202, s[58:59]
	v_cndmask_b32_e64 v230, v205, v204, s[58:59]
	s_mov_b32 s58, 0xaaaa5555
	s_mov_b32 s59, 0xaaaa5555
	v_min_u32_dpp v202, v229, v229 quad_perm:[1,0,3,2] row_mask:0xf bank_mask:0xf
	v_max_u32_dpp v203, v229, v229 quad_perm:[1,0,3,2] row_mask:0xf bank_mask:0xf
	v_min_u32_dpp v204, v230, v230 quad_perm:[1,0,3,2] row_mask:0xf bank_mask:0xf
	v_max_u32_dpp v205, v230, v230 quad_perm:[1,0,3,2] row_mask:0xf bank_mask:0xf
	v_cndmask_b32_e64 v229, v203, v202, s[58:59]
	v_cndmask_b32_e64 v230, v205, v204, s[58:59]
	s_nop 1
	v_permlane16_swap_b32_e32 v229, v230
	s_mov_b32 s58, -1
	s_mov_b32 s59, 0
	v_min_u32_e32 v202, v229, v230
	v_max_u32_e32 v203, v229, v230
	v_cndmask_b32_e64 v229, v203, v202, s[58:59]
	v_cndmask_b32_e64 v230, v202, v203, s[58:59]
	s_mov_b32 s58, 0xf0f0f0f
	s_mov_b32 s59, 0xf0f0f0f0
	v_mov_b32_dpp v202, v229 row_half_mirror row_mask:0xf bank_mask:0xf
	v_mov_b32_dpp v204, v230 row_half_mirror row_mask:0xf bank_mask:0xf
	s_nop 0
	v_max_u32_dpp v203, v202, v229 quad_perm:[3,2,1,0] row_mask:0xf bank_mask:0xf
	v_max_u32_dpp v205, v204, v230 quad_perm:[3,2,1,0] row_mask:0xf bank_mask:0xf
	v_min_u32_dpp v202, v202, v229 quad_perm:[3,2,1,0] row_mask:0xf bank_mask:0xf
	v_min_u32_dpp v204, v204, v230 quad_perm:[3,2,1,0] row_mask:0xf bank_mask:0xf
	v_cndmask_b32_e64 v229, v203, v202, s[58:59]
	v_cndmask_b32_e64 v230, v205, v204, s[58:59]
	s_mov_b32 s58, 0xff00ff
	s_mov_b32 s59, 0xff00ff00
	v_min_u32_dpp v202, v229, v229 row_ror:8 row_mask:0xf bank_mask:0xf
	v_max_u32_dpp v203, v229, v229 row_ror:8 row_mask:0xf bank_mask:0xf
	v_min_u32_dpp v204, v230, v230 row_ror:8 row_mask:0xf bank_mask:0xf
	v_max_u32_dpp v205, v230, v230 row_ror:8 row_mask:0xf bank_mask:0xf
	v_cndmask_b32_e64 v229, v203, v202, s[58:59]
	v_cndmask_b32_e64 v230, v205, v204, s[58:59]
	s_mov_b32 s58, 0x33333333
	s_mov_b32 s59, 0xcccccccc
	v_min_u32_dpp v202, v229, v229 quad_perm:[2,3,0,1] row_mask:0xf bank_mask:0xf
	v_max_u32_dpp v203, v229, v229 quad_perm:[2,3,0,1] row_mask:0xf bank_mask:0xf
	v_min_u32_dpp v204, v230, v230 quad_perm:[2,3,0,1] row_mask:0xf bank_mask:0xf
	v_max_u32_dpp v205, v230, v230 quad_perm:[2,3,0,1] row_mask:0xf bank_mask:0xf
	v_cndmask_b32_e64 v229, v203, v202, s[58:59]
	v_cndmask_b32_e64 v230, v205, v204, s[58:59]
	s_mov_b32 s58, 0x55555555
	s_mov_b32 s59, 0xaaaaaaaa
	v_min_u32_dpp v202, v229, v229 quad_perm:[1,0,3,2] row_mask:0xf bank_mask:0xf
	v_max_u32_dpp v203, v229, v229 quad_perm:[1,0,3,2] row_mask:0xf bank_mask:0xf
	v_min_u32_dpp v204, v230, v230 quad_perm:[1,0,3,2] row_mask:0xf bank_mask:0xf
	v_max_u32_dpp v205, v230, v230 quad_perm:[1,0,3,2] row_mask:0xf bank_mask:0xf
	v_cndmask_b32_e64 v229, v203, v202, s[58:59]
	v_cndmask_b32_e64 v230, v205, v204, s[58:59]
	s_nop 1
	v_permlane32_swap_b32_e32 v229, v230
	s_mov_b32 s58, 0xffff
	s_mov_b32 s59, 0xffff
	v_min_u32_e32 v202, v229, v230
	v_max_u32_e32 v203, v229, v230
	v_cndmask_b32_e64 v229, v203, v202, s[58:59]
	v_cndmask_b32_e64 v230, v202, v203, s[58:59]
	s_nop 1
	v_permlane32_swap_b32_e32 v229, v230
	s_mov_b32 s58, 0xffff
	s_mov_b32 s59, 0xffff
	v_min_u32_e32 v202, v229, v230
	v_max_u32_e32 v203, v229, v230
	v_cndmask_b32_e64 v229, v203, v202, s[58:59]
	v_cndmask_b32_e64 v230, v202, v203, s[58:59]
	s_mov_b32 s58, 0xf0f00f0f
	s_mov_b32 s59, 0xf0f00f0f
	v_mov_b32_dpp v202, v229 row_half_mirror row_mask:0xf bank_mask:0xf
	v_mov_b32_dpp v204, v230 row_half_mirror row_mask:0xf bank_mask:0xf
	s_nop 0
	v_max_u32_dpp v203, v202, v229 quad_perm:[3,2,1,0] row_mask:0xf bank_mask:0xf
	v_max_u32_dpp v205, v204, v230 quad_perm:[3,2,1,0] row_mask:0xf bank_mask:0xf
	v_min_u32_dpp v202, v202, v229 quad_perm:[3,2,1,0] row_mask:0xf bank_mask:0xf
	v_min_u32_dpp v204, v204, v230 quad_perm:[3,2,1,0] row_mask:0xf bank_mask:0xf
	v_cndmask_b32_e64 v229, v203, v202, s[58:59]
	v_cndmask_b32_e64 v230, v205, v204, s[58:59]
	s_mov_b32 s58, 0xff0000ff
	s_mov_b32 s59, 0xff0000ff
	v_min_u32_dpp v202, v229, v229 row_ror:8 row_mask:0xf bank_mask:0xf
	v_max_u32_dpp v203, v229, v229 row_ror:8 row_mask:0xf bank_mask:0xf
	v_min_u32_dpp v204, v230, v230 row_ror:8 row_mask:0xf bank_mask:0xf
	v_max_u32_dpp v205, v230, v230 row_ror:8 row_mask:0xf bank_mask:0xf
	v_cndmask_b32_e64 v229, v203, v202, s[58:59]
	v_cndmask_b32_e64 v230, v205, v204, s[58:59]
	s_mov_b32 s58, 0xcccc3333
	s_mov_b32 s59, 0xcccc3333
	v_min_u32_dpp v202, v229, v229 quad_perm:[2,3,0,1] row_mask:0xf bank_mask:0xf
	v_max_u32_dpp v203, v229, v229 quad_perm:[2,3,0,1] row_mask:0xf bank_mask:0xf
	v_min_u32_dpp v204, v230, v230 quad_perm:[2,3,0,1] row_mask:0xf bank_mask:0xf
	v_max_u32_dpp v205, v230, v230 quad_perm:[2,3,0,1] row_mask:0xf bank_mask:0xf
	v_cndmask_b32_e64 v229, v203, v202, s[58:59]
	v_cndmask_b32_e64 v230, v205, v204, s[58:59]
	s_mov_b32 s58, 0xaaaa5555
	s_mov_b32 s59, 0xaaaa5555
	v_min_u32_dpp v202, v229, v229 quad_perm:[1,0,3,2] row_mask:0xf bank_mask:0xf
	v_max_u32_dpp v203, v229, v229 quad_perm:[1,0,3,2] row_mask:0xf bank_mask:0xf
	v_min_u32_dpp v204, v230, v230 quad_perm:[1,0,3,2] row_mask:0xf bank_mask:0xf
	v_max_u32_dpp v205, v230, v230 quad_perm:[1,0,3,2] row_mask:0xf bank_mask:0xf
	v_cndmask_b32_e64 v229, v203, v202, s[58:59]
	v_cndmask_b32_e64 v230, v205, v204, s[58:59]
	s_nop 1
	v_permlane16_swap_b32_e32 v229, v230
	v_min_u32_e32 v202, v229, v230
	v_max_u32_e32 v230, v229, v230
	v_mov_b32_e32 v229, v202
; #define EXP_ROW(src, l) (*(const u32x4*)(UV + ((unsigned)__builtin_amdgcn_readlane((src), (l)) * 1024u + lo16)))
; #define EXP_XROW(tt) do { const char* g_ = (const char*)(xin + (size_t)(tt) * 1024) + lane * 16; LAS unsigned char* l_ = xslot + ((tt) & 1) * 2048; \
;         __builtin_amdgcn_global_load_lds((const unsigned*)g_, (LAS unsigned*)l_, 16, 0, 2); __builtin_amdgcn_global_load_lds((const unsigned*)(g_ + 1024), (LAS unsigned*)(l_ + 1024), 16, 0, 2); } while (0)
; __device__ __forceinline__ void expert_tokens(const unsigned char* __restrict__ UV, const float* __restrict__ US, const float* __restrict__ VS, ...
;     ...
;     const unsigned cw0 = (unsigned)IDX[(size_t)t0 * 128 + lane], cw1 = (unsigned)IDX[(size_t)t0 * 128 + 64 + lane];
;     int ci0 = (int)cw0 & rmask, ci1 = (int)cw1 & rmask;
;     float cg0 = __uint_as_float(cw0 & 0xFFFF0000u), cg1 = __uint_as_float(cw1 & 0xFFFF0000u);
;     float csu0 = US[ci0], csu1 = US[ci1], csv0 = VS[ci0], csv1 = VS[ci1];
;     ...
;     EXP_XROW(t0);
;     u32x4 A[EB], B[EB];
; #pragma unroll
;     for (int e = 0; e < EB; ++e) A[e] = EXP_ROW(ci0, e);
; #pragma unroll
;     for (int e = 0; e < EB; ++e) B[e] = EXP_ROW(ci0, EB + e);
	s_nop 1
	v_permlane32_swap_b32_e32 v229, v230
	v_min_u32_e32 v202, v229, v230
	v_max_u32_e32 v230, v229, v230
	v_mov_b32_e32 v229, v202
	s_nop 1
	v_permlane16_swap_b32_e32 v229, v230
	v_min_u32_e32 v202, v229, v230
	v_max_u32_e32 v230, v229, v230
	v_mov_b32_e32 v229, v202
	s_mov_b32 s58, 0xf0f0f0f
	s_mov_b32 s59, 0xf0f0f0f
	v_mov_b32_dpp v202, v229 row_half_mirror row_mask:0xf bank_mask:0xf
	v_mov_b32_dpp v204, v230 row_half_mirror row_mask:0xf bank_mask:0xf
	s_nop 0
	v_max_u32_dpp v203, v202, v229 quad_perm:[3,2,1,0] row_mask:0xf bank_mask:0xf
	v_max_u32_dpp v205, v204, v230 quad_perm:[3,2,1,0] row_mask:0xf bank_mask:0xf
	v_min_u32_dpp v202, v202, v229 quad_perm:[3,2,1,0] row_mask:0xf bank_mask:0xf
	v_min_u32_dpp v204, v204, v230 quad_perm:[3,2,1,0] row_mask:0xf bank_mask:0xf
	v_cndmask_b32_e64 v229, v203, v202, s[58:59]
	v_cndmask_b32_e64 v230, v205, v204, s[58:59]
	s_mov_b32 s58, 0xff00ff
	s_mov_b32 s59, 0xff00ff
	v_min_u32_dpp v202, v229, v229 row_ror:8 row_mask:0xf bank_mask:0xf
	v_max_u32_dpp v203, v229, v229 row_ror:8 row_mask:0xf bank_mask:0xf
	v_min_u32_dpp v204, v230, v230 row_ror:8 row_mask:0xf bank_mask:0xf
	v_max_u32_dpp v205, v230, v230 row_ror:8 row_mask:0xf bank_mask:0xf
	v_cndmask_b32_e64 v229, v203, v202, s[58:59]
	v_cndmask_b32_e64 v230, v205, v204, s[58:59]
	s_mov_b32 s58, 0x33333333
	s_mov_b32 s59, 0x33333333
	v_min_u32_dpp v202, v229, v229 quad_perm:[2,3,0,1] row_mask:0xf bank_mask:0xf
	v_max_u32_dpp v203, v229, v229 quad_perm:[2,3,0,1] row_mask:0xf bank_mask:0xf
	v_min_u32_dpp v204, v230, v230 quad_perm:[2,3,0,1] row_mask:0xf bank_mask:0xf
	v_max_u32_dpp v205, v230, v230 quad_perm:[2,3,0,1] row_mask:0xf bank_mask:0xf
	v_cndmask_b32_e64 v229, v203, v202, s[58:59]
	v_cndmask_b32_e64 v230, v205, v204, s[58:59]
	s_mov_b32 s58, 0x55555555
	s_mov_b32 s59, 0x55555555
	v_min_u32_dpp v202, v229, v229 quad_perm:[1,0,3,2] row_mask:0xf bank_mask:0xf
	v_max_u32_dpp v203, v229, v229 quad_perm:[1,0,3,2] row_mask:0xf bank_mask:0xf
	v_min_u32_dpp v204, v230, v230 quad_perm:[1,0,3,2] row_mask:0xf bank_mask:0xf
	v_max_u32_dpp v205, v230, v230 quad_perm:[1,0,3,2] row_mask:0xf bank_mask:0xf
	v_cndmask_b32_e64 v229, v203, v202, s[58:59]
	v_cndmask_b32_e64 v230, v205, v204, s[58:59]
	s_nop 1
	v_permlane16_swap_b32_e32 v229, v230
	s_nop 1
	v_permlane32_swap_b32_e32 v229, v230
	v_alignbit_b32 v229, v229, v229, 16
	v_alignbit_b32 v230, v230, v230, 16
	v_and_b32_e32 v231, 0x3fff, v229
	v_and_b32_e32 v232, 0x3fff, v230
	v_readlane_b32 s40, v231, 22
	v_readlane_b32 s41, v231, 23
	v_readlane_b32 s49, v231, 31
	v_lshlrev_b32_e32 v2, 3, v231
	v_lshlrev_b32_e32 v3, 3, v232
	v_readlane_b32 s33, v231, 15
	v_readlane_b32 s34, v231, 16
	v_readlane_b32 s35, v231, 17
	v_readlane_b32 s36, v231, 18
	v_readlane_b32 s37, v231, 19
	v_readlane_b32 s38, v231, 20
	v_readlane_b32 s39, v231, 21
	v_readlane_b32 s42, v231, 24
	v_readlane_b32 s43, v231, 25
	v_readlane_b32 s44, v231, 26
	v_readlane_b32 s45, v231, 27
	v_readlane_b32 s46, v231, 28
	v_readlane_b32 s47, v231, 29
	v_readlane_b32 s48, v231, 30
	v_lshl_or_b32 v42, s49, 10, v194
	v_lshl_or_b32 v50, s41, 10, v194
	v_lshl_or_b32 v51, s40, 10, v194
	v_readlane_b32 s30, v231, 13
	v_readlane_b32 s31, v231, 14
	global_load_dword v233, v2, s[12:13]
	global_load_dword v234, v3, s[12:13]
	global_load_dword v236, v3, s[12:13] offset:4
	global_load_dword v235, v2, s[12:13] offset:4
	v_lshl_or_b32 v43, s48, 10, v194
	v_lshl_or_b32 v44, s47, 10, v194
	v_lshl_or_b32 v45, s46, 10, v194
	v_lshl_or_b32 v46, s45, 10, v194
	v_lshl_or_b32 v47, s44, 10, v194
	v_lshl_or_b32 v48, s43, 10, v194
	v_lshl_or_b32 v49, s42, 10, v194
	global_load_dwordx4 v[2:5], v42, s[10:11]
	global_load_dwordx4 v[10:13], v43, s[10:11]
	global_load_dwordx4 v[6:9], v44, s[10:11]
	global_load_dwordx4 v[18:21], v45, s[10:11]
	global_load_dwordx4 v[14:17], v46, s[10:11]
	global_load_dwordx4 v[26:29], v47, s[10:11]
	global_load_dwordx4 v[22:25], v48, s[10:11]
	global_load_dwordx4 v[34:37], v49, s[10:11]
	global_load_dwordx4 v[30:33], v50, s[10:11]
	global_load_dwordx4 v[38:41], v51, s[10:11]
	v_lshl_or_b32 v50, s39, 10, v194
	v_lshl_or_b32 v51, s38, 10, v194
	v_lshl_or_b32 v58, s37, 10, v194
	v_lshl_or_b32 v59, s36, 10, v194
	v_lshl_or_b32 v66, s35, 10, v194
	v_lshl_or_b32 v67, s34, 10, v194
	v_lshl_or_b32 v75, s33, 10, v194
	v_readlane_b32 s28, v231, 11
	v_readlane_b32 s29, v231, 12
	global_load_dwordx4 v[42:45], v50, s[10:11]
	global_load_dwordx4 v[46:49], v51, s[10:11]
	s_nop 0
	global_load_dwordx4 v[50:53], v58, s[10:11]
	global_load_dwordx4 v[54:57], v59, s[10:11]
	s_nop 0
	global_load_dwordx4 v[58:61], v66, s[10:11]
	global_load_dwordx4 v[62:65], v67, s[10:11]
	v_lshl_or_b32 v76, s31, 10, v194
	global_load_dwordx4 v[66:69], v75, s[10:11]
	global_load_dwordx4 v[70:73], v76, s[10:11]
	v_lshl_or_b32 v75, s30, 10, v194
	v_readlane_b32 s25, v231, 9
	v_readlane_b32 s27, v231, 10
	v_lshl_or_b32 v76, s29, 10, v194
	global_load_dwordx4 v[112:115], v75, s[10:11]
	global_load_dwordx4 v[116:119], v76, s[10:11]
	v_lshl_or_b32 v75, s28, 10, v194
	v_readlane_b32 s23, v231, 7
	v_readlane_b32 s24, v231, 8
	v_lshl_or_b32 v76, s27, 10, v194
	global_load_dwordx4 v[144:147], v75, s[10:11]
	global_load_dwordx4 v[148:151], v76, s[10:11]
	v_lshl_or_b32 v75, s25, 10, v194
	v_readlane_b32 s21, v231, 5
	v_readlane_b32 s22, v231, 6
	v_lshl_or_b32 v76, s24, 10, v194
	global_load_dwordx4 v[152:155], v75, s[10:11]
	global_load_dwordx4 v[156:159], v76, s[10:11]
	v_lshl_or_b32 v75, s23, 10, v194
	v_readlane_b32 s19, v231, 3
	v_readlane_b32 s20, v231, 4
	v_lshl_or_b32 v76, s22, 10, v194
	global_load_dwordx4 v[160:163], v75, s[10:11]
	global_load_dwordx4 v[164:167], v76, s[10:11]
	v_lshl_or_b32 v75, s21, 10, v194
	v_readlane_b32 s16, v231, 1
	v_readlane_b32 s18, v231, 2
	v_lshl_or_b32 v76, s20, 10, v194
	global_load_dwordx4 v[168:171], v75, s[10:11]
	global_load_dwordx4 v[172:175], v76, s[10:11]
	v_lshl_or_b32 v75, s19, 10, v194
	v_readlane_b32 s9, v231, 0
	v_lshl_or_b32 v76, s18, 10, v194
	global_load_dwordx4 v[176:179], v75, s[10:11]
	global_load_dwordx4 v[180:183], v76, s[10:11]
	v_lshl_or_b32 v75, s16, 10, v194
	v_lshl_or_b32 v76, s9, 10, v194
	global_load_dwordx4 v[184:187], v75, s[10:11]
	global_load_dwordx4 v[188:191], v76, s[10:11]
	v_and_b32_e32 v75, 1, v0
	v_lshrrev_b32_e32 v76, 2, v0
	v_and_b32_e32 v0, 3, v0
	v_and_or_b32 v193, v76, 12, v0
	v_cmp_eq_u32_e64 s[2:3], 0, v75
	v_mbcnt_lo_u32_b32 v0, -1, 0
	s_mov_b32 s9, 0x800000
	s_mov_b32 s16, 0x45800000
	s_mov_b32 s27, 0x42ee0000
	s_mov_b32 s28, 0x3e6d3388
	s_mov_b32 s29, 0xc040c00
	s_mov_b32 s30, 0xc050c01
	s_mov_b32 s31, 0xc060c02
	s_mov_b32 s33, 0xc070c03
	v_mbcnt_hi_u32_b32 v228, -1, v0
	s_mov_b32 s20, s8
	s_branch .LBB0_1014
; #define LAS __attribute__((address_space(3)))
; __device__ __forceinline__ void expert_tokens(const unsigned char* __restrict__ UV, const float* __restrict__ US, const float* __restrict__ VS, ...
;     ...
;         float sy = 0.f;
;         const float sumc = wave_sum(sumc_l) * (0.25f / 4096.f);
; #pragma unroll
;         for (int i = 0; i < 16; ++i) { acc[i] = acc[i] * 4096.f - 7.5f * sumc; sy += acc[i] * acc[i]; }
;         const float ry = rsqrtf(wave_sum(sy) * (1.f / 1024.f) + EPS);
;         const float pscale = (t < 2048) ? 1.f + pd : 1.f;
; #pragma unroll
;         for (int j = 0; j < 4; ++j) { const f32x4 y = (f32x4){acc[4 * j], acc[4 * j + 1], acc[4 * j + 2], acc[4 * j + 3]};
;             float* op = out + (size_t)t * 1024 + 256 * j + 4 * lane;
;             const u32x2 xw = *(const LAS u32x2*)(xrow + 512 * j + 8 * lane);
;             { const f32x4 ov_ = pscale * (f32x4){__uint_as_float(xw.x << 16), __uint_as_float(xw.x & 0xffff0000u), __uint_as_float(xw.y << 16), __uint_as_float(xw.y & 0xffff0000u)} + pscale * *(const LAS f32x4*)(pvt + 2048 + 256 * j + 4 * lane) * (y * ry); __builtin_nontemporal_store(ov_, (f32x4*)op); } }
.LBB0_1013:
	v_add_f32_dpp v66, v252, v252 quad_perm:[1,0,3,2] row_mask:0xf bank_mask:0xf bound_ctrl:1
	s_ashr_i32 s21, s20, 31
	s_lshl_b64 s[4:5], s[20:21], 12
	v_add_f32_dpp v66, v66, v66 quad_perm:[2,3,0,1] row_mask:0xf bank_mask:0xf bound_ctrl:1
	v_lshl_add_u64 v[162:163], v[200:201], 0, s[4:5]
	s_waitcnt vmcnt(31)
	v_mov_b64_e32 v[190:191], v[80:81]
	v_add_f32_dpp v66, v66, v66 row_ror:4 row_mask:0xf bank_mask:0xf bound_ctrl:1
	s_waitcnt vmcnt(30)
	v_mov_b64_e32 v[186:187], v[76:77]
	s_waitcnt vmcnt(29)
	v_mov_b64_e32 v[182:183], v[88:89]
	v_add_f32_dpp v66, v66, v66 row_ror:8 row_mask:0xf bank_mask:0xf bound_ctrl:1
	v_mov_b32_e32 v67, v66
	s_nop 1
	v_permlane16_swap_b32_e32 v66, v67
	v_add_f32_e32 v66, v66, v67
	v_mov_b32_e32 v67, v66
	s_nop 1
	v_permlane32_swap_b32_e32 v66, v67
	v_add_f32_e32 v66, v66, v67
	v_mul_f32_e32 v66, 0x38800000, v66
	v_mul_f32_e32 v66, 0x40f00000, v66
	v_pk_fma_f32 v[118:119], v[224:225], s[16:17], v[66:67] op_sel_hi:[1,0,0] neg_lo:[0,0,1] neg_hi:[0,0,1]
	v_pk_fma_f32 v[144:145], v[222:223], s[16:17], v[66:67] op_sel_hi:[1,0,0] neg_lo:[0,0,1] neg_hi:[0,0,1]
	v_pk_mul_f32 v[68:69], v[118:119], v[118:119]
	v_pk_mul_f32 v[70:71], v[144:145], v[144:145]
	v_add_f32_e32 v68, v68, v69
	v_pk_fma_f32 v[148:149], v[220:221], s[16:17], v[66:67] op_sel_hi:[1,0,0] neg_lo:[0,0,1] neg_hi:[0,0,1]
	v_add_f32_e32 v68, v70, v68
	v_pk_mul_f32 v[72:73], v[148:149], v[148:149]
	v_add_f32_e32 v68, v71, v68
	v_pk_fma_f32 v[150:151], v[218:219], s[16:17], v[66:67] op_sel_hi:[1,0,0] neg_lo:[0,0,1] neg_hi:[0,0,1]
	v_add_f32_e32 v68, v72, v68
	v_pk_mul_f32 v[114:115], v[150:151], v[150:151]
	v_add_f32_e32 v68, v73, v68
	v_pk_fma_f32 v[152:153], v[216:217], s[16:17], v[66:67] op_sel_hi:[1,0,0] neg_lo:[0,0,1] neg_hi:[0,0,1]
	v_add_f32_e32 v68, v114, v68
	v_pk_mul_f32 v[116:117], v[152:153], v[152:153]
	v_add_f32_e32 v68, v115, v68
	v_pk_fma_f32 v[154:155], v[214:215], s[16:17], v[66:67] op_sel_hi:[1,0,0] neg_lo:[0,0,1] neg_hi:[0,0,1]
	v_add_f32_e32 v68, v116, v68
	v_pk_mul_f32 v[146:147], v[154:155], v[154:155]
	v_add_f32_e32 v68, v117, v68
	v_pk_fma_f32 v[156:157], v[212:213], s[16:17], v[66:67] op_sel_hi:[1,0,0] neg_lo:[0,0,1] neg_hi:[0,0,1]
	v_add_f32_e32 v68, v146, v68
	v_pk_mul_f32 v[158:159], v[156:157], v[156:157]
	v_add_f32_e32 v68, v147, v68
	v_pk_fma_f32 v[160:161], v[210:211], s[16:17], v[66:67] op_sel_hi:[1,0,0] neg_lo:[0,0,1] neg_hi:[0,0,1]
	v_add_f32_e32 v68, v158, v68
	v_pk_mul_f32 v[66:67], v[160:161], v[160:161]
	v_add_f32_e32 v68, v159, v68
	v_add_f32_e32 v66, v66, v68
	v_add_f32_e32 v66, v67, v66
	ds_read_b128 v[114:117], v240 offset:8192
	ds_read2st64_b64 v[70:73], v239 offset0:34 offset1:35
	v_add_f32_dpp v66, v66, v66 quad_perm:[1,0,3,2] row_mask:0xf bank_mask:0xf bound_ctrl:1
	s_waitcnt vmcnt(28)
	v_mov_b64_e32 v[178:179], v[84:85]
	s_waitcnt vmcnt(27)
	v_mov_b64_e32 v[174:175], v[96:97]
	v_add_f32_dpp v66, v66, v66 quad_perm:[2,3,0,1] row_mask:0xf bank_mask:0xf bound_ctrl:1
	s_waitcnt vmcnt(26)
; #define LAS __attribute__((address_space(3)))
; __device__ __forceinline__ void expert_tokens(const unsigned char* __restrict__ UV, const float* __restrict__ US, const float* __restrict__ VS, ...
;     ...
;         const float ry = rsqrtf(wave_sum(sy) * (1.f / 1024.f) + EPS);
;         const float pscale = (t < 2048) ? 1.f + pd : 1.f;
; #pragma unroll
;         for (int j = 0; j < 4; ++j) { const f32x4 y = (f32x4){acc[4 * j], acc[4 * j + 1], acc[4 * j + 2], acc[4 * j + 3]};
;             float* op = out + (size_t)t * 1024 + 256 * j + 4 * lane;
;             const u32x2 xw = *(const LAS u32x2*)(xrow + 512 * j + 8 * lane);
;             { const f32x4 ov_ = pscale * (f32x4){__uint_as_float(xw.x << 16), __uint_as_float(xw.x & 0xffff0000u), __uint_as_float(xw.y << 16), __uint_as_float(xw.y & 0xffff0000u)} + pscale * *(const LAS f32x4*)(pvt + 2048 + 256 * j + 4 * lane) * (y * ry); __builtin_nontemporal_store(ov_, (f32x4*)op); } }
;         ci0 = ni0; ci1 = ni1; cg0 = ng0; cg1 = ng1; csu0 = nsu0; csu1 = nsu1; csv0 = nsv0; csv1 = nsv1;
	v_mov_b64_e32 v[170:171], v[92:93]
	v_mov_b64_e32 v[188:189], v[78:79]
	v_add_f32_dpp v66, v66, v66 row_ror:4 row_mask:0xf bank_mask:0xf bound_ctrl:1
	v_mov_b64_e32 v[184:185], v[74:75]
	v_mov_b64_e32 v[180:181], v[86:87]
	v_add_f32_dpp v66, v66, v66 row_ror:8 row_mask:0xf bank_mask:0xf bound_ctrl:1
	v_mov_b32_e32 v67, v66
	s_nop 1
	v_permlane16_swap_b32_e32 v66, v67
	v_add_f32_e32 v66, v66, v67
	v_mov_b32_e32 v67, v66
	s_nop 1
	v_permlane32_swap_b32_e32 v66, v67
	v_add_f32_e32 v66, v66, v67
	v_fmamk_f32 v66, v66, 0x3a800000, v226
	v_mul_f32_e32 v67, 0x4b800000, v66
	v_cmp_gt_f32_e32 vcc, s9, v66
	v_mov_b64_e32 v[176:177], v[82:83]
	v_mov_b64_e32 v[172:173], v[94:95]
	v_cndmask_b32_e32 v66, v66, v67, vcc
	v_rsq_f32_e32 v66, v66
	v_mov_b64_e32 v[168:169], v[90:91]
	v_mov_b32_e32 v231, v242
	v_mov_b32_e32 v232, v243
	v_mul_f32_e32 v67, 0x45800000, v66
	v_cndmask_b32_e32 v158, v66, v67, vcc
	ds_read2st64_b64 v[66:69], v239 offset0:32 offset1:33
	v_pk_mul_f32 v[166:167], v[144:145], v[158:159] op_sel_hi:[1,0]
	ds_read_b128 v[144:147], v240 offset:9216
	v_pk_mul_f32 v[118:119], v[118:119], v[158:159] op_sel_hi:[1,0]
	s_and_b64 vcc, exec, s[18:19]
	s_waitcnt lgkmcnt(1)
	v_lshlrev_b32_e32 v164, 16, v66
	v_and_b32_e32 v165, 0xffff0000, v66
	v_lshlrev_b32_e32 v66, 16, v67
	v_and_b32_e32 v67, 0xffff0000, v67
	v_pk_fma_f32 v[116:117], v[116:117], v[166:167], v[66:67]
	v_pk_fma_f32 v[114:115], v[114:115], v[118:119], v[164:165]
	global_store_dwordx4 v[162:163], v[114:117], off nt
	v_lshlrev_b32_e32 v66, 16, v68
	v_and_b32_e32 v67, 0xffff0000, v68
	v_lshlrev_b32_e32 v68, 16, v69
	v_and_b32_e32 v69, 0xffff0000, v69
	v_pk_mul_f32 v[114:115], v[148:149], v[158:159] op_sel_hi:[1,0]
	v_pk_mul_f32 v[116:117], v[150:151], v[158:159] op_sel_hi:[1,0]
	s_waitcnt lgkmcnt(0)
	v_pk_fma_f32 v[66:67], v[144:145], v[114:115], v[66:67]
	v_pk_fma_f32 v[68:69], v[146:147], v[116:117], v[68:69]
	global_store_dwordx4 v[162:163], v[66:69], off offset:1024 nt
	ds_read_b128 v[66:69], v240 offset:10240
	ds_read_b128 v[114:117], v240 offset:11264
	v_lshlrev_b32_e32 v118, 16, v70
	v_and_b32_e32 v119, 0xffff0000, v70
	v_lshlrev_b32_e32 v70, 16, v71
	v_and_b32_e32 v71, 0xffff0000, v71
	v_pk_mul_f32 v[144:145], v[152:153], v[158:159] op_sel_hi:[1,0]
	v_pk_mul_f32 v[146:147], v[154:155], v[158:159] op_sel_hi:[1,0]
	s_waitcnt lgkmcnt(1)
	v_pk_fma_f32 v[66:67], v[66:67], v[144:145], v[118:119]
	v_pk_fma_f32 v[68:69], v[68:69], v[146:147], v[70:71]
	global_store_dwordx4 v[162:163], v[66:69], off offset:2048 nt
	v_pk_mul_f32 v[70:71], v[156:157], v[158:159] op_sel_hi:[1,0]
	s_waitcnt vmcnt(28)
	v_mov_b64_e32 v[166:167], v[104:105]
	v_lshlrev_b32_e32 v66, 16, v72
	v_and_b32_e32 v67, 0xffff0000, v72
	v_lshlrev_b32_e32 v68, 16, v73
	v_and_b32_e32 v69, 0xffff0000, v73
	v_pk_mul_f32 v[72:73], v[160:161], v[158:159] op_sel_hi:[1,0]
	s_waitcnt lgkmcnt(0)
	v_pk_fma_f32 v[66:67], v[114:115], v[70:71], v[66:67]
	v_pk_fma_f32 v[68:69], v[116:117], v[72:73], v[68:69]
	s_waitcnt vmcnt(26)
	v_mov_b64_e32 v[158:159], v[112:113]
	global_store_dwordx4 v[162:163], v[66:69], off offset:3072 nt
	v_mov_b64_e32 v[162:163], v[100:101]
	v_mov_b64_e32 v[156:157], v[110:111]
	s_waitcnt vmcnt(26)
	v_mov_b64_e32 v[154:155], v[108:109]
	s_waitcnt vmcnt(25)
	v_mov_b64_e32 v[150:151], v[126:127]
	s_waitcnt vmcnt(24)
	v_mov_b64_e32 v[146:147], v[122:123]
	s_waitcnt vmcnt(23)
	v_mov_b64_e32 v[116:117], v[132:133]
	s_waitcnt vmcnt(22)
	v_mov_b64_e32 v[112:113], v[128:129]
	s_waitcnt vmcnt(21)
	v_mov_b64_e32 v[70:71], v[140:141]
	s_waitcnt vmcnt(20)
	v_mov_b64_e32 v[66:67], v[136:137]
	v_mov_b64_e32 v[164:165], v[102:103]
	v_mov_b64_e32 v[160:161], v[98:99]
	v_mov_b64_e32 v[152:153], v[106:107]
	v_mov_b64_e32 v[148:149], v[124:125]
	v_mov_b64_e32 v[144:145], v[120:121]
	v_mov_b64_e32 v[118:119], v[134:135]
	v_mov_b64_e32 v[114:115], v[130:131]
	v_mov_b64_e32 v[72:73], v[142:143]
	v_mov_b64_e32 v[68:69], v[138:139]
	v_mov_b32_e32 v229, v237
	v_mov_b32_e32 v230, v238
	v_mov_b32_e32 v233, v202
	v_mov_b32_e32 v234, v204
	v_mov_b32_e32 v235, v203
	v_mov_b32_e32 v236, v205
	s_mov_b32 s20, s34
	s_cbranch_vccnz .LBB0_1025

.Lp10_nobar_i:
	v_mov_b32_e32 v88, 0
	v_dot8c_i32_i4_e32 v88, v248, v70
	v_dot8c_i32_i4_e32 v88, v250, v71
	v_mov_b32_e32 v74, 0
	v_mov_b32_e32 v75, 0
	v_mov_b32_e32 v76, 0
	v_lshlrev_b32_e32 v88, 4, v88
	v_mov_b32_e32 v77, 0
	v_mov_b32_e32 v78, 0
	v_mov_b32_e32 v79, 0
	v_mov_b32_e32 v80, 0
	v_mov_b32_e32 v81, 0
	v_mov_b32_e32 v82, 0
	v_mov_b32_e32 v83, 0
	v_mov_b32_e32 v84, 0
	v_mov_b32_e32 v85, 0
	v_mov_b32_e32 v86, 0
	v_mov_b32_e32 v87, 0
	v_dot8c_i32_i4_e32 v88, v247, v70
	v_mov_b32_e32 v70, 0
	v_dot8c_i32_i4_e32 v74, v248, v188
	v_dot8c_i32_i4_e32 v75, v248, v184
	v_dot8c_i32_i4_e32 v76, v248, v180
	v_dot8c_i32_i4_e32 v77, v248, v176
	v_dot8c_i32_i4_e32 v78, v248, v172
	v_dot8c_i32_i4_e32 v79, v248, v168
	v_dot8c_i32_i4_e32 v80, v248, v164
	v_dot8c_i32_i4_e32 v81, v248, v160
	v_dot8c_i32_i4_e32 v82, v248, v156
	v_dot8c_i32_i4_e32 v83, v248, v152
	v_dot8c_i32_i4_e32 v84, v248, v148
	v_dot8c_i32_i4_e32 v85, v248, v144
	v_dot8c_i32_i4_e32 v86, v248, v116
	v_dot8c_i32_i4_e32 v87, v248, v112
	v_dot8c_i32_i4_e32 v70, v248, v66
	v_dot8c_i32_i4_e32 v74, v250, v189
	v_dot8c_i32_i4_e32 v75, v250, v185
	v_dot8c_i32_i4_e32 v76, v250, v181
	v_dot8c_i32_i4_e32 v77, v250, v177
	v_dot8c_i32_i4_e32 v78, v250, v173
	v_dot8c_i32_i4_e32 v79, v250, v169
	v_dot8c_i32_i4_e32 v80, v250, v165
	v_dot8c_i32_i4_e32 v81, v250, v161
	v_dot8c_i32_i4_e32 v82, v250, v157
	v_dot8c_i32_i4_e32 v83, v250, v153
	v_dot8c_i32_i4_e32 v84, v250, v149
	v_dot8c_i32_i4_e32 v85, v250, v145
	v_dot8c_i32_i4_e32 v86, v250, v117
	v_dot8c_i32_i4_e32 v87, v250, v113
	v_dot8c_i32_i4_e32 v70, v250, v67
	v_lshlrev_b32_e32 v74, 4, v74
	v_lshlrev_b32_e32 v75, 4, v75
	v_lshlrev_b32_e32 v76, 4, v76
	v_lshlrev_b32_e32 v77, 4, v77
	v_lshlrev_b32_e32 v78, 4, v78
	v_lshlrev_b32_e32 v79, 4, v79
	v_lshlrev_b32_e32 v80, 4, v80
	v_lshlrev_b32_e32 v81, 4, v81
	v_lshlrev_b32_e32 v82, 4, v82
	v_lshlrev_b32_e32 v83, 4, v83
	v_lshlrev_b32_e32 v84, 4, v84
	v_lshlrev_b32_e32 v85, 4, v85
	v_lshlrev_b32_e32 v86, 4, v86
	v_lshlrev_b32_e32 v87, 4, v87
	v_lshlrev_b32_e32 v70, 4, v70
	v_dot8c_i32_i4_e32 v74, v247, v188
	v_dot8c_i32_i4_e32 v75, v247, v184
	v_dot8c_i32_i4_e32 v76, v247, v180
	v_dot8c_i32_i4_e32 v77, v247, v176
	v_dot8c_i32_i4_e32 v78, v247, v172
	v_dot8c_i32_i4_e32 v79, v247, v168
	v_dot8c_i32_i4_e32 v80, v247, v164
	v_dot8c_i32_i4_e32 v81, v247, v160
	v_dot8c_i32_i4_e32 v82, v247, v156
	v_dot8c_i32_i4_e32 v83, v247, v152
	v_dot8c_i32_i4_e32 v84, v247, v148
	v_dot8c_i32_i4_e32 v85, v247, v144
	v_dot8c_i32_i4_e32 v86, v247, v116
	v_dot8c_i32_i4_e32 v87, v247, v112
	v_dot8c_i32_i4_e32 v70, v247, v66
	v_dot8c_i32_i4_e32 v74, v249, v189
	v_dot8c_i32_i4_e32 v75, v249, v185
	v_dot8c_i32_i4_e32 v76, v249, v181
	v_dot8c_i32_i4_e32 v77, v249, v177
	v_dot8c_i32_i4_e32 v78, v249, v173
	v_dot8c_i32_i4_e32 v79, v249, v169
	v_dot8c_i32_i4_e32 v80, v249, v165
	v_dot8c_i32_i4_e32 v81, v249, v161
	v_dot8c_i32_i4_e32 v82, v249, v157
	v_dot8c_i32_i4_e32 v83, v249, v153
	v_dot8c_i32_i4_e32 v84, v249, v149
	v_dot8c_i32_i4_e32 v85, v249, v145
	v_dot8c_i32_i4_e32 v86, v249, v117
	v_dot8c_i32_i4_e32 v87, v249, v113
	v_dot8c_i32_i4_e32 v88, v249, v71
	v_dot8c_i32_i4_e32 v70, v249, v67
	v_permlane32_swap_b32_e32 v74, v82
	v_permlane32_swap_b32_e32 v75, v83
	v_permlane32_swap_b32_e32 v76, v84
	v_permlane32_swap_b32_e32 v77, v85
	v_permlane32_swap_b32_e32 v78, v86
	v_permlane32_swap_b32_e32 v79, v87
	v_permlane32_swap_b32_e32 v80, v88
	v_permlane32_swap_b32_e32 v81, v70
	v_add_u32_e32 v66, v74, v82
	v_add_u32_e32 v67, v75, v83
	v_add_u32_e32 v71, v76, v84
	v_add_u32_e32 v74, v77, v85
	v_add_u32_e32 v75, v78, v86
	v_add_u32_e32 v76, v79, v87
	v_add_u32_e32 v77, v80, v88
	v_add_u32_e32 v70, v81, v70
	v_permlane16_swap_b32_e32 v66, v75
	v_permlane16_swap_b32_e32 v67, v76
	v_permlane16_swap_b32_e32 v71, v77
	v_permlane16_swap_b32_e32 v74, v70
	v_add_u32_e32 v66, v66, v75
	v_add_u32_e32 v67, v67, v76
	v_add_u32_e32 v71, v71, v77
	v_add_u32_e32 v70, v74, v70
	v_cndmask_b32_e64 v74, v71, v66, s[0:1]
	v_cndmask_b32_e64 v66, v66, v71, s[0:1]
	v_cndmask_b32_e64 v71, v70, v67, s[0:1]
	v_cndmask_b32_e64 v67, v67, v70, s[0:1]
	v_add_u32_dpp v66, v66, v74 quad_perm:[2,3,0,1] row_mask:0xf bank_mask:0xf bound_ctrl:1
	s_sub_i32 s4, s21, 32
	v_add_u32_dpp v67, v67, v71 quad_perm:[2,3,0,1] row_mask:0xf bank_mask:0xf bound_ctrl:1
	v_cndmask_b32_e64 v70, v67, v66, s[2:3]
	v_cndmask_b32_e64 v66, v66, v67, s[2:3]
	s_cmp_lt_u32 s25, 4
	s_cselect_b64 vcc, -1, 0
	v_add_u32_dpp v66, v66, v70 quad_perm:[1,0,3,2] row_mask:0xf bank_mask:0xf bound_ctrl:1
	v_cndmask_b32_e32 v70, v234, v233, vcc
	v_cndmask_b32_e32 v71, v230, v229, vcc
	v_add_u32_dpp v66, v66, v66 row_ror:8 row_mask:0xf bank_mask:0xf bound_ctrl:1
	s_cmp_eq_u32 s21, 32
	s_nop 0
	v_add_u32_dpp v67, v66, v66 row_ror:4 row_mask:0xf bank_mask:0xf bound_ctrl:1
	v_and_or_b32 v66, s4, 32, v193
	v_lshlrev_b32_e32 v66, 2, v66
	v_cvt_f32_i32_e32 v74, v67
	ds_bpermute_b32 v75, v66, v70
	v_and_b32_e32 v67, 0xffff0000, v71
	ds_bpermute_b32 v76, v66, v67
	v_add_f32_e32 v71, v251, v74
	v_mul_f32_e32 v71, v244, v71
	s_waitcnt lgkmcnt(1)
	v_mul_f32_e32 v74, v71, v75
	v_fma_f32 v71, |v74|, s28, 1.0
	v_rcp_f32_e32 v75, v71
	v_mul_f32_e32 v79, v74, v74
	v_mul_f32_e32 v79, 0xbf38aa3b, v79
	v_exp_f32_e32 v79, v79
	v_fmamk_f32 v78, v75, 0x3f07dc22, v227
	v_fmaak_f32 v78, v75, v78, 0x3f35f0e3
	v_fmaak_f32 v78, v75, v78, 0xbe11a98e
	v_cndmask_b32_e32 v71, v236, v235, vcc
	v_fmaak_f32 v78, v75, v78, 0x3e027906
	ds_bpermute_b32 v77, v66, v71
	v_mul_f32_e32 v75, v75, v78
	v_mul_f32_e32 v75, v79, v75
	v_mul_f32_e32 v78, v74, v75
	v_fma_f32 v75, -v74, v75, v74
	v_cmp_gt_f32_e32 vcc, 0, v74
	s_nop 1
	v_cndmask_b32_e32 v74, v75, v78, vcc
	s_waitcnt lgkmcnt(1)
; __device__ __forceinline__ void expert_tokens(const unsigned char* __restrict__ UV, const float* __restrict__ US, const float* __restrict__ VS, ...
;     ...
;         const unsigned nw0 = (unsigned)IDX[(size_t)tn * 128 + lane], nw1 = (unsigned)IDX[(size_t)tn * 128 + 64 + lane];
;         const int ni0 = (int)nw0 & rmask, ni1 = (int)nw1 & rmask;
	v_mul_f32_e32 v74, v74, v76
	s_cselect_b64 vcc, -1, 0
	s_cmp_gt_u32 s25, 5
	s_waitcnt lgkmcnt(0)
	v_mul_f32_e32 v74, v74, v77
	s_cselect_b64 s[22:23], -1, 0
	s_cmp_lt_u32 s25, 6
	v_fma_mixlo_f16 v116, v74, s16, 0
	s_cselect_b64 s[4:5], -1, 0
	v_and_b32_e32 v117, 0xffff, v116
	v_cndmask_b32_e64 v74, v242, v232, s[4:5]
	s_add_i32 s24, s21, 1
	s_add_i32 s35, s21, 2
	s_add_i32 s36, s21, 3
	s_add_i32 s37, s21, 4
	s_add_i32 s38, s21, 5
	s_add_i32 s39, s21, 6
	s_add_i32 s40, s21, 7
	s_add_i32 s49, s21, 8
	s_add_i32 s50, s21, 9
	s_add_i32 s51, s21, 10
	s_add_i32 s52, s21, 11
	s_add_i32 s53, s21, 12
	s_add_i32 s54, s21, 13
	s_add_i32 s55, s21, 14
	s_add_i32 s56, s21, 15
	v_cndmask_b32_e32 v136, v74, v231, vcc
	v_readlane_b32 s47, v117, 0
	v_readlane_b32 s48, v117, 1
	s_cmp_lg_u32 s21, 32
	v_readlane_b32 s4, v136, s21
	s_nop 1
	v_lshl_or_b32 v74, s4, 10, v194
	v_readlane_b32 s4, v136, s24
	s_nop 1
	v_lshl_or_b32 v75, s4, 10, v194
	global_load_dwordx4 v[78:81], v74, s[10:11]
	s_nop 0
	global_load_dwordx4 v[74:77], v75, s[10:11]
	v_readlane_b32 s45, v117, 2
	v_readlane_b32 s46, v117, 3
	v_readlane_b32 s4, v136, s35
	s_nop 1
	v_lshl_or_b32 v82, s4, 10, v194
	v_readlane_b32 s4, v136, s36
	s_nop 1
	v_lshl_or_b32 v83, s4, 10, v194
	global_load_dwordx4 v[86:89], v82, s[10:11]
	s_nop 0
	global_load_dwordx4 v[82:85], v83, s[10:11]
	v_readlane_b32 s43, v117, 16
	v_readlane_b32 s44, v117, 17
	v_readlane_b32 s4, v136, s37
	s_nop 1
	v_lshl_or_b32 v90, s4, 10, v194
	v_readlane_b32 s4, v136, s38
	s_nop 1
	v_lshl_or_b32 v91, s4, 10, v194
	global_load_dwordx4 v[94:97], v90, s[10:11]
	s_nop 0
	global_load_dwordx4 v[90:93], v91, s[10:11]
	v_readlane_b32 s41, v117, 18
	v_readlane_b32 s42, v117, 19
	v_readlane_b32 s4, v136, s39
	s_nop 1
	v_lshl_or_b32 v98, s4, 10, v194
	v_readlane_b32 s4, v136, s40
	s_nop 1
	v_lshl_or_b32 v99, s4, 10, v194
	global_load_dwordx4 v[102:105], v98, s[10:11]
	s_nop 0
	global_load_dwordx4 v[98:101], v99, s[10:11]
	v_readlane_b32 s39, v117, 32
	v_readlane_b32 s40, v117, 33
	v_readlane_b32 s4, v136, s49
	s_nop 1
	v_lshl_or_b32 v106, s4, 10, v194
	v_readlane_b32 s4, v136, s50
	s_nop 1
	v_lshl_or_b32 v107, s4, 10, v194
	global_load_dwordx4 v[110:113], v106, s[10:11]
	s_nop 0
	global_load_dwordx4 v[106:109], v107, s[10:11]
	v_readlane_b32 s37, v117, 34
	v_readlane_b32 s38, v117, 35
	v_readlane_b32 s4, v136, s51
	s_nop 1
	v_lshl_or_b32 v120, s4, 10, v194
	v_readlane_b32 s4, v136, s52
	s_nop 1
	v_lshl_or_b32 v121, s4, 10, v194
	global_load_dwordx4 v[124:127], v120, s[10:11]
	s_nop 0
	global_load_dwordx4 v[120:123], v121, s[10:11]
	v_readlane_b32 s35, v117, 48
	v_readlane_b32 s36, v117, 49
	v_readlane_b32 s4, v136, s53
	s_nop 1
	v_lshl_or_b32 v128, s4, 10, v194
	v_readlane_b32 s4, v136, s54
	s_nop 1
	v_lshl_or_b32 v129, s4, 10, v194
	global_load_dwordx4 v[132:135], v128, s[10:11]
	s_nop 0
	global_load_dwordx4 v[128:131], v129, s[10:11]
	v_readlane_b32 s4, v117, 50
	v_readlane_b32 s5, v117, 51
	v_readlane_b32 s24, v136, s55
	s_nop 1
	v_lshl_or_b32 v117, s24, 10, v194
	v_readlane_b32 s24, v136, s56
	s_nop 1
	v_lshl_or_b32 v136, s24, 10, v194
	global_load_dwordx4 v[140:143], v117, s[10:11]
	s_nop 0
	global_load_dwordx4 v[136:139], v136, s[10:11]
	s_cbranch_scc1 .LBB0_1021
	s_waitcnt vmcnt(16)
	s_bfe_i32 s60, s34, 0x10000
	v_alignbit_b32 v237, v237, v237, 16
	v_alignbit_b32 v238, v238, v238, 16
	v_xor_b32_e32 v237, s60, v237
	v_xor_b32_e32 v238, s60, v238
	s_nop 1
	s_mov_b32 s58, 0x99999999
	s_mov_b32 s59, 0x99999999
	v_min_u32_dpp v202, v237, v237 quad_perm:[1,0,3,2] row_mask:0xf bank_mask:0xf
	v_max_u32_dpp v203, v237, v237 quad_perm:[1,0,3,2] row_mask:0xf bank_mask:0xf
	v_min_u32_dpp v204, v238, v238 quad_perm:[1,0,3,2] row_mask:0xf bank_mask:0xf
	v_max_u32_dpp v205, v238, v238 quad_perm:[1,0,3,2] row_mask:0xf bank_mask:0xf
	v_cndmask_b32_e64 v237, v203, v202, s[58:59]
	v_cndmask_b32_e64 v238, v205, v204, s[58:59]
	s_mov_b32 s58, 0xcc33cc33
	s_mov_b32 s59, 0xcc33cc33
	v_min_u32_dpp v202, v237, v237 quad_perm:[2,3,0,1] row_mask:0xf bank_mask:0xf
	v_max_u32_dpp v203, v237, v237 quad_perm:[2,3,0,1] row_mask:0xf bank_mask:0xf
	v_min_u32_dpp v204, v238, v238 quad_perm:[2,3,0,1] row_mask:0xf bank_mask:0xf
	v_max_u32_dpp v205, v238, v238 quad_perm:[2,3,0,1] row_mask:0xf bank_mask:0xf
	v_cndmask_b32_e64 v237, v203, v202, s[58:59]
	v_cndmask_b32_e64 v238, v205, v204, s[58:59]
	s_mov_b32 s58, 0xaa55aa55
	s_mov_b32 s59, 0xaa55aa55
	v_min_u32_dpp v202, v237, v237 quad_perm:[1,0,3,2] row_mask:0xf bank_mask:0xf
	v_max_u32_dpp v203, v237, v237 quad_perm:[1,0,3,2] row_mask:0xf bank_mask:0xf
	v_min_u32_dpp v204, v238, v238 quad_perm:[1,0,3,2] row_mask:0xf bank_mask:0xf
	v_max_u32_dpp v205, v238, v238 quad_perm:[1,0,3,2] row_mask:0xf bank_mask:0xf
	v_cndmask_b32_e64 v237, v203, v202, s[58:59]
	v_cndmask_b32_e64 v238, v205, v204, s[58:59]
	s_mov_b32 s58, 0xf00ff00f
	s_mov_b32 s59, 0xf00ff00f
	v_min_u32_dpp v202, v237, v237 row_ror:8 row_mask:0xf bank_mask:0xf
	v_max_u32_dpp v203, v237, v237 row_ror:8 row_mask:0xf bank_mask:0xf
	v_min_u32_dpp v204, v238, v238 row_ror:8 row_mask:0xf bank_mask:0xf
	v_max_u32_dpp v205, v238, v238 row_ror:8 row_mask:0xf bank_mask:0xf
	v_cndmask_b32_e64 v237, v203, v202, s[58:59]
	v_cndmask_b32_e64 v238, v205, v204, s[58:59]
	s_mov_b32 s58, 0xc3c3c3c3
	s_mov_b32 s59, 0xc3c3c3c3
	v_min_u32_dpp v202, v237, v237 quad_perm:[2,3,0,1] row_mask:0xf bank_mask:0xf
	v_max_u32_dpp v203, v237, v237 quad_perm:[2,3,0,1] row_mask:0xf bank_mask:0xf
	v_min_u32_dpp v204, v238, v238 quad_perm:[2,3,0,1] row_mask:0xf bank_mask:0xf
	v_max_u32_dpp v205, v238, v238 quad_perm:[2,3,0,1] row_mask:0xf bank_mask:0xf
	v_cndmask_b32_e64 v237, v203, v202, s[58:59]
; __device__ __forceinline__ void expert_tokens(const unsigned char* __restrict__ UV, const float* __restrict__ US, const float* __restrict__ VS, ...
;     ...
;         const unsigned nw0 = (unsigned)IDX[(size_t)tn * 128 + lane], nw1 = (unsigned)IDX[(size_t)tn * 128 + 64 + lane];
;         const int ni0 = (int)nw0 & rmask, ni1 = (int)nw1 & rmask;
	v_cndmask_b32_e64 v238, v205, v204, s[58:59]
	s_mov_b32 s58, 0xa5a5a5a5
	s_mov_b32 s59, 0xa5a5a5a5
	v_min_u32_dpp v202, v237, v237 quad_perm:[1,0,3,2] row_mask:0xf bank_mask:0xf
	v_max_u32_dpp v203, v237, v237 quad_perm:[1,0,3,2] row_mask:0xf bank_mask:0xf
	v_min_u32_dpp v204, v238, v238 quad_perm:[1,0,3,2] row_mask:0xf bank_mask:0xf
	v_max_u32_dpp v205, v238, v238 quad_perm:[1,0,3,2] row_mask:0xf bank_mask:0xf
	v_cndmask_b32_e64 v237, v203, v202, s[58:59]
	v_cndmask_b32_e64 v238, v205, v204, s[58:59]
	s_mov_b32 s58, 0xf0f00f0f
	s_mov_b32 s59, 0xf0f00f0f
	v_mov_b32_dpp v202, v237 row_half_mirror row_mask:0xf bank_mask:0xf
	v_mov_b32_dpp v204, v238 row_half_mirror row_mask:0xf bank_mask:0xf
	s_nop 0
	v_max_u32_dpp v203, v202, v237 quad_perm:[3,2,1,0] row_mask:0xf bank_mask:0xf
	v_max_u32_dpp v205, v204, v238 quad_perm:[3,2,1,0] row_mask:0xf bank_mask:0xf
	v_min_u32_dpp v202, v202, v237 quad_perm:[3,2,1,0] row_mask:0xf bank_mask:0xf
	v_min_u32_dpp v204, v204, v238 quad_perm:[3,2,1,0] row_mask:0xf bank_mask:0xf
	v_cndmask_b32_e64 v237, v203, v202, s[58:59]
	v_cndmask_b32_e64 v238, v205, v204, s[58:59]
	s_mov_b32 s58, 0xff0000ff
	s_mov_b32 s59, 0xff0000ff
	v_min_u32_dpp v202, v237, v237 row_ror:8 row_mask:0xf bank_mask:0xf
	v_max_u32_dpp v203, v237, v237 row_ror:8 row_mask:0xf bank_mask:0xf
	v_min_u32_dpp v204, v238, v238 row_ror:8 row_mask:0xf bank_mask:0xf
	v_max_u32_dpp v205, v238, v238 row_ror:8 row_mask:0xf bank_mask:0xf
	v_cndmask_b32_e64 v237, v203, v202, s[58:59]
	v_cndmask_b32_e64 v238, v205, v204, s[58:59]
	s_mov_b32 s58, 0xcccc3333
	s_mov_b32 s59, 0xcccc3333
	v_min_u32_dpp v202, v237, v237 quad_perm:[2,3,0,1] row_mask:0xf bank_mask:0xf
	v_max_u32_dpp v203, v237, v237 quad_perm:[2,3,0,1] row_mask:0xf bank_mask:0xf
	v_min_u32_dpp v204, v238, v238 quad_perm:[2,3,0,1] row_mask:0xf bank_mask:0xf
	v_max_u32_dpp v205, v238, v238 quad_perm:[2,3,0,1] row_mask:0xf bank_mask:0xf
	v_cndmask_b32_e64 v237, v203, v202, s[58:59]
	v_cndmask_b32_e64 v238, v205, v204, s[58:59]
	s_mov_b32 s58, 0xaaaa5555
	s_mov_b32 s59, 0xaaaa5555
	v_min_u32_dpp v202, v237, v237 quad_perm:[1,0,3,2] row_mask:0xf bank_mask:0xf
	v_max_u32_dpp v203, v237, v237 quad_perm:[1,0,3,2] row_mask:0xf bank_mask:0xf
	v_min_u32_dpp v204, v238, v238 quad_perm:[1,0,3,2] row_mask:0xf bank_mask:0xf
	v_max_u32_dpp v205, v238, v238 quad_perm:[1,0,3,2] row_mask:0xf bank_mask:0xf
	v_cndmask_b32_e64 v237, v203, v202, s[58:59]
	v_cndmask_b32_e64 v238, v205, v204, s[58:59]
	s_nop 1
	v_permlane16_swap_b32_e32 v237, v238
	s_mov_b32 s58, -1
	s_mov_b32 s59, 0
	v_min_u32_e32 v202, v237, v238
	v_max_u32_e32 v203, v237, v238
	v_cndmask_b32_e64 v237, v203, v202, s[58:59]
	v_cndmask_b32_e64 v238, v202, v203, s[58:59]
	s_mov_b32 s58, 0xf0f0f0f
	s_mov_b32 s59, 0xf0f0f0f0
	v_mov_b32_dpp v202, v237 row_half_mirror row_mask:0xf bank_mask:0xf
	v_mov_b32_dpp v204, v238 row_half_mirror row_mask:0xf bank_mask:0xf
	s_nop 0
	v_max_u32_dpp v203, v202, v237 quad_perm:[3,2,1,0] row_mask:0xf bank_mask:0xf
	v_max_u32_dpp v205, v204, v238 quad_perm:[3,2,1,0] row_mask:0xf bank_mask:0xf
	v_min_u32_dpp v202, v202, v237 quad_perm:[3,2,1,0] row_mask:0xf bank_mask:0xf
	v_min_u32_dpp v204, v204, v238 quad_perm:[3,2,1,0] row_mask:0xf bank_mask:0xf
	v_cndmask_b32_e64 v237, v203, v202, s[58:59]
	v_cndmask_b32_e64 v238, v205, v204, s[58:59]
	s_mov_b32 s58, 0xff00ff
	s_mov_b32 s59, 0xff00ff00
	v_min_u32_dpp v202, v237, v237 row_ror:8 row_mask:0xf bank_mask:0xf
	v_max_u32_dpp v203, v237, v237 row_ror:8 row_mask:0xf bank_mask:0xf
	v_min_u32_dpp v204, v238, v238 row_ror:8 row_mask:0xf bank_mask:0xf
	v_max_u32_dpp v205, v238, v238 row_ror:8 row_mask:0xf bank_mask:0xf
	v_cndmask_b32_e64 v237, v203, v202, s[58:59]
	v_cndmask_b32_e64 v238, v205, v204, s[58:59]
	s_mov_b32 s58, 0x33333333
	s_mov_b32 s59, 0xcccccccc
	v_min_u32_dpp v202, v237, v237 quad_perm:[2,3,0,1] row_mask:0xf bank_mask:0xf
	v_max_u32_dpp v203, v237, v237 quad_perm:[2,3,0,1] row_mask:0xf bank_mask:0xf
	v_min_u32_dpp v204, v238, v238 quad_perm:[2,3,0,1] row_mask:0xf bank_mask:0xf
	v_max_u32_dpp v205, v238, v238 quad_perm:[2,3,0,1] row_mask:0xf bank_mask:0xf
	v_cndmask_b32_e64 v237, v203, v202, s[58:59]
	v_cndmask_b32_e64 v238, v205, v204, s[58:59]
	s_mov_b32 s58, 0x55555555
	s_mov_b32 s59, 0xaaaaaaaa
	v_min_u32_dpp v202, v237, v237 quad_perm:[1,0,3,2] row_mask:0xf bank_mask:0xf
	v_max_u32_dpp v203, v237, v237 quad_perm:[1,0,3,2] row_mask:0xf bank_mask:0xf
	v_min_u32_dpp v204, v238, v238 quad_perm:[1,0,3,2] row_mask:0xf bank_mask:0xf
	v_max_u32_dpp v205, v238, v238 quad_perm:[1,0,3,2] row_mask:0xf bank_mask:0xf
	v_cndmask_b32_e64 v237, v203, v202, s[58:59]
	v_cndmask_b32_e64 v238, v205, v204, s[58:59]
	s_nop 1
	v_permlane32_swap_b32_e32 v237, v238
	s_mov_b32 s58, 0xffff
	s_mov_b32 s59, 0xffff
	v_min_u32_e32 v202, v237, v238
	v_max_u32_e32 v203, v237, v238
	v_cndmask_b32_e64 v237, v203, v202, s[58:59]
	v_cndmask_b32_e64 v238, v202, v203, s[58:59]
	s_nop 1
	v_permlane32_swap_b32_e32 v237, v238
	s_mov_b32 s58, 0xffff
; __device__ __forceinline__ void expert_tokens(const unsigned char* __restrict__ UV, const float* __restrict__ US, const float* __restrict__ VS, ...
;     ...
;         const unsigned nw0 = (unsigned)IDX[(size_t)tn * 128 + lane], nw1 = (unsigned)IDX[(size_t)tn * 128 + 64 + lane];
;         const int ni0 = (int)nw0 & rmask, ni1 = (int)nw1 & rmask;
;         const float ng0 = __uint_as_float(nw0 & 0xFFFF0000u), ng1 = __uint_as_float(nw1 & 0xFFFF0000u);
;     ...
;             if (bi == 0) { nsu0 = US[ni0]; nsu1 = US[ni1]; nsv0 = VS[ni0]; nsv1 = VS[ni1]; }
	s_mov_b32 s59, 0xffff
	v_min_u32_e32 v202, v237, v238
	v_max_u32_e32 v203, v237, v238
	v_cndmask_b32_e64 v237, v203, v202, s[58:59]
	v_cndmask_b32_e64 v238, v202, v203, s[58:59]
	s_mov_b32 s58, 0xf0f00f0f
	s_mov_b32 s59, 0xf0f00f0f
	v_mov_b32_dpp v202, v237 row_half_mirror row_mask:0xf bank_mask:0xf
	v_mov_b32_dpp v204, v238 row_half_mirror row_mask:0xf bank_mask:0xf
	s_nop 0
	v_max_u32_dpp v203, v202, v237 quad_perm:[3,2,1,0] row_mask:0xf bank_mask:0xf
	v_max_u32_dpp v205, v204, v238 quad_perm:[3,2,1,0] row_mask:0xf bank_mask:0xf
	v_min_u32_dpp v202, v202, v237 quad_perm:[3,2,1,0] row_mask:0xf bank_mask:0xf
	v_min_u32_dpp v204, v204, v238 quad_perm:[3,2,1,0] row_mask:0xf bank_mask:0xf
	v_cndmask_b32_e64 v237, v203, v202, s[58:59]
	v_cndmask_b32_e64 v238, v205, v204, s[58:59]
	s_mov_b32 s58, 0xff0000ff
	s_mov_b32 s59, 0xff0000ff
	v_min_u32_dpp v202, v237, v237 row_ror:8 row_mask:0xf bank_mask:0xf
	v_max_u32_dpp v203, v237, v237 row_ror:8 row_mask:0xf bank_mask:0xf
	v_min_u32_dpp v204, v238, v238 row_ror:8 row_mask:0xf bank_mask:0xf
	v_max_u32_dpp v205, v238, v238 row_ror:8 row_mask:0xf bank_mask:0xf
	v_cndmask_b32_e64 v237, v203, v202, s[58:59]
	v_cndmask_b32_e64 v238, v205, v204, s[58:59]
	s_mov_b32 s58, 0xcccc3333
	s_mov_b32 s59, 0xcccc3333
	v_min_u32_dpp v202, v237, v237 quad_perm:[2,3,0,1] row_mask:0xf bank_mask:0xf
	v_max_u32_dpp v203, v237, v237 quad_perm:[2,3,0,1] row_mask:0xf bank_mask:0xf
	v_min_u32_dpp v204, v238, v238 quad_perm:[2,3,0,1] row_mask:0xf bank_mask:0xf
	v_max_u32_dpp v205, v238, v238 quad_perm:[2,3,0,1] row_mask:0xf bank_mask:0xf
	v_cndmask_b32_e64 v237, v203, v202, s[58:59]
	v_cndmask_b32_e64 v238, v205, v204, s[58:59]
	s_mov_b32 s58, 0xaaaa5555
	s_mov_b32 s59, 0xaaaa5555
	v_min_u32_dpp v202, v237, v237 quad_perm:[1,0,3,2] row_mask:0xf bank_mask:0xf
	v_max_u32_dpp v203, v237, v237 quad_perm:[1,0,3,2] row_mask:0xf bank_mask:0xf
	v_min_u32_dpp v204, v238, v238 quad_perm:[1,0,3,2] row_mask:0xf bank_mask:0xf
	v_max_u32_dpp v205, v238, v238 quad_perm:[1,0,3,2] row_mask:0xf bank_mask:0xf
	v_cndmask_b32_e64 v237, v203, v202, s[58:59]
	v_cndmask_b32_e64 v238, v205, v204, s[58:59]
	s_nop 1
	v_permlane16_swap_b32_e32 v237, v238
	v_min_u32_e32 v202, v237, v238
	v_max_u32_e32 v238, v237, v238
	v_mov_b32_e32 v237, v202
	s_nop 1
	v_permlane32_swap_b32_e32 v237, v238
	v_min_u32_e32 v202, v237, v238
	v_max_u32_e32 v238, v237, v238
	v_mov_b32_e32 v237, v202
	s_nop 1
	v_permlane16_swap_b32_e32 v237, v238
	v_min_u32_e32 v202, v237, v238
	v_max_u32_e32 v238, v237, v238
	v_mov_b32_e32 v237, v202
	s_mov_b32 s58, 0xf0f0f0f
	s_mov_b32 s59, 0xf0f0f0f
	v_mov_b32_dpp v202, v237 row_half_mirror row_mask:0xf bank_mask:0xf
	v_mov_b32_dpp v204, v238 row_half_mirror row_mask:0xf bank_mask:0xf
	s_nop 0
	v_max_u32_dpp v203, v202, v237 quad_perm:[3,2,1,0] row_mask:0xf bank_mask:0xf
	v_max_u32_dpp v205, v204, v238 quad_perm:[3,2,1,0] row_mask:0xf bank_mask:0xf
	v_min_u32_dpp v202, v202, v237 quad_perm:[3,2,1,0] row_mask:0xf bank_mask:0xf
	v_min_u32_dpp v204, v204, v238 quad_perm:[3,2,1,0] row_mask:0xf bank_mask:0xf
	v_cndmask_b32_e64 v237, v203, v202, s[58:59]
	v_cndmask_b32_e64 v238, v205, v204, s[58:59]
	s_mov_b32 s58, 0xff00ff
	s_mov_b32 s59, 0xff00ff
	v_min_u32_dpp v202, v237, v237 row_ror:8 row_mask:0xf bank_mask:0xf
	v_max_u32_dpp v203, v237, v237 row_ror:8 row_mask:0xf bank_mask:0xf
	v_min_u32_dpp v204, v238, v238 row_ror:8 row_mask:0xf bank_mask:0xf
	v_max_u32_dpp v205, v238, v238 row_ror:8 row_mask:0xf bank_mask:0xf
	v_cndmask_b32_e64 v237, v203, v202, s[58:59]
	v_cndmask_b32_e64 v238, v205, v204, s[58:59]
	s_mov_b32 s58, 0x33333333
	s_mov_b32 s59, 0x33333333
	v_min_u32_dpp v202, v237, v237 quad_perm:[2,3,0,1] row_mask:0xf bank_mask:0xf
	v_max_u32_dpp v203, v237, v237 quad_perm:[2,3,0,1] row_mask:0xf bank_mask:0xf
	v_min_u32_dpp v204, v238, v238 quad_perm:[2,3,0,1] row_mask:0xf bank_mask:0xf
	v_max_u32_dpp v205, v238, v238 quad_perm:[2,3,0,1] row_mask:0xf bank_mask:0xf
	v_cndmask_b32_e64 v237, v203, v202, s[58:59]
	v_cndmask_b32_e64 v238, v205, v204, s[58:59]
	s_mov_b32 s58, 0x55555555
	s_mov_b32 s59, 0x55555555
	v_min_u32_dpp v202, v237, v237 quad_perm:[1,0,3,2] row_mask:0xf bank_mask:0xf
	v_max_u32_dpp v203, v237, v237 quad_perm:[1,0,3,2] row_mask:0xf bank_mask:0xf
	v_min_u32_dpp v204, v238, v238 quad_perm:[1,0,3,2] row_mask:0xf bank_mask:0xf
	v_max_u32_dpp v205, v238, v238 quad_perm:[1,0,3,2] row_mask:0xf bank_mask:0xf
	v_cndmask_b32_e64 v237, v203, v202, s[58:59]
	v_cndmask_b32_e64 v238, v205, v204, s[58:59]
	s_nop 1
	v_permlane16_swap_b32_e32 v237, v238
	s_nop 1
	v_permlane32_swap_b32_e32 v237, v238
	v_xor_b32_e32 v237, s60, v237
	v_xor_b32_e32 v238, s60, v238
	v_alignbit_b32 v237, v237, v237, 16
	v_alignbit_b32 v238, v238, v238, 16
	v_and_b32_e32 v242, 0x3fff, v237
	v_and_b32_e32 v243, 0x3fff, v238
	v_lshlrev_b32_e32 v208, 3, v242
	v_lshlrev_b32_e32 v206, 3, v243
	global_load_dwordx2 v[202:203], v208, s[12:13]
	global_load_dwordx2 v[204:205], v206, s[12:13]
